# sc1 epilogue stores, P2 deferred row/col-sum loads issued in prologue, redundant lgkmcnt waits removed, loop bookkeeping moved into MFMA shadow
# speedup vs baseline: 1.0253x; 1.0253x over previous
.LBB2_33:
	s_waitcnt vmcnt(6)
	s_barrier
	s_setprio 1
	v_mfma_i32_16x16x64_i8 v[48:51], v[144:147], v[184:187], v[48:51]
	s_add_i32 s74, s74, 2
	s_add_u32 s70, s70, 0x100
	s_addc_u32 s71, s71, 0
	s_add_u32 s72, s72, 0x100
	s_addc_u32 s73, s73, 0
	s_cmp_gt_u32 s74, 13
	v_mfma_i32_16x16x64_i8 v[40:43], v[148:151], v[184:187], v[40:43]
	v_mfma_i32_16x16x64_i8 v[32:35], v[144:147], v[172:175], v[32:35]
	v_mfma_i32_16x16x64_i8 v[24:27], v[148:151], v[172:175], v[24:27]
	v_mfma_i32_16x16x64_i8 v[16:19], v[144:147], v[168:171], v[16:19]
	v_mfma_i32_16x16x64_i8 v[8:11], v[148:151], v[168:171], v[8:11]
	v_mfma_i32_16x16x64_i8 v[4:7], v[144:147], v[160:163], v[4:7]
	v_mfma_i32_16x16x64_i8 v[0:3], v[148:151], v[160:163], v[0:3]
	v_mfma_i32_16x16x64_i8 v[48:51], v[156:159], v[188:191], v[48:51]
	v_mfma_i32_16x16x64_i8 v[40:43], v[152:155], v[188:191], v[40:43]
	v_mfma_i32_16x16x64_i8 v[32:35], v[156:159], v[176:179], v[32:35]
	v_mfma_i32_16x16x64_i8 v[24:27], v[152:155], v[176:179], v[24:27]
	v_mfma_i32_16x16x64_i8 v[16:19], v[156:159], v[180:183], v[16:19]
	v_mfma_i32_16x16x64_i8 v[8:11], v[152:155], v[180:183], v[8:11]
	v_mfma_i32_16x16x64_i8 v[4:7], v[156:159], v[164:167], v[4:7]
	v_mfma_i32_16x16x64_i8 v[0:3], v[152:155], v[164:167], v[0:3]
	s_setprio 0
	s_barrier
	s_cbranch_scc1 .LBB2_50
.LBB2_34:
	ds_read_b128 v[144:147], v203
	ds_read_b128 v[148:151], v203 offset:2048
	ds_read_b128 v[156:159], v204
	ds_read_b128 v[152:155], v204 offset:2048
	s_cmp_lg_u32 s74, 12
	s_cselect_b64 s[0:1], -1, 0
	s_and_b64 s[4:5], s[0:1], exec
	s_cselect_b32 s75, s73, s68
	s_cselect_b32 s16, s72, s69
	s_mov_b32 m0, s53
	s_and_b32 s5, s71, 0xffff
	s_mov_b32 s4, s70
	ds_read_b128 v[184:187], v205
	ds_read_b128 v[172:175], v205 offset:2048
	ds_read_b128 v[188:191], v206
	ds_read_b128 v[176:179], v206 offset:2048
	ds_read_b128 v[168:171], v205 offset:4096
	ds_read_b128 v[160:163], v205 offset:6144
	ds_read_b128 v[180:183], v206 offset:4096
	ds_read_b128 v[164:167], v206 offset:6144
	buffer_load_dwordx4 v193, s[4:7], 0 offen lds
	s_mov_b32 m0, s54
	s_or_b64 s[36:37], s[28:29], s[0:1]
	buffer_load_dwordx4 v197, s[4:7], 0 offen lds
	s_waitcnt lgkmcnt(8)
	s_barrier
	s_waitcnt lgkmcnt(0)
	s_setprio 1
	v_mfma_i32_16x16x64_i8 v[124:127], v[144:147], v[184:187], v[124:127]
	s_xor_b64 s[34:35], s[36:37], -1
	v_mfma_i32_16x16x64_i8 v[120:123], v[148:151], v[184:187], v[120:123]
	v_mfma_i32_16x16x64_i8 v[108:111], v[144:147], v[172:175], v[108:111]
	v_mfma_i32_16x16x64_i8 v[104:107], v[148:151], v[172:175], v[104:107]
	v_mfma_i32_16x16x64_i8 v[96:99], v[144:147], v[168:171], v[96:99]
	v_mfma_i32_16x16x64_i8 v[88:91], v[148:151], v[168:171], v[88:91]
	v_mfma_i32_16x16x64_i8 v[80:83], v[144:147], v[160:163], v[80:83]
	v_mfma_i32_16x16x64_i8 v[72:75], v[148:151], v[160:163], v[72:75]
	v_mfma_i32_16x16x64_i8 v[124:127], v[156:159], v[188:191], v[124:127]
	v_mfma_i32_16x16x64_i8 v[120:123], v[152:155], v[188:191], v[120:123]
	v_mfma_i32_16x16x64_i8 v[108:111], v[156:159], v[176:179], v[108:111]
	v_mfma_i32_16x16x64_i8 v[104:107], v[152:155], v[176:179], v[104:107]
	v_mfma_i32_16x16x64_i8 v[96:99], v[156:159], v[180:183], v[96:99]
	v_mfma_i32_16x16x64_i8 v[88:91], v[152:155], v[180:183], v[88:91]
	v_mfma_i32_16x16x64_i8 v[80:83], v[156:159], v[164:167], v[80:83]
	v_mfma_i32_16x16x64_i8 v[72:75], v[152:155], v[164:167], v[72:75]
	s_setprio 0
	s_barrier
	ds_read_b128 v[128:131], v207
	ds_read_b128 v[132:135], v207 offset:2048
	ds_read_b128 v[140:143], v208
	ds_read_b128 v[136:139], v208 offset:2048
	s_and_b64 vcc, exec, s[34:35]
	s_cbranch_vccnz .LBB2_36
	s_and_b32 s17, s75, 0xffff
	s_mov_b32 s18, s6
	s_mov_b32 s19, s7
	s_mov_b32 m0, s39
	s_nop 0
	buffer_load_dwordx4 v196, s[16:19], 0 offen lds
	s_mov_b32 m0, s40
	s_nop 0
	buffer_load_dwordx4 v198, s[16:19], 0 offen lds
.LBB2_36:
	s_add_u32 s4, s70, 0xfffc0080
	s_addc_u32 s5, s71, -1
	s_barrier
	s_waitcnt lgkmcnt(0)
	s_setprio 1
	v_mfma_i32_16x16x64_i8 v[116:119], v[128:131], v[184:187], v[116:119]
	s_and_b64 s[0:1], s[0:1], exec
	s_cselect_b32 s17, s5, s66
	s_cselect_b32 s4, s4, s67
	v_mfma_i32_16x16x64_i8 v[112:115], v[132:135], v[184:187], v[112:115]
	v_mfma_i32_16x16x64_i8 v[100:103], v[128:131], v[172:175], v[100:103]
	v_mfma_i32_16x16x64_i8 v[92:95], v[132:135], v[172:175], v[92:95]
	v_mfma_i32_16x16x64_i8 v[84:87], v[128:131], v[168:171], v[84:87]
	v_mfma_i32_16x16x64_i8 v[76:79], v[132:135], v[168:171], v[76:79]
	v_mfma_i32_16x16x64_i8 v[68:71], v[128:131], v[160:163], v[68:71]
	v_mfma_i32_16x16x64_i8 v[64:67], v[132:135], v[160:163], v[64:67]
	v_mfma_i32_16x16x64_i8 v[116:119], v[140:143], v[188:191], v[116:119]
	v_mfma_i32_16x16x64_i8 v[112:115], v[136:139], v[188:191], v[112:115]
	v_mfma_i32_16x16x64_i8 v[100:103], v[140:143], v[176:179], v[100:103]
	v_mfma_i32_16x16x64_i8 v[92:95], v[136:139], v[176:179], v[92:95]
	v_mfma_i32_16x16x64_i8 v[84:87], v[140:143], v[180:183], v[84:87]
	v_mfma_i32_16x16x64_i8 v[76:79], v[136:139], v[180:183], v[76:79]
	v_mfma_i32_16x16x64_i8 v[68:71], v[140:143], v[164:167], v[68:71]
	v_mfma_i32_16x16x64_i8 v[64:67], v[136:139], v[164:167], v[64:67]
	s_setprio 0
	s_barrier
	ds_read_b128 v[184:187], v205 offset:16384
	ds_read_b128 v[172:175], v205 offset:18432
	ds_read_b128 v[188:191], v206 offset:16384
	ds_read_b128 v[176:179], v206 offset:18432
	ds_read_b128 v[168:171], v205 offset:20480
	ds_read_b128 v[160:163], v205 offset:22528
	ds_read_b128 v[180:183], v206 offset:20480
	ds_read_b128 v[164:167], v206 offset:22528
	v_cndmask_b32_e64 v194, 0, 1, s[36:37]
	v_cmp_ne_u32_e64 s[0:1], 1, v194
	s_andn2_b64 vcc, exec, s[36:37]
	s_cbranch_vccnz .LBB2_38
	s_and_b32 s5, s17, 0xffff
	s_mov_b32 m0, s38
	s_nop 0
	buffer_load_dwordx4 v193, s[4:7], 0 offen lds
	s_mov_b32 m0, s41
	s_nop 0
	buffer_load_dwordx4 v197, s[4:7], 0 offen lds
.LBB2_38:
	s_barrier
	s_waitcnt lgkmcnt(0)
	s_setprio 1
	v_mfma_i32_16x16x64_i8 v[60:63], v[144:147], v[184:187], v[60:63]
	v_mfma_i32_16x16x64_i8 v[56:59], v[148:151], v[184:187], v[56:59]
	v_mfma_i32_16x16x64_i8 v[52:55], v[144:147], v[172:175], v[52:55]
	v_mfma_i32_16x16x64_i8 v[44:47], v[148:151], v[172:175], v[44:47]
	v_mfma_i32_16x16x64_i8 v[36:39], v[144:147], v[168:171], v[36:39]
	v_mfma_i32_16x16x64_i8 v[28:31], v[148:151], v[168:171], v[28:31]
	v_mfma_i32_16x16x64_i8 v[20:23], v[144:147], v[160:163], v[20:23]
	v_mfma_i32_16x16x64_i8 v[12:15], v[148:151], v[160:163], v[12:15]
	v_mfma_i32_16x16x64_i8 v[60:63], v[156:159], v[188:191], v[60:63]
	v_mfma_i32_16x16x64_i8 v[56:59], v[152:155], v[188:191], v[56:59]
	v_mfma_i32_16x16x64_i8 v[52:55], v[156:159], v[176:179], v[52:55]
	v_mfma_i32_16x16x64_i8 v[44:47], v[152:155], v[176:179], v[44:47]
	v_mfma_i32_16x16x64_i8 v[36:39], v[156:159], v[180:183], v[36:39]
	v_mfma_i32_16x16x64_i8 v[28:31], v[152:155], v[180:183], v[28:31]
	v_mfma_i32_16x16x64_i8 v[20:23], v[156:159], v[164:167], v[20:23]
	v_mfma_i32_16x16x64_i8 v[12:15], v[152:155], v[164:167], v[12:15]
	s_setprio 0
	s_barrier
	s_mov_b64 s[18:19], -1
	s_and_b64 vcc, exec, s[34:35]
	s_cbranch_vccz .LBB2_40
	s_waitcnt vmcnt(0)
	s_mov_b64 s[18:19], 0

.LBB2_42:
	s_barrier
	s_setprio 1
	v_mfma_i32_16x16x64_i8 v[48:51], v[128:131], v[184:187], v[48:51]
	s_add_i32 s5, 0, 0x18000
	v_add_u32_e32 v210, s5, v199
	v_add_u32_e32 v211, s5, v200
	v_mfma_i32_16x16x64_i8 v[40:43], v[132:135], v[184:187], v[40:43]
	v_mfma_i32_16x16x64_i8 v[32:35], v[128:131], v[172:175], v[32:35]
	v_mfma_i32_16x16x64_i8 v[24:27], v[132:135], v[172:175], v[24:27]
	v_mfma_i32_16x16x64_i8 v[16:19], v[128:131], v[168:171], v[16:19]
	v_mfma_i32_16x16x64_i8 v[8:11], v[132:135], v[168:171], v[8:11]
	v_mfma_i32_16x16x64_i8 v[4:7], v[128:131], v[160:163], v[4:7]
	v_mfma_i32_16x16x64_i8 v[0:3], v[132:135], v[160:163], v[0:3]
	v_mfma_i32_16x16x64_i8 v[48:51], v[140:143], v[188:191], v[48:51]
	v_mfma_i32_16x16x64_i8 v[40:43], v[136:139], v[188:191], v[40:43]
	v_mfma_i32_16x16x64_i8 v[32:35], v[140:143], v[176:179], v[32:35]
	v_mfma_i32_16x16x64_i8 v[24:27], v[136:139], v[176:179], v[24:27]
	v_mfma_i32_16x16x64_i8 v[16:19], v[140:143], v[180:183], v[16:19]
	v_mfma_i32_16x16x64_i8 v[8:11], v[136:139], v[180:183], v[8:11]
	v_mfma_i32_16x16x64_i8 v[4:7], v[140:143], v[164:167], v[4:7]
	v_mfma_i32_16x16x64_i8 v[0:3], v[136:139], v[164:167], v[0:3]
	s_setprio 0
	s_barrier
	ds_read_b128 v[128:131], v210
	ds_read_b128 v[132:135], v210 offset:2048
	ds_read_b128 v[140:143], v211
	ds_read_b128 v[136:139], v211 offset:2048
	ds_read_b128 v[184:187], v205 offset:32768
	ds_read_b128 v[172:175], v205 offset:34816
	ds_read_b128 v[188:191], v206 offset:32768
	ds_read_b128 v[176:179], v206 offset:34816
	ds_read_b128 v[168:171], v205 offset:36864
	ds_read_b128 v[160:163], v205 offset:38912
	ds_read_b128 v[180:183], v206 offset:36864
	ds_read_b128 v[164:167], v206 offset:38912
	s_and_b64 vcc, exec, s[0:1]
	s_cbranch_vccnz .LBB2_44
	s_add_u32 s76, s4, 0x40000
	s_addc_u32 s5, s17, 0
	s_and_b32 s77, s5, 0xffff
	s_mov_b32 s78, s6
	s_mov_b32 s79, s7
	s_mov_b32 m0, s44
	s_nop 0
	buffer_load_dwordx4 v193, s[76:79], 0 offen lds
	s_mov_b32 m0, s45
	s_nop 0
	buffer_load_dwordx4 v197, s[76:79], 0 offen lds
.LBB2_44:
	s_waitcnt lgkmcnt(8)
	s_barrier
	s_waitcnt lgkmcnt(0)
	s_setprio 1
	v_mfma_i32_16x16x64_i8 v[124:127], v[128:131], v[184:187], v[124:127]
	v_mfma_i32_16x16x64_i8 v[120:123], v[132:135], v[184:187], v[120:123]
	v_mfma_i32_16x16x64_i8 v[108:111], v[128:131], v[172:175], v[108:111]
	v_mfma_i32_16x16x64_i8 v[104:107], v[132:135], v[172:175], v[104:107]
	v_mfma_i32_16x16x64_i8 v[96:99], v[128:131], v[168:171], v[96:99]
	v_mfma_i32_16x16x64_i8 v[88:91], v[132:135], v[168:171], v[88:91]
	v_mfma_i32_16x16x64_i8 v[80:83], v[128:131], v[160:163], v[80:83]
	v_mfma_i32_16x16x64_i8 v[72:75], v[132:135], v[160:163], v[72:75]
	v_mfma_i32_16x16x64_i8 v[124:127], v[140:143], v[188:191], v[124:127]
	v_mfma_i32_16x16x64_i8 v[120:123], v[136:139], v[188:191], v[120:123]
	v_mfma_i32_16x16x64_i8 v[108:111], v[140:143], v[176:179], v[108:111]
	v_mfma_i32_16x16x64_i8 v[104:107], v[136:139], v[176:179], v[104:107]
	v_mfma_i32_16x16x64_i8 v[96:99], v[140:143], v[180:183], v[96:99]
	v_mfma_i32_16x16x64_i8 v[88:91], v[136:139], v[180:183], v[88:91]
	v_mfma_i32_16x16x64_i8 v[80:83], v[140:143], v[164:167], v[80:83]
	v_mfma_i32_16x16x64_i8 v[72:75], v[136:139], v[164:167], v[72:75]
	s_setprio 0
	s_barrier
	s_add_i32 s5, 0, 0x1c000
	v_add_u32_e32 v148, s5, v199
	v_add_u32_e32 v152, s5, v200
	ds_read_b128 v[144:147], v148
	ds_read_b128 v[148:151], v148 offset:2048
	ds_read_b128 v[156:159], v152
	ds_read_b128 v[152:155], v152 offset:2048
	s_and_b64 vcc, exec, s[0:1]
	s_cbranch_vccnz .LBB2_46
	s_add_u32 s76, s16, 0x80
	s_addc_u32 s5, s75, 0
	s_and_b32 s77, s5, 0xffff
	s_mov_b32 s78, s6
	s_mov_b32 s79, s7
	s_mov_b32 m0, s47
	s_nop 0
	buffer_load_dwordx4 v196, s[76:79], 0 offen lds
	s_mov_b32 m0, s48
	s_nop 0
	buffer_load_dwordx4 v198, s[76:79], 0 offen lds
.LBB2_46:
	s_barrier
	s_waitcnt lgkmcnt(0)
	s_setprio 1
	v_mfma_i32_16x16x64_i8 v[116:119], v[144:147], v[184:187], v[116:119]
	v_mfma_i32_16x16x64_i8 v[112:115], v[148:151], v[184:187], v[112:115]
	v_mfma_i32_16x16x64_i8 v[100:103], v[144:147], v[172:175], v[100:103]
	v_mfma_i32_16x16x64_i8 v[92:95], v[148:151], v[172:175], v[92:95]
	v_mfma_i32_16x16x64_i8 v[84:87], v[144:147], v[168:171], v[84:87]
	v_mfma_i32_16x16x64_i8 v[76:79], v[148:151], v[168:171], v[76:79]
	v_mfma_i32_16x16x64_i8 v[68:71], v[144:147], v[160:163], v[68:71]
	v_mfma_i32_16x16x64_i8 v[64:67], v[148:151], v[160:163], v[64:67]
	v_mfma_i32_16x16x64_i8 v[116:119], v[156:159], v[188:191], v[116:119]
	v_mfma_i32_16x16x64_i8 v[112:115], v[152:155], v[188:191], v[112:115]
	v_mfma_i32_16x16x64_i8 v[100:103], v[156:159], v[176:179], v[100:103]
	v_mfma_i32_16x16x64_i8 v[92:95], v[152:155], v[176:179], v[92:95]
	v_mfma_i32_16x16x64_i8 v[84:87], v[156:159], v[180:183], v[84:87]
	v_mfma_i32_16x16x64_i8 v[76:79], v[152:155], v[180:183], v[76:79]
	v_mfma_i32_16x16x64_i8 v[68:71], v[156:159], v[164:167], v[68:71]
	v_mfma_i32_16x16x64_i8 v[64:67], v[152:155], v[164:167], v[64:67]
	s_setprio 0
	s_barrier
	ds_read_b128 v[184:187], v205 offset:49152
	ds_read_b128 v[172:175], v205 offset:51200
	ds_read_b128 v[188:191], v206 offset:49152
	ds_read_b128 v[176:179], v206 offset:51200
	ds_read_b128 v[168:171], v205 offset:53248
	ds_read_b128 v[160:163], v205 offset:55296
	ds_read_b128 v[180:183], v206 offset:53248
	ds_read_b128 v[164:167], v206 offset:55296
	s_and_b64 vcc, exec, s[0:1]
	s_cbranch_vccnz .LBB2_48
	s_add_u32 s4, s4, 0x80
	s_addc_u32 s5, s17, 0
	s_and_b32 s5, s5, 0xffff
	s_mov_b32 m0, s49
	s_nop 0
	buffer_load_dwordx4 v193, s[4:7], 0 offen lds
	s_mov_b32 m0, s50
	s_nop 0
	buffer_load_dwordx4 v197, s[4:7], 0 offen lds
.LBB2_48:
	s_barrier
	s_waitcnt lgkmcnt(0)
	s_setprio 1
	v_mfma_i32_16x16x64_i8 v[60:63], v[128:131], v[184:187], v[60:63]
	v_mfma_i32_16x16x64_i8 v[56:59], v[132:135], v[184:187], v[56:59]
	v_mfma_i32_16x16x64_i8 v[52:55], v[128:131], v[172:175], v[52:55]
	v_mfma_i32_16x16x64_i8 v[44:47], v[132:135], v[172:175], v[44:47]
	v_mfma_i32_16x16x64_i8 v[36:39], v[128:131], v[168:171], v[36:39]
	v_mfma_i32_16x16x64_i8 v[28:31], v[132:135], v[168:171], v[28:31]
	v_mfma_i32_16x16x64_i8 v[20:23], v[128:131], v[160:163], v[20:23]
	v_mfma_i32_16x16x64_i8 v[12:15], v[132:135], v[160:163], v[12:15]
	v_mfma_i32_16x16x64_i8 v[60:63], v[140:143], v[188:191], v[60:63]
	v_mfma_i32_16x16x64_i8 v[56:59], v[136:139], v[188:191], v[56:59]
	v_mfma_i32_16x16x64_i8 v[52:55], v[140:143], v[176:179], v[52:55]
	v_mfma_i32_16x16x64_i8 v[44:47], v[136:139], v[176:179], v[44:47]
	v_mfma_i32_16x16x64_i8 v[36:39], v[140:143], v[180:183], v[36:39]
	v_mfma_i32_16x16x64_i8 v[28:31], v[136:139], v[180:183], v[28:31]
	v_mfma_i32_16x16x64_i8 v[20:23], v[140:143], v[164:167], v[20:23]
	v_mfma_i32_16x16x64_i8 v[12:15], v[136:139], v[164:167], v[12:15]
	s_setprio 0
	s_barrier
	s_and_b64 vcc, exec, s[0:1]
	s_cbranch_vccnz .LBB2_33
	s_add_u32 s4, s16, 0x4080
	s_addc_u32 s0, s75, 0
	s_and_b32 s5, s0, 0xffff
	s_mov_b32 m0, s51
	s_nop 0
	buffer_load_dwordx4 v196, s[4:7], 0 offen lds
	s_mov_b32 m0, s52
	s_nop 0
	buffer_load_dwordx4 v198, s[4:7], 0 offen lds
	s_branch .LBB2_33
.LBB2_50:
	s_mul_i32 s0, s65, 0xc00
	v_cvt_f32_i32_e32 v149, v125
	v_cvt_f32_i32_e32 v148, v124
	v_cvt_f32_i32_e32 v151, v127
	v_cvt_f32_i32_e32 v150, v126
	s_add_i32 s0, s0, 0
	s_add_i32 s4, s0, 0x20000
	v_lshl_or_b32 v144, s64, 8, v202
	v_lshl_add_u32 v146, s23, 8, v201
	s_mov_b64 s[0:1], -1
	s_and_b64 vcc, exec, s[30:31]
	v_ashrrev_i32_e32 v145, 31, v144
	v_lshl_add_u32 v163, v202, 2, s4
	v_lshl_add_u32 v162, v201, 2, s4
	s_cbranch_vccz .LBB2_86
	ds_read2st64_b32 v[152:153], v162 offset1:4
	ds_read_b128 v[136:139], v163 offset:2048
	ds_read_b128 v[132:135], v163 offset:2064
	ds_read_b128 v[128:131], v163 offset:2080
	ds_read_b128 v[124:127], v163 offset:2096
	s_waitcnt lgkmcnt(4)
	v_mov_b32_e32 v154, v153
	v_mov_b32_e32 v153, v152
	v_mov_b32_e32 v155, v154
	s_waitcnt lgkmcnt(3)
	v_pk_mul_f32 v[140:141], v[138:139], v[150:151]
	v_pk_mul_f32 v[142:143], v[136:137], v[148:149]
	s_cmp_gt_i32 s23, 7
	v_pk_fma_f32 v[156:157], v[142:143], v[152:153], v[154:155] op_sel_hi:[1,0,0]
	v_pk_fma_f32 v[158:159], v[140:141], v[152:153], v[154:155] op_sel_hi:[1,0,0]
	s_cbranch_scc0 .LBB2_67
	v_cvt_f32_i32_e32 v141, v121
	v_cvt_f32_i32_e32 v143, v123
	v_cvt_f32_i32_e32 v142, v122
	v_cvt_f32_i32_e32 v140, v120
	v_cvt_f32_i32_e32 v169, v119
	v_cvt_f32_i32_e32 v168, v118
	s_waitcnt lgkmcnt(2)
	v_pk_mul_f32 v[142:143], v[134:135], v[142:143]
	v_pk_mul_f32 v[140:141], v[132:133], v[140:141]
	v_mov_b32_e32 v160, v154
	v_mov_b32_e32 v161, v154
	v_mov_b32_e32 v164, v152
	v_mov_b32_e32 v165, v152
	v_cvt_f32_i32_e32 v167, v117
	v_cvt_f32_i32_e32 v166, v116
	v_pk_fma_f32 v[170:171], v[142:143], v[164:165], v[160:161]
	v_pk_fma_f32 v[142:143], v[140:141], v[152:153], v[154:155]
	s_waitcnt lgkmcnt(1)
	v_pk_mul_f32 v[140:141], v[130:131], v[168:169]
	v_cvt_f32_i32_e32 v173, v113
	v_cvt_f32_i32_e32 v172, v112
	v_pk_fma_f32 v[168:169], v[140:141], v[164:165], v[160:161]
	v_pk_mul_f32 v[166:167], v[128:129], v[166:167]
	v_cvt_pk_fp8_f32 v140, v156, v157
	v_cvt_pk_fp8_f32 v141, v142, v143
	v_cvt_f32_i32_e32 v175, v115
	v_cvt_f32_i32_e32 v174, v114
	s_waitcnt lgkmcnt(0)
	v_pk_mul_f32 v[172:173], v[124:125], v[172:173]
	v_pk_fma_f32 v[166:167], v[166:167], v[152:153], v[154:155]
	v_pk_fma_f32 v[172:173], v[172:173], v[152:153], v[154:155]
	v_cvt_pk_fp8_f32 v140, v158, v159 op_sel:[0,0,1]
	v_cvt_pk_fp8_f32 v142, v166, v167
	v_cvt_pk_fp8_f32 v143, v172, v173
	v_cvt_pk_fp8_f32 v141, v170, v171 op_sel:[0,0,1]
	v_pk_mul_f32 v[174:175], v[126:127], v[174:175]
	v_cvt_pk_fp8_f32 v142, v168, v169 op_sel:[0,0,1]
	v_pk_fma_f32 v[160:161], v[174:175], v[164:165], v[160:161]
	s_mov_b32 s23, s22
	v_cvt_pk_fp8_f32 v143, v160, v161 op_sel:[0,0,1]
	v_mov_b64_e32 v[168:169], s[22:23]
	v_mov_b32_e32 v147, v195
	v_lshlrev_b64 v[160:161], 13, v[146:147]
	v_mfma_f32_16x16x32_fp8_fp8 v[164:167], v[140:141], v[168:169], 0
	v_lshl_add_u64 v[160:161], s[10:11], 0, v[160:161]
	v_lshl_add_u64 v[160:161], v[160:161], 0, v[144:145]
	global_store_dwordx4 v[160:161], v[140:143], off sc1
	s_nop 1
	v_mfma_f32_16x16x32_fp8_fp8 v[140:143], v[142:143], v[168:169], v[164:167]
	s_and_saveexec_b64 s[0:1], s[20:21]
	s_cbranch_execz .LBB2_54
	s_lshl_b32 s4, s64, 2
	s_or_b32 s4, s4, s46
	s_ashr_i32 s5, s4, 31
	s_lshl_b64 s[4:5], s[4:5], 14
	s_add_u32 s4, s2, s4
	s_addc_u32 s5, s3, s5
	v_lshl_add_u64 v[160:161], v[146:147], 2, s[4:5]
	v_lshlrev_b32_e32 v194, 2, v192
	v_lshl_add_u64 v[160:161], v[160:161], 0, v[194:195]
	global_store_dwordx4 v[160:161], v[140:143], off sc1
.LBB2_54:
	s_or_b64 exec, exec, s[0:1]
	v_add_u32_e32 v160, 64, v162
	ds_read2st64_b32 v[164:165], v160 offset1:4
	s_nop 2
	v_cvt_f32_i32_e32 v141, v109
	v_cvt_f32_i32_e32 v140, v108
	v_cvt_f32_i32_e32 v171, v107
	v_cvt_f32_i32_e32 v170, v106
	v_cvt_f32_i32_e32 v175, v103
	v_cvt_f32_i32_e32 v174, v102
	v_cvt_f32_i32_e32 v169, v105
	v_cvt_f32_i32_e32 v168, v104
	v_pk_mul_f32 v[140:141], v[136:137], v[140:141]
	s_waitcnt lgkmcnt(0)
	v_mov_b32_e32 v166, v165
	v_pk_fma_f32 v[172:173], v[140:141], v[164:165], v[166:167] op_sel_hi:[1,0,0]
	v_pk_mul_f32 v[140:141], v[134:135], v[170:171]
	v_cvt_f32_i32_e32 v143, v111
	v_cvt_f32_i32_e32 v142, v110
	v_pk_fma_f32 v[176:177], v[140:141], v[164:165], v[166:167] op_sel_hi:[1,0,0]
	v_pk_mul_f32 v[140:141], v[130:131], v[174:175]
	v_pk_mul_f32 v[168:169], v[132:133], v[168:169]
	v_cvt_f32_i32_e32 v171, v101
	v_cvt_f32_i32_e32 v170, v100
	v_pk_fma_f32 v[174:175], v[140:141], v[164:165], v[166:167] op_sel_hi:[1,0,0]
	v_cvt_f32_i32_e32 v179, v93
	v_cvt_f32_i32_e32 v178, v92
	v_pk_fma_f32 v[168:169], v[168:169], v[164:165], v[166:167] op_sel_hi:[1,0,0]
	v_cvt_pk_fp8_f32 v140, v172, v173
	v_pk_mul_f32 v[142:143], v[138:139], v[142:143]
	v_cvt_pk_fp8_f32 v141, v168, v169
	v_pk_fma_f32 v[142:143], v[142:143], v[164:165], v[166:167] op_sel_hi:[1,0,0]
	v_pk_mul_f32 v[170:171], v[128:129], v[170:171]
	v_cvt_f32_i32_e32 v181, v95
	v_cvt_f32_i32_e32 v180, v94
	v_pk_mul_f32 v[168:169], v[124:125], v[178:179]
	v_pk_fma_f32 v[170:171], v[170:171], v[164:165], v[166:167] op_sel_hi:[1,0,0]
	v_pk_fma_f32 v[168:169], v[168:169], v[164:165], v[166:167] op_sel_hi:[1,0,0]
	v_cvt_pk_fp8_f32 v140, v142, v143 op_sel:[0,0,1]
	v_cvt_pk_fp8_f32 v141, v176, v177 op_sel:[0,0,1]
	v_cvt_pk_fp8_f32 v142, v170, v171
	v_cvt_pk_fp8_f32 v143, v168, v169
	v_pk_mul_f32 v[168:169], v[126:127], v[180:181]
	v_mov_b64_e32 v[170:171], s[22:23]
	v_pk_fma_f32 v[164:165], v[168:169], v[164:165], v[166:167] op_sel_hi:[1,0,0]
	v_cvt_pk_fp8_f32 v142, v174, v175 op_sel:[0,0,1]
	v_cvt_pk_fp8_f32 v143, v164, v165 op_sel:[0,0,1]
	v_or_b32_e32 v194, 16, v146
	v_mfma_f32_16x16x32_fp8_fp8 v[164:167], v[140:141], v[170:171], 0
	v_lshlrev_b64 v[168:169], 13, v[194:195]
	v_lshl_add_u64 v[168:169], s[10:11], 0, v[168:169]
	v_lshl_add_u64 v[168:169], v[168:169], 0, v[144:145]
	global_store_dwordx4 v[168:169], v[140:143], off sc1
	s_nop 1
	v_mfma_f32_16x16x32_fp8_fp8 v[140:143], v[142:143], v[170:171], v[164:167]
	s_and_saveexec_b64 s[0:1], s[20:21]
	s_cbranch_execz .LBB2_56
	s_lshl_b32 s4, s64, 2
	s_or_b32 s4, s4, s46
	s_ashr_i32 s5, s4, 31
	s_lshl_b64 s[4:5], s[4:5], 14
	s_add_u32 s4, s2, s4
	s_addc_u32 s5, s3, s5
	v_lshl_add_u64 v[164:165], v[146:147], 2, s[4:5]
	v_lshlrev_b32_e32 v194, 2, v192
	v_lshl_add_u64 v[164:165], v[164:165], 0, v[194:195]
	global_store_dwordx4 v[164:165], v[140:143], off offset:64 sc1
.LBB2_56:
	s_or_b64 exec, exec, s[0:1]
	v_add_u32_e32 v161, 0x80, v162
	ds_read2st64_b32 v[164:165], v161 offset1:4
	s_nop 2
	v_cvt_f32_i32_e32 v141, v97
	v_cvt_f32_i32_e32 v140, v96
	v_cvt_f32_i32_e32 v171, v91
	v_cvt_f32_i32_e32 v170, v90
	v_cvt_f32_i32_e32 v175, v87
	v_cvt_f32_i32_e32 v174, v86
	v_cvt_f32_i32_e32 v169, v89
	v_cvt_f32_i32_e32 v168, v88
	v_pk_mul_f32 v[140:141], v[136:137], v[140:141]
	s_waitcnt lgkmcnt(0)
	v_mov_b32_e32 v166, v165
	v_pk_fma_f32 v[172:173], v[140:141], v[164:165], v[166:167] op_sel_hi:[1,0,0]
	v_pk_mul_f32 v[140:141], v[134:135], v[170:171]
	v_cvt_f32_i32_e32 v143, v99
	v_cvt_f32_i32_e32 v142, v98
	v_pk_fma_f32 v[176:177], v[140:141], v[164:165], v[166:167] op_sel_hi:[1,0,0]
	v_pk_mul_f32 v[140:141], v[130:131], v[174:175]
	v_pk_mul_f32 v[168:169], v[132:133], v[168:169]
	v_cvt_f32_i32_e32 v171, v85
	v_cvt_f32_i32_e32 v170, v84
	v_pk_fma_f32 v[178:179], v[140:141], v[164:165], v[166:167] op_sel_hi:[1,0,0]
	v_cvt_f32_i32_e32 v181, v77
	v_cvt_f32_i32_e32 v180, v76
	v_pk_fma_f32 v[168:169], v[168:169], v[164:165], v[166:167] op_sel_hi:[1,0,0]
	v_cvt_pk_fp8_f32 v140, v172, v173
	v_pk_mul_f32 v[142:143], v[138:139], v[142:143]
	v_cvt_pk_fp8_f32 v141, v168, v169
	v_pk_fma_f32 v[142:143], v[142:143], v[164:165], v[166:167] op_sel_hi:[1,0,0]
	v_pk_mul_f32 v[170:171], v[128:129], v[170:171]
	v_cvt_f32_i32_e32 v175, v79
	v_cvt_f32_i32_e32 v174, v78
	v_pk_mul_f32 v[168:169], v[124:125], v[180:181]
	v_pk_fma_f32 v[170:171], v[170:171], v[164:165], v[166:167] op_sel_hi:[1,0,0]
	v_pk_fma_f32 v[168:169], v[168:169], v[164:165], v[166:167] op_sel_hi:[1,0,0]
	v_cvt_pk_fp8_f32 v140, v142, v143 op_sel:[0,0,1]
	v_cvt_pk_fp8_f32 v141, v176, v177 op_sel:[0,0,1]
	v_cvt_pk_fp8_f32 v142, v170, v171
	v_cvt_pk_fp8_f32 v143, v168, v169
	v_pk_mul_f32 v[174:175], v[126:127], v[174:175]
	s_mov_b32 s23, s22
	v_pk_fma_f32 v[164:165], v[174:175], v[164:165], v[166:167] op_sel_hi:[1,0,0]
	v_cvt_pk_fp8_f32 v142, v178, v179 op_sel:[0,0,1]
	v_cvt_pk_fp8_f32 v143, v164, v165 op_sel:[0,0,1]
	v_mov_b64_e32 v[170:171], s[22:23]
	v_or_b32_e32 v194, 32, v146
	v_lshlrev_b64 v[168:169], 13, v[194:195]
	v_mfma_f32_16x16x32_fp8_fp8 v[164:167], v[140:141], v[170:171], 0
	v_lshl_add_u64 v[168:169], s[10:11], 0, v[168:169]
	v_lshl_add_u64 v[168:169], v[168:169], 0, v[144:145]
	global_store_dwordx4 v[168:169], v[140:143], off sc1
	s_nop 1
	v_mfma_f32_16x16x32_fp8_fp8 v[140:143], v[142:143], v[170:171], v[164:167]
	s_and_saveexec_b64 s[0:1], s[20:21]
	s_cbranch_execz .LBB2_58
	s_lshl_b32 s4, s64, 2
	s_or_b32 s4, s4, s46
	s_ashr_i32 s5, s4, 31
	s_lshl_b64 s[4:5], s[4:5], 14
	s_add_u32 s4, s2, s4
	s_addc_u32 s5, s3, s5
	v_lshl_add_u64 v[164:165], v[146:147], 2, s[4:5]
	v_lshlrev_b32_e32 v194, 2, v192
	v_lshl_add_u64 v[164:165], v[164:165], 0, v[194:195]
	global_store_dwordx4 v[164:165], v[140:143], off offset:128 sc1
.LBB2_58:
	s_or_b64 exec, exec, s[0:1]
	v_add_u32_e32 v164, 0xc0, v162
	ds_read2st64_b32 v[166:167], v164 offset1:4
	s_nop 2
	v_cvt_f32_i32_e32 v141, v81
	v_cvt_f32_i32_e32 v140, v80
	v_cvt_f32_i32_e32 v173, v75
	v_cvt_f32_i32_e32 v172, v74
	v_cvt_f32_i32_e32 v177, v71
	v_cvt_f32_i32_e32 v176, v70
	v_cvt_f32_i32_e32 v171, v73
	v_cvt_f32_i32_e32 v170, v72
	v_pk_mul_f32 v[140:141], v[136:137], v[140:141]
	s_waitcnt lgkmcnt(0)
	v_mov_b32_e32 v168, v167
	v_pk_fma_f32 v[174:175], v[140:141], v[166:167], v[168:169] op_sel_hi:[1,0,0]
	v_pk_mul_f32 v[140:141], v[134:135], v[172:173]
	v_cvt_f32_i32_e32 v143, v83
	v_cvt_f32_i32_e32 v142, v82
	v_pk_fma_f32 v[178:179], v[140:141], v[166:167], v[168:169] op_sel_hi:[1,0,0]
	v_pk_mul_f32 v[140:141], v[130:131], v[176:177]
	v_pk_mul_f32 v[170:171], v[132:133], v[170:171]
	v_cvt_f32_i32_e32 v173, v69
	v_cvt_f32_i32_e32 v172, v68
	v_pk_fma_f32 v[176:177], v[140:141], v[166:167], v[168:169] op_sel_hi:[1,0,0]
	v_cvt_f32_i32_e32 v181, v65
	v_cvt_f32_i32_e32 v180, v64
	v_pk_fma_f32 v[170:171], v[170:171], v[166:167], v[168:169] op_sel_hi:[1,0,0]
	v_cvt_pk_fp8_f32 v140, v174, v175
	v_pk_mul_f32 v[142:143], v[138:139], v[142:143]
	v_cvt_pk_fp8_f32 v141, v170, v171
	v_pk_fma_f32 v[142:143], v[142:143], v[166:167], v[168:169] op_sel_hi:[1,0,0]
	v_pk_mul_f32 v[172:173], v[128:129], v[172:173]
	v_cvt_f32_i32_e32 v183, v67
	v_cvt_f32_i32_e32 v182, v66
	v_pk_mul_f32 v[170:171], v[124:125], v[180:181]
	v_pk_fma_f32 v[172:173], v[172:173], v[166:167], v[168:169] op_sel_hi:[1,0,0]
	v_pk_fma_f32 v[170:171], v[170:171], v[166:167], v[168:169] op_sel_hi:[1,0,0]
	v_cvt_pk_fp8_f32 v140, v142, v143 op_sel:[0,0,1]
	v_cvt_pk_fp8_f32 v141, v178, v179 op_sel:[0,0,1]
	v_cvt_pk_fp8_f32 v142, v172, v173
	v_cvt_pk_fp8_f32 v143, v170, v171
	v_pk_mul_f32 v[170:171], v[126:127], v[182:183]
	v_mov_b64_e32 v[172:173], s[22:23]
	v_pk_fma_f32 v[166:167], v[170:171], v[166:167], v[168:169] op_sel_hi:[1,0,0]
	v_cvt_pk_fp8_f32 v142, v176, v177 op_sel:[0,0,1]
	v_cvt_pk_fp8_f32 v143, v166, v167 op_sel:[0,0,1]
	v_or_b32_e32 v194, 48, v146
	v_mfma_f32_16x16x32_fp8_fp8 v[166:169], v[140:141], v[172:173], 0
	v_lshlrev_b64 v[170:171], 13, v[194:195]
	v_lshl_add_u64 v[170:171], s[10:11], 0, v[170:171]
	v_lshl_add_u64 v[170:171], v[170:171], 0, v[144:145]
	global_store_dwordx4 v[170:171], v[140:143], off sc1
	s_nop 1
	v_mfma_f32_16x16x32_fp8_fp8 v[140:143], v[142:143], v[172:173], v[166:169]
	s_and_saveexec_b64 s[0:1], s[20:21]
	s_cbranch_execz .LBB2_60
	s_lshl_b32 s4, s64, 2
	s_or_b32 s4, s4, s46
	s_ashr_i32 s5, s4, 31
	s_lshl_b64 s[4:5], s[4:5], 14
	s_add_u32 s4, s2, s4
	s_addc_u32 s5, s3, s5
	v_lshl_add_u64 v[166:167], v[146:147], 2, s[4:5]
	v_lshlrev_b32_e32 v194, 2, v192
	v_lshl_add_u64 v[166:167], v[166:167], 0, v[194:195]
	global_store_dwordx4 v[166:167], v[140:143], off offset:192 sc1
.LBB2_60:
	s_or_b64 exec, exec, s[0:1]
	ds_read2st64_b32 v[166:167], v162 offset0:2 offset1:6
	s_nop 3
	v_cvt_f32_i32_e32 v141, v61
	v_cvt_f32_i32_e32 v140, v60
	v_cvt_f32_i32_e32 v173, v59
	v_cvt_f32_i32_e32 v172, v58
	v_cvt_f32_i32_e32 v177, v51
	v_cvt_f32_i32_e32 v176, v50
	v_cvt_f32_i32_e32 v171, v57
	v_cvt_f32_i32_e32 v170, v56
	v_pk_mul_f32 v[140:141], v[136:137], v[140:141]
	s_waitcnt lgkmcnt(0)
	v_mov_b32_e32 v168, v167
	v_pk_fma_f32 v[174:175], v[140:141], v[166:167], v[168:169] op_sel_hi:[1,0,0]
	v_pk_mul_f32 v[140:141], v[134:135], v[172:173]
	v_cvt_f32_i32_e32 v143, v63
	v_cvt_f32_i32_e32 v142, v62
	v_pk_fma_f32 v[178:179], v[140:141], v[166:167], v[168:169] op_sel_hi:[1,0,0]
	v_pk_mul_f32 v[140:141], v[130:131], v[176:177]
	v_pk_mul_f32 v[170:171], v[132:133], v[170:171]
	v_cvt_f32_i32_e32 v173, v49
	v_cvt_f32_i32_e32 v172, v48
	v_pk_fma_f32 v[176:177], v[140:141], v[166:167], v[168:169] op_sel_hi:[1,0,0]
	v_cvt_f32_i32_e32 v181, v41
	v_cvt_f32_i32_e32 v180, v40
	v_pk_fma_f32 v[170:171], v[170:171], v[166:167], v[168:169] op_sel_hi:[1,0,0]
	v_cvt_pk_fp8_f32 v140, v174, v175
	v_pk_mul_f32 v[142:143], v[138:139], v[142:143]
	v_cvt_pk_fp8_f32 v141, v170, v171
	v_pk_fma_f32 v[142:143], v[142:143], v[166:167], v[168:169] op_sel_hi:[1,0,0]
	v_pk_mul_f32 v[172:173], v[128:129], v[172:173]
	v_cvt_f32_i32_e32 v183, v43
	v_cvt_f32_i32_e32 v182, v42
	v_pk_mul_f32 v[170:171], v[124:125], v[180:181]
	v_pk_fma_f32 v[172:173], v[172:173], v[166:167], v[168:169] op_sel_hi:[1,0,0]
	v_pk_fma_f32 v[170:171], v[170:171], v[166:167], v[168:169] op_sel_hi:[1,0,0]
	v_cvt_pk_fp8_f32 v140, v142, v143 op_sel:[0,0,1]
	v_cvt_pk_fp8_f32 v141, v178, v179 op_sel:[0,0,1]
	v_cvt_pk_fp8_f32 v142, v172, v173
	v_cvt_pk_fp8_f32 v143, v170, v171
	v_pk_mul_f32 v[170:171], v[126:127], v[182:183]
	s_mov_b32 s23, s22
	v_pk_fma_f32 v[166:167], v[170:171], v[166:167], v[168:169] op_sel_hi:[1,0,0]
	v_cvt_pk_fp8_f32 v142, v176, v177 op_sel:[0,0,1]
	v_cvt_pk_fp8_f32 v143, v166, v167 op_sel:[0,0,1]
	v_mov_b64_e32 v[172:173], s[22:23]
	v_add_u32_e32 v194, 0x80, v146
	v_lshlrev_b64 v[170:171], 13, v[194:195]
	v_mfma_f32_16x16x32_fp8_fp8 v[166:169], v[140:141], v[172:173], 0
	v_lshl_add_u64 v[170:171], s[10:11], 0, v[170:171]
	v_lshl_add_u64 v[170:171], v[170:171], 0, v[144:145]
	global_store_dwordx4 v[170:171], v[140:143], off sc1
	s_nop 1
	v_mfma_f32_16x16x32_fp8_fp8 v[140:143], v[142:143], v[172:173], v[166:169]
	s_and_saveexec_b64 s[0:1], s[20:21]
	s_cbranch_execz .LBB2_62
	s_lshl_b32 s4, s64, 2
	s_or_b32 s4, s4, s46
	s_ashr_i32 s5, s4, 31
	s_lshl_b64 s[4:5], s[4:5], 14
	s_add_u32 s4, s2, s4
	s_addc_u32 s5, s3, s5
	v_lshl_add_u64 v[166:167], v[146:147], 2, s[4:5]
	v_lshlrev_b32_e32 v194, 2, v192
	v_lshl_add_u64 v[166:167], v[166:167], 0, v[194:195]
	global_store_dwordx4 v[166:167], v[140:143], off offset:512 sc1
.LBB2_62:
	s_or_b64 exec, exec, s[0:1]
	ds_read2st64_b32 v[166:167], v160 offset0:2 offset1:6
	s_nop 3
	v_cvt_f32_i32_e32 v141, v53
	v_cvt_f32_i32_e32 v140, v52
	v_cvt_f32_i32_e32 v171, v47
	v_cvt_f32_i32_e32 v170, v46
	v_cvt_f32_i32_e32 v175, v35
	v_cvt_f32_i32_e32 v174, v34
	v_cvt_f32_i32_e32 v169, v45
	v_cvt_f32_i32_e32 v168, v44
	v_pk_mul_f32 v[140:141], v[136:137], v[140:141]
	s_waitcnt lgkmcnt(0)
	v_mov_b32_e32 v160, v167
	v_pk_fma_f32 v[172:173], v[140:141], v[166:167], v[160:161] op_sel_hi:[1,0,0]
	v_pk_mul_f32 v[140:141], v[134:135], v[170:171]
	v_cvt_f32_i32_e32 v143, v55
	v_cvt_f32_i32_e32 v142, v54
	v_pk_fma_f32 v[176:177], v[140:141], v[166:167], v[160:161] op_sel_hi:[1,0,0]
	v_pk_mul_f32 v[140:141], v[130:131], v[174:175]
	v_pk_mul_f32 v[168:169], v[132:133], v[168:169]
	v_cvt_f32_i32_e32 v171, v33
	v_cvt_f32_i32_e32 v170, v32
	v_pk_fma_f32 v[174:175], v[140:141], v[166:167], v[160:161] op_sel_hi:[1,0,0]
	v_cvt_f32_i32_e32 v179, v25
	v_cvt_f32_i32_e32 v178, v24
	v_pk_fma_f32 v[168:169], v[168:169], v[166:167], v[160:161] op_sel_hi:[1,0,0]
	v_cvt_pk_fp8_f32 v140, v172, v173
	v_pk_mul_f32 v[142:143], v[138:139], v[142:143]
	v_cvt_pk_fp8_f32 v141, v168, v169
	v_pk_fma_f32 v[142:143], v[142:143], v[166:167], v[160:161] op_sel_hi:[1,0,0]
	v_pk_mul_f32 v[170:171], v[128:129], v[170:171]
	v_cvt_f32_i32_e32 v181, v27
	v_cvt_f32_i32_e32 v180, v26
	v_pk_mul_f32 v[168:169], v[124:125], v[178:179]
	v_pk_fma_f32 v[170:171], v[170:171], v[166:167], v[160:161] op_sel_hi:[1,0,0]
	v_pk_fma_f32 v[168:169], v[168:169], v[166:167], v[160:161] op_sel_hi:[1,0,0]
	v_cvt_pk_fp8_f32 v140, v142, v143 op_sel:[0,0,1]
	v_cvt_pk_fp8_f32 v141, v176, v177 op_sel:[0,0,1]
	v_cvt_pk_fp8_f32 v142, v170, v171
	v_cvt_pk_fp8_f32 v143, v168, v169
	v_pk_mul_f32 v[168:169], v[126:127], v[180:181]
	v_mov_b64_e32 v[172:173], s[22:23]
	v_pk_fma_f32 v[166:167], v[168:169], v[166:167], v[160:161] op_sel_hi:[1,0,0]
	v_cvt_pk_fp8_f32 v142, v174, v175 op_sel:[0,0,1]
	v_cvt_pk_fp8_f32 v143, v166, v167 op_sel:[0,0,1]
	v_add_u32_e32 v194, 0x90, v146
	v_mfma_f32_16x16x32_fp8_fp8 v[166:169], v[140:141], v[172:173], 0
	v_lshlrev_b64 v[170:171], 13, v[194:195]
	v_lshl_add_u64 v[170:171], s[10:11], 0, v[170:171]
	v_lshl_add_u64 v[170:171], v[170:171], 0, v[144:145]
	global_store_dwordx4 v[170:171], v[140:143], off sc1
	s_nop 1
	v_mfma_f32_16x16x32_fp8_fp8 v[140:143], v[142:143], v[172:173], v[166:169]
	s_and_saveexec_b64 s[0:1], s[20:21]
	s_cbranch_execz .LBB2_64
	s_lshl_b32 s4, s64, 2
	s_or_b32 s4, s4, s46
	s_ashr_i32 s5, s4, 31
	s_lshl_b64 s[4:5], s[4:5], 14
	s_add_u32 s4, s2, s4
	s_addc_u32 s5, s3, s5
	v_lshl_add_u64 v[166:167], v[146:147], 2, s[4:5]
	v_lshlrev_b32_e32 v194, 2, v192
	v_lshl_add_u64 v[166:167], v[166:167], 0, v[194:195]
	global_store_dwordx4 v[166:167], v[140:143], off offset:576 sc1
.LBB2_64:
	s_or_b64 exec, exec, s[0:1]
	ds_read2st64_b32 v[160:161], v161 offset0:2 offset1:6
	s_nop 3
	v_cvt_f32_i32_e32 v141, v37
	v_cvt_f32_i32_e32 v140, v36
	v_cvt_f32_i32_e32 v171, v31
	v_cvt_f32_i32_e32 v170, v30
	v_cvt_f32_i32_e32 v175, v19
	v_cvt_f32_i32_e32 v174, v18
	v_cvt_f32_i32_e32 v169, v29
	v_cvt_f32_i32_e32 v168, v28
	v_pk_mul_f32 v[140:141], v[136:137], v[140:141]
	s_waitcnt lgkmcnt(0)
	v_mov_b32_e32 v166, v161
	v_pk_fma_f32 v[172:173], v[140:141], v[160:161], v[166:167] op_sel_hi:[1,0,0]
	v_pk_mul_f32 v[140:141], v[134:135], v[170:171]
	v_cvt_f32_i32_e32 v143, v39
	v_cvt_f32_i32_e32 v142, v38
	v_pk_fma_f32 v[176:177], v[140:141], v[160:161], v[166:167] op_sel_hi:[1,0,0]
	v_pk_mul_f32 v[140:141], v[130:131], v[174:175]
	v_pk_mul_f32 v[168:169], v[132:133], v[168:169]
	v_cvt_f32_i32_e32 v171, v17
	v_cvt_f32_i32_e32 v170, v16
	v_pk_fma_f32 v[178:179], v[140:141], v[160:161], v[166:167] op_sel_hi:[1,0,0]
	v_cvt_f32_i32_e32 v181, v9
	v_cvt_f32_i32_e32 v180, v8
	v_pk_fma_f32 v[168:169], v[168:169], v[160:161], v[166:167] op_sel_hi:[1,0,0]
	v_cvt_pk_fp8_f32 v140, v172, v173
	v_pk_mul_f32 v[142:143], v[138:139], v[142:143]
	v_cvt_pk_fp8_f32 v141, v168, v169
	v_pk_fma_f32 v[142:143], v[142:143], v[160:161], v[166:167] op_sel_hi:[1,0,0]
	v_pk_mul_f32 v[170:171], v[128:129], v[170:171]
	v_cvt_f32_i32_e32 v175, v11
	v_cvt_f32_i32_e32 v174, v10
	v_pk_mul_f32 v[168:169], v[124:125], v[180:181]
	v_pk_fma_f32 v[170:171], v[170:171], v[160:161], v[166:167] op_sel_hi:[1,0,0]
	v_pk_fma_f32 v[168:169], v[168:169], v[160:161], v[166:167] op_sel_hi:[1,0,0]
	v_cvt_pk_fp8_f32 v140, v142, v143 op_sel:[0,0,1]
	v_cvt_pk_fp8_f32 v141, v176, v177 op_sel:[0,0,1]
	v_cvt_pk_fp8_f32 v142, v170, v171
	v_cvt_pk_fp8_f32 v143, v168, v169
	v_pk_mul_f32 v[174:175], v[126:127], v[174:175]
	s_mov_b32 s23, s22
	v_pk_fma_f32 v[160:161], v[174:175], v[160:161], v[166:167] op_sel_hi:[1,0,0]
	v_cvt_pk_fp8_f32 v142, v178, v179 op_sel:[0,0,1]
	v_cvt_pk_fp8_f32 v143, v160, v161 op_sel:[0,0,1]
	v_mov_b64_e32 v[170:171], s[22:23]
	v_add_u32_e32 v194, 0xa0, v146
	v_lshlrev_b64 v[160:161], 13, v[194:195]
	v_mfma_f32_16x16x32_fp8_fp8 v[166:169], v[140:141], v[170:171], 0
	v_lshl_add_u64 v[160:161], s[10:11], 0, v[160:161]
	v_lshl_add_u64 v[160:161], v[160:161], 0, v[144:145]
	global_store_dwordx4 v[160:161], v[140:143], off sc1
	s_nop 1
	v_mfma_f32_16x16x32_fp8_fp8 v[140:143], v[142:143], v[170:171], v[166:169]
	s_and_saveexec_b64 s[0:1], s[20:21]
	s_cbranch_execz .LBB2_66
	s_lshl_b32 s4, s64, 2
	s_or_b32 s4, s4, s46
	s_ashr_i32 s5, s4, 31
	s_lshl_b64 s[4:5], s[4:5], 14
	s_add_u32 s4, s2, s4
	s_addc_u32 s5, s3, s5
	v_lshl_add_u64 v[160:161], v[146:147], 2, s[4:5]
	v_lshlrev_b32_e32 v194, 2, v192
	v_lshl_add_u64 v[160:161], v[160:161], 0, v[194:195]
	global_store_dwordx4 v[160:161], v[140:143], off offset:640 sc1
.LBB2_66:
	s_or_b64 exec, exec, s[0:1]
	ds_read2st64_b32 v[160:161], v164 offset0:2 offset1:6
	s_nop 3
	v_cvt_f32_i32_e32 v141, v21
	v_cvt_f32_i32_e32 v140, v20
	v_cvt_f32_i32_e32 v169, v15
	v_cvt_f32_i32_e32 v168, v14
	v_cvt_f32_i32_e32 v173, v7
	v_cvt_f32_i32_e32 v172, v6
	v_cvt_f32_i32_e32 v167, v13
	v_cvt_f32_i32_e32 v166, v12
	v_pk_mul_f32 v[140:141], v[136:137], v[140:141]
	s_waitcnt lgkmcnt(0)
	v_mov_b32_e32 v164, v161
	v_pk_fma_f32 v[170:171], v[140:141], v[160:161], v[164:165] op_sel_hi:[1,0,0]
	v_pk_mul_f32 v[140:141], v[134:135], v[168:169]
	v_cvt_f32_i32_e32 v143, v23
	v_cvt_f32_i32_e32 v142, v22
	v_pk_fma_f32 v[174:175], v[140:141], v[160:161], v[164:165] op_sel_hi:[1,0,0]
	v_pk_mul_f32 v[140:141], v[130:131], v[172:173]
	v_pk_mul_f32 v[166:167], v[132:133], v[166:167]
	v_cvt_f32_i32_e32 v169, v5
	v_cvt_f32_i32_e32 v168, v4
	v_pk_fma_f32 v[172:173], v[140:141], v[160:161], v[164:165] op_sel_hi:[1,0,0]
	v_cvt_f32_i32_e32 v177, v1
	v_cvt_f32_i32_e32 v176, v0
	v_pk_fma_f32 v[166:167], v[166:167], v[160:161], v[164:165] op_sel_hi:[1,0,0]
	v_cvt_pk_fp8_f32 v140, v170, v171
	v_pk_mul_f32 v[142:143], v[138:139], v[142:143]
	v_cvt_pk_fp8_f32 v141, v166, v167
	v_pk_fma_f32 v[142:143], v[142:143], v[160:161], v[164:165] op_sel_hi:[1,0,0]
	v_pk_mul_f32 v[168:169], v[128:129], v[168:169]
	v_cvt_f32_i32_e32 v179, v3
	v_cvt_f32_i32_e32 v178, v2
	v_pk_mul_f32 v[166:167], v[124:125], v[176:177]
	v_pk_fma_f32 v[168:169], v[168:169], v[160:161], v[164:165] op_sel_hi:[1,0,0]
	v_pk_fma_f32 v[166:167], v[166:167], v[160:161], v[164:165] op_sel_hi:[1,0,0]
	v_cvt_pk_fp8_f32 v140, v142, v143 op_sel:[0,0,1]
	v_cvt_pk_fp8_f32 v141, v174, v175 op_sel:[0,0,1]
	v_cvt_pk_fp8_f32 v142, v168, v169
	v_cvt_pk_fp8_f32 v143, v166, v167
	v_pk_mul_f32 v[166:167], v[126:127], v[178:179]
	v_mov_b64_e32 v[168:169], s[22:23]
	v_pk_fma_f32 v[160:161], v[166:167], v[160:161], v[164:165] op_sel_hi:[1,0,0]
	v_cvt_pk_fp8_f32 v142, v172, v173 op_sel:[0,0,1]
	v_cvt_pk_fp8_f32 v143, v160, v161 op_sel:[0,0,1]
	v_add_u32_e32 v194, 0xb0, v146
	v_mfma_f32_16x16x32_fp8_fp8 v[164:167], v[140:141], v[168:169], 0
	v_lshlrev_b64 v[160:161], 13, v[194:195]
	v_lshl_add_u64 v[160:161], s[10:11], 0, v[160:161]
	v_lshl_add_u64 v[160:161], v[160:161], 0, v[144:145]
	global_store_dwordx4 v[160:161], v[140:143], off sc1
	s_mov_b64 s[0:1], s[20:21]
	s_nop 0
	v_mfma_f32_16x16x32_fp8_fp8 v[140:143], v[142:143], v[168:169], v[164:167]
	v_mov_b64_e32 v[160:161], v[194:195]
	s_branch .LBB2_83
.LBB2_67:
	s_mov_b64 s[0:1], 0
	s_cbranch_execz .LBB2_83
	v_cvt_f32_i32_e32 v141, v121
	v_cvt_f32_i32_e32 v143, v123
	v_cvt_f32_i32_e32 v142, v122
	v_cvt_f32_i32_e32 v140, v120
	v_cvt_f32_i32_e32 v169, v119
	v_cvt_f32_i32_e32 v168, v118
	s_waitcnt lgkmcnt(2)
	v_pk_mul_f32 v[142:143], v[134:135], v[142:143]
	v_pk_mul_f32 v[140:141], v[132:133], v[140:141]
	v_mov_b32_e32 v160, v154
	v_mov_b32_e32 v161, v154
	v_mov_b32_e32 v164, v152
	v_mov_b32_e32 v165, v152
	v_pk_fma_f32 v[142:143], v[142:143], v[164:165], v[160:161]
	v_pk_fma_f32 v[140:141], v[140:141], v[152:153], v[154:155]
	v_cvt_f32_i32_e32 v167, v117
	v_cvt_f32_i32_e32 v166, v116
	v_pk_mul_f32 v[170:171], v[142:143], v[142:143]
	v_pk_mul_f32 v[142:143], v[140:141], v[140:141]
	s_waitcnt lgkmcnt(1)
	v_pk_mul_f32 v[140:141], v[130:131], v[168:169]
	v_cvt_f32_i32_e32 v169, v113
	v_cvt_f32_i32_e32 v168, v112
	v_pk_fma_f32 v[140:141], v[140:141], v[164:165], v[160:161]
	v_pk_mul_f32 v[156:157], v[156:157], v[156:157]
	v_pk_mul_f32 v[174:175], v[140:141], v[140:141]
	v_pk_mul_f32 v[166:167], v[128:129], v[166:167]
	v_cvt_pk_fp8_f32 v140, v156, v157
	v_cvt_pk_fp8_f32 v141, v142, v143
	v_cvt_f32_i32_e32 v173, v115
	v_cvt_f32_i32_e32 v172, v114
	s_waitcnt lgkmcnt(0)
	v_pk_mul_f32 v[168:169], v[124:125], v[168:169]
	v_pk_fma_f32 v[166:167], v[166:167], v[152:153], v[154:155]
	v_pk_fma_f32 v[152:153], v[168:169], v[152:153], v[154:155]
	v_pk_mul_f32 v[158:159], v[158:159], v[158:159]
	v_pk_mul_f32 v[166:167], v[166:167], v[166:167]
	v_pk_mul_f32 v[152:153], v[152:153], v[152:153]
	v_cvt_pk_fp8_f32 v140, v158, v159 op_sel:[0,0,1]
	v_cvt_pk_fp8_f32 v142, v166, v167
	v_cvt_pk_fp8_f32 v143, v152, v153
	v_cvt_pk_fp8_f32 v141, v170, v171 op_sel:[0,0,1]
	v_pk_mul_f32 v[172:173], v[126:127], v[172:173]
	v_cvt_pk_fp8_f32 v142, v174, v175 op_sel:[0,0,1]
	v_pk_fma_f32 v[156:157], v[172:173], v[164:165], v[160:161]
	s_mov_b32 s23, s22
	v_pk_mul_f32 v[152:153], v[156:157], v[156:157]
	v_mov_b64_e32 v[158:159], s[22:23]
	v_cvt_pk_fp8_f32 v143, v152, v153 op_sel:[0,0,1]
	v_ashrrev_i32_e32 v147, 31, v146
	v_mfma_f32_16x16x32_fp8_fp8 v[152:155], v[140:141], v[158:159], 0
	v_lshlrev_b64 v[156:157], 13, v[146:147]
	v_lshl_add_u64 v[156:157], s[10:11], 0, v[156:157]
	v_lshl_add_u64 v[156:157], v[156:157], 0, v[144:145]
	global_store_dwordx4 v[156:157], v[140:143], off sc1
	s_nop 1
	v_mfma_f32_16x16x32_fp8_fp8 v[140:143], v[142:143], v[158:159], v[152:155]
	s_and_saveexec_b64 s[0:1], s[20:21]
	s_cbranch_execz .LBB2_70
	s_lshl_b32 s4, s64, 2
	s_or_b32 s4, s4, s46
	s_ashr_i32 s5, s4, 31
	s_lshl_b64 s[4:5], s[4:5], 14
	s_add_u32 s4, s2, s4
	s_addc_u32 s5, s3, s5
	v_lshl_add_u64 v[152:153], v[146:147], 2, s[4:5]
	v_lshlrev_b32_e32 v194, 2, v192
	v_lshl_add_u64 v[152:153], v[152:153], 0, v[194:195]
	global_store_dwordx4 v[152:153], v[140:143], off sc1
.LBB2_70:
	s_or_b64 exec, exec, s[0:1]
	v_add_u32_e32 v154, 64, v162
	s_nop 3
	ds_read2st64_b32 v[142:143], v154 offset1:4
	v_cvt_f32_i32_e32 v141, v109
	v_cvt_f32_i32_e32 v140, v108
	v_cvt_f32_i32_e32 v161, v107
	v_cvt_f32_i32_e32 v160, v106
	s_waitcnt lgkmcnt(0)
	v_mov_b32_e32 v156, v143
	v_pk_mul_f32 v[140:141], v[136:137], v[140:141]
	v_cvt_f32_i32_e32 v167, v103
	v_cvt_f32_i32_e32 v166, v102
	v_pk_fma_f32 v[140:141], v[140:141], v[142:143], v[156:157] op_sel_hi:[1,0,0]
	v_cvt_f32_i32_e32 v159, v105
	v_pk_mul_f32 v[164:165], v[140:141], v[140:141]
	v_pk_mul_f32 v[140:141], v[134:135], v[160:161]
	v_cvt_f32_i32_e32 v158, v104
	v_pk_fma_f32 v[140:141], v[140:141], v[142:143], v[156:157] op_sel_hi:[1,0,0]
	v_cvt_f32_i32_e32 v153, v111
	v_pk_mul_f32 v[168:169], v[140:141], v[140:141]
	v_pk_mul_f32 v[140:141], v[130:131], v[166:167]
	v_cvt_f32_i32_e32 v167, v93
	v_cvt_f32_i32_e32 v166, v92
	v_cvt_f32_i32_e32 v152, v110
	v_pk_mul_f32 v[158:159], v[132:133], v[158:159]
	v_cvt_f32_i32_e32 v161, v101
	v_cvt_f32_i32_e32 v160, v100
	v_pk_fma_f32 v[140:141], v[140:141], v[142:143], v[156:157] op_sel_hi:[1,0,0]
	v_pk_fma_f32 v[158:159], v[158:159], v[142:143], v[156:157] op_sel_hi:[1,0,0]
	v_cvt_f32_i32_e32 v171, v95
	v_cvt_f32_i32_e32 v170, v94
	v_pk_mul_f32 v[172:173], v[140:141], v[140:141]
	v_pk_mul_f32 v[140:141], v[124:125], v[166:167]
	v_pk_mul_f32 v[158:159], v[158:159], v[158:159]
	v_pk_fma_f32 v[166:167], v[140:141], v[142:143], v[156:157] op_sel_hi:[1,0,0]
	v_pk_mul_f32 v[152:153], v[138:139], v[152:153]
	v_cvt_pk_fp8_f32 v140, v164, v165
	v_cvt_pk_fp8_f32 v141, v158, v159
	v_pk_mul_f32 v[160:161], v[128:129], v[160:161]
	v_pk_fma_f32 v[152:153], v[152:153], v[142:143], v[156:157] op_sel_hi:[1,0,0]
	v_pk_fma_f32 v[160:161], v[160:161], v[142:143], v[156:157] op_sel_hi:[1,0,0]
	v_pk_mul_f32 v[170:171], v[126:127], v[170:171]
	v_pk_mul_f32 v[152:153], v[152:153], v[152:153]
	v_pk_mul_f32 v[160:161], v[160:161], v[160:161]
	v_pk_fma_f32 v[156:157], v[170:171], v[142:143], v[156:157] op_sel_hi:[1,0,0]
	v_pk_mul_f32 v[158:159], v[166:167], v[166:167]
	v_cvt_pk_fp8_f32 v140, v152, v153 op_sel:[0,0,1]
	v_cvt_pk_fp8_f32 v141, v168, v169 op_sel:[0,0,1]
	v_cvt_pk_fp8_f32 v142, v160, v161
	v_cvt_pk_fp8_f32 v143, v158, v159
	v_pk_mul_f32 v[152:153], v[156:157], v[156:157]
	v_or_b32_e32 v156, 16, v146
	v_cvt_pk_fp8_f32 v142, v172, v173 op_sel:[0,0,1]
	v_cvt_pk_fp8_f32 v143, v152, v153 op_sel:[0,0,1]
	v_ashrrev_i32_e32 v157, 31, v156
	v_mov_b64_e32 v[160:161], s[22:23]
	v_lshlrev_b64 v[152:153], 13, v[156:157]
	v_lshl_add_u64 v[152:153], s[10:11], 0, v[152:153]
	v_mfma_f32_16x16x32_fp8_fp8 v[156:159], v[140:141], v[160:161], 0
	v_lshl_add_u64 v[152:153], v[152:153], 0, v[144:145]
	global_store_dwordx4 v[152:153], v[140:143], off sc1
	s_nop 1
	v_mfma_f32_16x16x32_fp8_fp8 v[140:143], v[142:143], v[160:161], v[156:159]
	s_and_saveexec_b64 s[0:1], s[20:21]
	s_cbranch_execz .LBB2_72
	s_lshl_b32 s4, s64, 2
	s_or_b32 s4, s4, s46
	s_ashr_i32 s5, s4, 31
	s_lshl_b64 s[4:5], s[4:5], 14
	s_add_u32 s4, s2, s4
	s_addc_u32 s5, s3, s5
	v_lshl_add_u64 v[152:153], v[146:147], 2, s[4:5]
	v_lshlrev_b32_e32 v194, 2, v192
	v_lshl_add_u64 v[152:153], v[152:153], 0, v[194:195]
	global_store_dwordx4 v[152:153], v[140:143], off offset:64 sc1
.LBB2_72:
	s_or_b64 exec, exec, s[0:1]
	v_add_u32_e32 v155, 0x80, v162
	s_nop 3
	ds_read2st64_b32 v[142:143], v155 offset1:4
	v_cvt_f32_i32_e32 v141, v97
	v_cvt_f32_i32_e32 v140, v96
	v_cvt_f32_i32_e32 v161, v91
	v_cvt_f32_i32_e32 v160, v90
	s_waitcnt lgkmcnt(0)
	v_mov_b32_e32 v156, v143
	v_pk_mul_f32 v[140:141], v[136:137], v[140:141]
	v_cvt_f32_i32_e32 v167, v87
	v_cvt_f32_i32_e32 v166, v86
	v_pk_fma_f32 v[140:141], v[140:141], v[142:143], v[156:157] op_sel_hi:[1,0,0]
	v_cvt_f32_i32_e32 v159, v89
	v_pk_mul_f32 v[164:165], v[140:141], v[140:141]
	v_pk_mul_f32 v[140:141], v[134:135], v[160:161]
	v_cvt_f32_i32_e32 v158, v88
	v_pk_fma_f32 v[140:141], v[140:141], v[142:143], v[156:157] op_sel_hi:[1,0,0]
	v_cvt_f32_i32_e32 v153, v99
	v_pk_mul_f32 v[168:169], v[140:141], v[140:141]
	v_pk_mul_f32 v[140:141], v[130:131], v[166:167]
	v_cvt_f32_i32_e32 v167, v77
	v_cvt_f32_i32_e32 v166, v76
	v_cvt_f32_i32_e32 v152, v98
	v_pk_mul_f32 v[158:159], v[132:133], v[158:159]
	v_cvt_f32_i32_e32 v161, v85
	v_cvt_f32_i32_e32 v160, v84
	v_pk_fma_f32 v[140:141], v[140:141], v[142:143], v[156:157] op_sel_hi:[1,0,0]
	v_cvt_f32_i32_e32 v171, v79
	v_cvt_f32_i32_e32 v170, v78
	v_pk_fma_f32 v[158:159], v[158:159], v[142:143], v[156:157] op_sel_hi:[1,0,0]
	v_pk_mul_f32 v[172:173], v[140:141], v[140:141]
	v_pk_mul_f32 v[140:141], v[124:125], v[166:167]
	v_pk_mul_f32 v[158:159], v[158:159], v[158:159]
	v_pk_fma_f32 v[166:167], v[140:141], v[142:143], v[156:157] op_sel_hi:[1,0,0]
	v_pk_mul_f32 v[152:153], v[138:139], v[152:153]
	v_cvt_pk_fp8_f32 v140, v164, v165
	v_cvt_pk_fp8_f32 v141, v158, v159
	v_pk_mul_f32 v[160:161], v[128:129], v[160:161]
	v_pk_mul_f32 v[170:171], v[126:127], v[170:171]
	v_pk_fma_f32 v[152:153], v[152:153], v[142:143], v[156:157] op_sel_hi:[1,0,0]
	v_pk_fma_f32 v[160:161], v[160:161], v[142:143], v[156:157] op_sel_hi:[1,0,0]
	v_pk_fma_f32 v[142:143], v[170:171], v[142:143], v[156:157] op_sel_hi:[1,0,0]
	v_pk_mul_f32 v[152:153], v[152:153], v[152:153]
	v_pk_mul_f32 v[160:161], v[160:161], v[160:161]
	v_pk_mul_f32 v[156:157], v[166:167], v[166:167]
	v_pk_mul_f32 v[164:165], v[142:143], v[142:143]
	v_cvt_pk_fp8_f32 v140, v152, v153 op_sel:[0,0,1]
	v_cvt_pk_fp8_f32 v142, v160, v161
	v_cvt_pk_fp8_f32 v143, v156, v157
	v_cvt_pk_fp8_f32 v141, v168, v169 op_sel:[0,0,1]
	s_mov_b32 s23, s22
	v_cvt_pk_fp8_f32 v142, v172, v173 op_sel:[0,0,1]
	v_cvt_pk_fp8_f32 v143, v164, v165 op_sel:[0,0,1]
	v_or_b32_e32 v152, 32, v146
	v_mov_b64_e32 v[160:161], s[22:23]
	v_ashrrev_i32_e32 v153, 31, v152
	v_lshlrev_b64 v[152:153], 13, v[152:153]
	v_mfma_f32_16x16x32_fp8_fp8 v[156:159], v[140:141], v[160:161], 0
	v_lshl_add_u64 v[152:153], s[10:11], 0, v[152:153]
	v_lshl_add_u64 v[152:153], v[152:153], 0, v[144:145]
	global_store_dwordx4 v[152:153], v[140:143], off sc1
	s_nop 1
	v_mfma_f32_16x16x32_fp8_fp8 v[140:143], v[142:143], v[160:161], v[156:159]
	s_and_saveexec_b64 s[0:1], s[20:21]
	s_cbranch_execz .LBB2_74
	s_lshl_b32 s4, s64, 2
	s_or_b32 s4, s4, s46
	s_ashr_i32 s5, s4, 31
	s_lshl_b64 s[4:5], s[4:5], 14
	s_add_u32 s4, s2, s4
	s_addc_u32 s5, s3, s5
	v_lshl_add_u64 v[152:153], v[146:147], 2, s[4:5]
	v_lshlrev_b32_e32 v194, 2, v192
	v_lshl_add_u64 v[152:153], v[152:153], 0, v[194:195]
	global_store_dwordx4 v[152:153], v[140:143], off offset:128 sc1
.LBB2_74:
	s_or_b64 exec, exec, s[0:1]
	v_add_u32_e32 v156, 0xc0, v162
	s_nop 3
	ds_read2st64_b32 v[142:143], v156 offset1:4
	v_cvt_f32_i32_e32 v141, v81
	v_cvt_f32_i32_e32 v140, v80
	v_cvt_f32_i32_e32 v165, v75
	v_cvt_f32_i32_e32 v164, v74
	s_waitcnt lgkmcnt(0)
	v_mov_b32_e32 v158, v143
	v_pk_mul_f32 v[140:141], v[136:137], v[140:141]
	v_cvt_f32_i32_e32 v169, v71
	v_cvt_f32_i32_e32 v168, v70
	v_pk_fma_f32 v[140:141], v[140:141], v[142:143], v[158:159] op_sel_hi:[1,0,0]
	v_cvt_f32_i32_e32 v161, v73
	v_pk_mul_f32 v[166:167], v[140:141], v[140:141]
	v_pk_mul_f32 v[140:141], v[134:135], v[164:165]
	v_cvt_f32_i32_e32 v160, v72
	v_pk_fma_f32 v[140:141], v[140:141], v[142:143], v[158:159] op_sel_hi:[1,0,0]
	v_cvt_f32_i32_e32 v153, v83
	v_pk_mul_f32 v[170:171], v[140:141], v[140:141]
	v_pk_mul_f32 v[140:141], v[130:131], v[168:169]
	v_cvt_f32_i32_e32 v169, v65
	v_cvt_f32_i32_e32 v168, v64
	v_cvt_f32_i32_e32 v152, v82
	v_pk_mul_f32 v[160:161], v[132:133], v[160:161]
	v_cvt_f32_i32_e32 v165, v69
	v_cvt_f32_i32_e32 v164, v68
	v_pk_fma_f32 v[140:141], v[140:141], v[142:143], v[158:159] op_sel_hi:[1,0,0]
	v_pk_fma_f32 v[160:161], v[160:161], v[142:143], v[158:159] op_sel_hi:[1,0,0]
	v_cvt_f32_i32_e32 v173, v67
	v_cvt_f32_i32_e32 v172, v66
	v_pk_mul_f32 v[174:175], v[140:141], v[140:141]
	v_pk_mul_f32 v[140:141], v[124:125], v[168:169]
	v_pk_mul_f32 v[160:161], v[160:161], v[160:161]
	v_pk_fma_f32 v[168:169], v[140:141], v[142:143], v[158:159] op_sel_hi:[1,0,0]
	v_pk_mul_f32 v[152:153], v[138:139], v[152:153]
	v_cvt_pk_fp8_f32 v140, v166, v167
	v_cvt_pk_fp8_f32 v141, v160, v161
	v_pk_mul_f32 v[164:165], v[128:129], v[164:165]
	v_pk_fma_f32 v[152:153], v[152:153], v[142:143], v[158:159] op_sel_hi:[1,0,0]
	v_pk_fma_f32 v[164:165], v[164:165], v[142:143], v[158:159] op_sel_hi:[1,0,0]
	v_pk_mul_f32 v[172:173], v[126:127], v[172:173]
	v_pk_mul_f32 v[152:153], v[152:153], v[152:153]
	v_pk_mul_f32 v[164:165], v[164:165], v[164:165]
	v_pk_fma_f32 v[158:159], v[172:173], v[142:143], v[158:159] op_sel_hi:[1,0,0]
	v_pk_mul_f32 v[160:161], v[168:169], v[168:169]
	v_cvt_pk_fp8_f32 v140, v152, v153 op_sel:[0,0,1]
	v_cvt_pk_fp8_f32 v141, v170, v171 op_sel:[0,0,1]
	v_cvt_pk_fp8_f32 v142, v164, v165
	v_cvt_pk_fp8_f32 v143, v160, v161
	v_pk_mul_f32 v[152:153], v[158:159], v[158:159]
	v_or_b32_e32 v158, 48, v146
	v_cvt_pk_fp8_f32 v142, v174, v175 op_sel:[0,0,1]
	v_cvt_pk_fp8_f32 v143, v152, v153 op_sel:[0,0,1]
	v_ashrrev_i32_e32 v159, 31, v158
	v_mov_b64_e32 v[164:165], s[22:23]
	v_lshlrev_b64 v[152:153], 13, v[158:159]
	v_lshl_add_u64 v[152:153], s[10:11], 0, v[152:153]
	v_mfma_f32_16x16x32_fp8_fp8 v[158:161], v[140:141], v[164:165], 0
	v_lshl_add_u64 v[152:153], v[152:153], 0, v[144:145]
	global_store_dwordx4 v[152:153], v[140:143], off sc1
	s_nop 1
	v_mfma_f32_16x16x32_fp8_fp8 v[140:143], v[142:143], v[164:165], v[158:161]
	s_and_saveexec_b64 s[0:1], s[20:21]
	s_cbranch_execz .LBB2_76
	s_lshl_b32 s4, s64, 2
	s_or_b32 s4, s4, s46
	s_ashr_i32 s5, s4, 31
	s_lshl_b64 s[4:5], s[4:5], 14
	s_add_u32 s4, s2, s4
	s_addc_u32 s5, s3, s5
	v_lshl_add_u64 v[152:153], v[146:147], 2, s[4:5]
	v_lshlrev_b32_e32 v194, 2, v192
	v_lshl_add_u64 v[152:153], v[152:153], 0, v[194:195]
	global_store_dwordx4 v[152:153], v[140:143], off offset:192 sc1
.LBB2_76:
	s_or_b64 exec, exec, s[0:1]
	s_nop 4
	ds_read2st64_b32 v[140:141], v162 offset0:2 offset1:6
	v_cvt_f32_i32_e32 v143, v61
	v_cvt_f32_i32_e32 v153, v63
	v_cvt_f32_i32_e32 v152, v62
	v_cvt_f32_i32_e32 v142, v60
	v_cvt_f32_i32_e32 v161, v57
	v_cvt_f32_i32_e32 v165, v59
	v_cvt_f32_i32_e32 v164, v58
	v_cvt_f32_i32_e32 v160, v56
	v_cvt_f32_i32_e32 v167, v49
	v_cvt_f32_i32_e32 v169, v51
	v_cvt_f32_i32_e32 v168, v50
	v_cvt_f32_i32_e32 v166, v48
	v_cvt_f32_i32_e32 v171, v41
	v_cvt_f32_i32_e32 v173, v43
	v_cvt_f32_i32_e32 v172, v42
	v_cvt_f32_i32_e32 v170, v40
	v_pk_mul_f32 v[152:153], v[138:139], v[152:153]
	v_pk_mul_f32 v[142:143], v[136:137], v[142:143]
	s_waitcnt lgkmcnt(0)
	v_mov_b32_e32 v158, v141
	v_pk_mul_f32 v[164:165], v[134:135], v[164:165]
	v_pk_mul_f32 v[160:161], v[132:133], v[160:161]
	v_pk_mul_f32 v[168:169], v[130:131], v[168:169]
	v_pk_mul_f32 v[166:167], v[128:129], v[166:167]
	v_pk_mul_f32 v[172:173], v[126:127], v[172:173]
	v_pk_mul_f32 v[170:171], v[124:125], v[170:171]
	v_pk_fma_f32 v[142:143], v[142:143], v[140:141], v[158:159] op_sel_hi:[1,0,0]
	v_pk_fma_f32 v[152:153], v[152:153], v[140:141], v[158:159] op_sel_hi:[1,0,0]
	v_pk_fma_f32 v[160:161], v[160:161], v[140:141], v[158:159] op_sel_hi:[1,0,0]
	v_pk_fma_f32 v[164:165], v[164:165], v[140:141], v[158:159] op_sel_hi:[1,0,0]
	v_pk_fma_f32 v[166:167], v[166:167], v[140:141], v[158:159] op_sel_hi:[1,0,0]
	v_pk_fma_f32 v[168:169], v[168:169], v[140:141], v[158:159] op_sel_hi:[1,0,0]
	v_pk_fma_f32 v[170:171], v[170:171], v[140:141], v[158:159] op_sel_hi:[1,0,0]
	v_pk_fma_f32 v[140:141], v[172:173], v[140:141], v[158:159] op_sel_hi:[1,0,0]
	v_pk_mul_f32 v[142:143], v[142:143], v[142:143]
	v_pk_mul_f32 v[160:161], v[160:161], v[160:161]
	v_pk_mul_f32 v[158:159], v[170:171], v[170:171]
	v_pk_mul_f32 v[170:171], v[140:141], v[140:141]
	v_pk_mul_f32 v[152:153], v[152:153], v[152:153]
	v_cvt_pk_fp8_f32 v140, v142, v143
	v_cvt_pk_fp8_f32 v141, v160, v161
	v_pk_mul_f32 v[164:165], v[164:165], v[164:165]
	v_pk_mul_f32 v[166:167], v[166:167], v[166:167]
	v_cvt_pk_fp8_f32 v140, v152, v153 op_sel:[0,0,1]
	v_cvt_pk_fp8_f32 v142, v166, v167
	v_cvt_pk_fp8_f32 v143, v158, v159
	v_cvt_pk_fp8_f32 v141, v164, v165 op_sel:[0,0,1]
	v_pk_mul_f32 v[168:169], v[168:169], v[168:169]
	s_mov_b32 s23, s22
	v_cvt_pk_fp8_f32 v142, v168, v169 op_sel:[0,0,1]
	v_cvt_pk_fp8_f32 v143, v170, v171 op_sel:[0,0,1]
	v_lshlrev_b64 v[152:153], 13, v[146:147]
	v_mov_b64_e32 v[166:167], s[22:23]
	v_lshl_add_u64 v[152:153], s[10:11], 0, v[152:153]
	v_lshl_add_u64 v[152:153], v[152:153], 0, v[144:145]
	v_mfma_f32_16x16x32_fp8_fp8 v[158:161], v[140:141], v[166:167], 0
	v_add_co_u32_e32 v164, vcc, s56, v152
	s_nop 1
	v_addc_co_u32_e32 v165, vcc, 0, v153, vcc
	global_store_dwordx4 v[164:165], v[140:143], off sc1
	s_nop 1
	v_mfma_f32_16x16x32_fp8_fp8 v[140:143], v[142:143], v[166:167], v[158:161]
	s_and_saveexec_b64 s[0:1], s[20:21]
	s_cbranch_execz .LBB2_78
	s_lshl_b32 s4, s64, 2
	s_or_b32 s4, s4, s46
	s_ashr_i32 s5, s4, 31
	s_lshl_b64 s[4:5], s[4:5], 14
	s_add_u32 s4, s2, s4
	s_addc_u32 s5, s3, s5
	v_lshl_add_u64 v[158:159], v[146:147], 2, s[4:5]
	v_lshlrev_b32_e32 v194, 2, v192
	v_lshl_add_u64 v[158:159], v[158:159], 0, v[194:195]
	global_store_dwordx4 v[158:159], v[140:143], off offset:512 sc1
.LBB2_78:
	s_or_b64 exec, exec, s[0:1]
	ds_read2st64_b32 v[158:159], v154 offset0:2 offset1:6
	s_nop 3
	v_cvt_f32_i32_e32 v141, v53
	v_cvt_f32_i32_e32 v140, v52
	v_cvt_f32_i32_e32 v165, v47
	v_cvt_f32_i32_e32 v164, v46
	s_waitcnt lgkmcnt(0)
	v_mov_b32_e32 v154, v159
	v_pk_mul_f32 v[140:141], v[136:137], v[140:141]
	v_cvt_f32_i32_e32 v169, v35
	v_cvt_f32_i32_e32 v168, v34
	v_pk_fma_f32 v[140:141], v[140:141], v[158:159], v[154:155] op_sel_hi:[1,0,0]
	v_cvt_f32_i32_e32 v161, v45
	v_cvt_f32_i32_e32 v160, v44
	v_pk_mul_f32 v[166:167], v[140:141], v[140:141]
	v_pk_mul_f32 v[140:141], v[134:135], v[164:165]
	v_cvt_f32_i32_e32 v143, v55
	v_pk_fma_f32 v[140:141], v[140:141], v[158:159], v[154:155] op_sel_hi:[1,0,0]
	v_cvt_f32_i32_e32 v142, v54
	v_pk_mul_f32 v[170:171], v[140:141], v[140:141]
	v_pk_mul_f32 v[140:141], v[130:131], v[168:169]
	v_pk_mul_f32 v[160:161], v[132:133], v[160:161]
	v_cvt_f32_i32_e32 v165, v33
	v_cvt_f32_i32_e32 v164, v32
	v_pk_fma_f32 v[140:141], v[140:141], v[158:159], v[154:155] op_sel_hi:[1,0,0]
	v_cvt_f32_i32_e32 v169, v25
	v_cvt_f32_i32_e32 v168, v24
	v_pk_fma_f32 v[160:161], v[160:161], v[158:159], v[154:155] op_sel_hi:[1,0,0]
	v_pk_mul_f32 v[174:175], v[140:141], v[140:141]
	v_pk_mul_f32 v[160:161], v[160:161], v[160:161]
	v_cvt_pk_fp8_f32 v140, v166, v167
	v_pk_mul_f32 v[142:143], v[138:139], v[142:143]
	v_cvt_pk_fp8_f32 v141, v160, v161
	v_pk_fma_f32 v[142:143], v[142:143], v[158:159], v[154:155] op_sel_hi:[1,0,0]
	v_pk_mul_f32 v[164:165], v[128:129], v[164:165]
	v_cvt_f32_i32_e32 v173, v27
	v_cvt_f32_i32_e32 v172, v26
	v_pk_mul_f32 v[168:169], v[124:125], v[168:169]
	v_pk_mul_f32 v[142:143], v[142:143], v[142:143]
	v_pk_fma_f32 v[164:165], v[164:165], v[158:159], v[154:155] op_sel_hi:[1,0,0]
	v_pk_fma_f32 v[160:161], v[168:169], v[158:159], v[154:155] op_sel_hi:[1,0,0]
	v_pk_mul_f32 v[164:165], v[164:165], v[164:165]
	v_pk_mul_f32 v[160:161], v[160:161], v[160:161]
	v_cvt_pk_fp8_f32 v140, v142, v143 op_sel:[0,0,1]
	v_cvt_pk_fp8_f32 v141, v170, v171 op_sel:[0,0,1]
	v_cvt_pk_fp8_f32 v142, v164, v165
	v_cvt_pk_fp8_f32 v143, v160, v161
	v_pk_mul_f32 v[172:173], v[126:127], v[172:173]
	v_mov_b64_e32 v[164:165], s[22:23]
	v_pk_fma_f32 v[158:159], v[172:173], v[158:159], v[154:155] op_sel_hi:[1,0,0]
	v_cvt_pk_fp8_f32 v142, v174, v175 op_sel:[0,0,1]
	v_pk_mul_f32 v[158:159], v[158:159], v[158:159]
	v_add_co_u32_e32 v152, vcc, 0x120000, v152
	v_cvt_pk_fp8_f32 v143, v158, v159 op_sel:[0,0,1]
	v_mfma_f32_16x16x32_fp8_fp8 v[158:161], v[140:141], v[164:165], 0
	v_addc_co_u32_e32 v153, vcc, 0, v153, vcc
	global_store_dwordx4 v[152:153], v[140:143], off sc1
	s_nop 1
	v_mfma_f32_16x16x32_fp8_fp8 v[140:143], v[142:143], v[164:165], v[158:161]
	s_and_saveexec_b64 s[0:1], s[20:21]
	s_cbranch_execz .LBB2_80
	s_lshl_b32 s4, s64, 2
	s_or_b32 s4, s4, s46
	s_ashr_i32 s5, s4, 31
	s_lshl_b64 s[4:5], s[4:5], 14
	s_add_u32 s4, s2, s4
	s_addc_u32 s5, s3, s5
	v_lshl_add_u64 v[152:153], v[146:147], 2, s[4:5]
	v_lshlrev_b32_e32 v194, 2, v192
	v_lshl_add_u64 v[152:153], v[152:153], 0, v[194:195]
	global_store_dwordx4 v[152:153], v[140:143], off offset:576 sc1
.LBB2_80:
	s_or_b64 exec, exec, s[0:1]
	s_nop 4
	ds_read2st64_b32 v[140:141], v155 offset0:2 offset1:6
	v_cvt_f32_i32_e32 v143, v37
	v_cvt_f32_i32_e32 v153, v39
	v_cvt_f32_i32_e32 v152, v38
	v_cvt_f32_i32_e32 v142, v36
	v_cvt_f32_i32_e32 v159, v29
	v_cvt_f32_i32_e32 v161, v31
	v_cvt_f32_i32_e32 v160, v30
	v_cvt_f32_i32_e32 v158, v28
	v_cvt_f32_i32_e32 v165, v17
	v_cvt_f32_i32_e32 v167, v19
	v_cvt_f32_i32_e32 v166, v18
	v_cvt_f32_i32_e32 v164, v16
	v_cvt_f32_i32_e32 v169, v9
	v_cvt_f32_i32_e32 v171, v11
	v_cvt_f32_i32_e32 v170, v10
	v_cvt_f32_i32_e32 v168, v8
	v_pk_mul_f32 v[152:153], v[138:139], v[152:153]
	v_pk_mul_f32 v[142:143], v[136:137], v[142:143]
	s_waitcnt lgkmcnt(0)
	v_mov_b32_e32 v154, v141
	v_pk_mul_f32 v[160:161], v[134:135], v[160:161]
	v_pk_mul_f32 v[158:159], v[132:133], v[158:159]
	v_pk_mul_f32 v[166:167], v[130:131], v[166:167]
	v_pk_mul_f32 v[164:165], v[128:129], v[164:165]
	v_pk_mul_f32 v[170:171], v[126:127], v[170:171]
	v_pk_mul_f32 v[168:169], v[124:125], v[168:169]
	v_pk_fma_f32 v[142:143], v[142:143], v[140:141], v[154:155] op_sel_hi:[1,0,0]
	v_pk_fma_f32 v[152:153], v[152:153], v[140:141], v[154:155] op_sel_hi:[1,0,0]
	v_pk_fma_f32 v[158:159], v[158:159], v[140:141], v[154:155] op_sel_hi:[1,0,0]
	v_pk_fma_f32 v[160:161], v[160:161], v[140:141], v[154:155] op_sel_hi:[1,0,0]
	v_pk_fma_f32 v[164:165], v[164:165], v[140:141], v[154:155] op_sel_hi:[1,0,0]
	v_pk_fma_f32 v[166:167], v[166:167], v[140:141], v[154:155] op_sel_hi:[1,0,0]
	v_pk_fma_f32 v[168:169], v[168:169], v[140:141], v[154:155] op_sel_hi:[1,0,0]
	v_pk_fma_f32 v[140:141], v[170:171], v[140:141], v[154:155] op_sel_hi:[1,0,0]
	v_pk_mul_f32 v[142:143], v[142:143], v[142:143]
	v_pk_mul_f32 v[158:159], v[158:159], v[158:159]
	v_pk_mul_f32 v[154:155], v[168:169], v[168:169]
	v_pk_mul_f32 v[168:169], v[140:141], v[140:141]
	v_pk_mul_f32 v[152:153], v[152:153], v[152:153]
	v_cvt_pk_fp8_f32 v140, v142, v143
	v_cvt_pk_fp8_f32 v141, v158, v159
	v_pk_mul_f32 v[160:161], v[160:161], v[160:161]
	v_pk_mul_f32 v[164:165], v[164:165], v[164:165]
	v_cvt_pk_fp8_f32 v140, v152, v153 op_sel:[0,0,1]
	v_cvt_pk_fp8_f32 v142, v164, v165
	v_cvt_pk_fp8_f32 v143, v154, v155
	v_cvt_pk_fp8_f32 v141, v160, v161 op_sel:[0,0,1]
	v_pk_mul_f32 v[166:167], v[166:167], v[166:167]
	v_lshlrev_b64 v[152:153], 13, v[146:147]
	v_cvt_pk_fp8_f32 v142, v166, v167 op_sel:[0,0,1]
	v_cvt_pk_fp8_f32 v143, v168, v169 op_sel:[0,0,1]
	s_mov_b32 s23, s22
	v_lshl_add_u64 v[152:153], s[10:11], 0, v[152:153]
	v_mov_b64_e32 v[160:161], s[22:23]
	v_lshl_add_u64 v[158:159], v[152:153], 0, v[144:145]
	v_add_co_u32_e32 v158, vcc, s57, v158
	v_mfma_f32_16x16x32_fp8_fp8 v[152:155], v[140:141], v[160:161], 0
	s_nop 0
	v_addc_co_u32_e32 v159, vcc, 0, v159, vcc
	global_store_dwordx4 v[158:159], v[140:143], off sc1
	s_nop 1
	v_mfma_f32_16x16x32_fp8_fp8 v[140:143], v[142:143], v[160:161], v[152:155]
	s_and_saveexec_b64 s[0:1], s[20:21]
	s_cbranch_execz .LBB2_82
	s_lshl_b32 s4, s64, 2
	s_or_b32 s4, s4, s46
	s_ashr_i32 s5, s4, 31
	s_lshl_b64 s[4:5], s[4:5], 14
	s_add_u32 s4, s2, s4
	s_addc_u32 s5, s3, s5
	v_lshl_add_u64 v[152:153], v[146:147], 2, s[4:5]
	v_lshlrev_b32_e32 v194, 2, v192
	v_lshl_add_u64 v[152:153], v[152:153], 0, v[194:195]
	global_store_dwordx4 v[152:153], v[140:143], off offset:640 sc1
.LBB2_82:
	s_or_b64 exec, exec, s[0:1]
	v_cvt_f32_i32_e32 v153, v23
	v_cvt_f32_i32_e32 v152, v22
	v_cvt_f32_i32_e32 v155, v15
	v_cvt_f32_i32_e32 v154, v14
	s_nop 0
	ds_read2st64_b32 v[140:141], v156 offset0:2 offset1:6
	v_pk_mul_f32 v[138:139], v[138:139], v[152:153]
	v_cvt_f32_i32_e32 v153, v13
	v_cvt_f32_i32_e32 v152, v12
	v_cvt_f32_i32_e32 v143, v21
	v_cvt_f32_i32_e32 v142, v20
	v_pk_mul_f32 v[134:135], v[134:135], v[154:155]
	v_pk_mul_f32 v[132:133], v[132:133], v[152:153]
	v_cvt_f32_i32_e32 v153, v5
	v_cvt_f32_i32_e32 v152, v4
	v_cvt_f32_i32_e32 v155, v7
	v_cvt_f32_i32_e32 v154, v6
	v_pk_mul_f32 v[136:137], v[136:137], v[142:143]
	v_pk_mul_f32 v[128:129], v[128:129], v[152:153]
	v_cvt_f32_i32_e32 v153, v1
	v_cvt_f32_i32_e32 v152, v0
	s_waitcnt lgkmcnt(0)
	v_mov_b32_e32 v142, v141
	v_pk_fma_f32 v[136:137], v[136:137], v[140:141], v[142:143] op_sel_hi:[1,0,0]
	v_pk_fma_f32 v[132:133], v[132:133], v[140:141], v[142:143] op_sel_hi:[1,0,0]
	v_pk_mul_f32 v[130:131], v[130:131], v[154:155]
	v_cvt_f32_i32_e32 v155, v3
	v_cvt_f32_i32_e32 v154, v2
	v_pk_mul_f32 v[124:125], v[124:125], v[152:153]
	v_pk_mul_f32 v[136:137], v[136:137], v[136:137]
	v_pk_mul_f32 v[132:133], v[132:133], v[132:133]
	v_pk_fma_f32 v[152:153], v[124:125], v[140:141], v[142:143] op_sel_hi:[1,0,0]
	v_pk_fma_f32 v[138:139], v[138:139], v[140:141], v[142:143] op_sel_hi:[1,0,0]
	v_cvt_pk_fp8_f32 v124, v136, v137
	v_cvt_pk_fp8_f32 v125, v132, v133
	v_pk_fma_f32 v[134:135], v[134:135], v[140:141], v[142:143] op_sel_hi:[1,0,0]
	v_pk_fma_f32 v[128:129], v[128:129], v[140:141], v[142:143] op_sel_hi:[1,0,0]
	v_pk_mul_f32 v[126:127], v[126:127], v[154:155]
	v_pk_mul_f32 v[138:139], v[138:139], v[138:139]
	v_pk_mul_f32 v[134:135], v[134:135], v[134:135]
	v_pk_mul_f32 v[128:129], v[128:129], v[128:129]
	v_pk_fma_f32 v[132:133], v[126:127], v[140:141], v[142:143] op_sel_hi:[1,0,0]
	v_pk_mul_f32 v[136:137], v[152:153], v[152:153]
	v_cvt_pk_fp8_f32 v124, v138, v139 op_sel:[0,0,1]
	v_cvt_pk_fp8_f32 v125, v134, v135 op_sel:[0,0,1]
	v_cvt_pk_fp8_f32 v126, v128, v129
	v_cvt_pk_fp8_f32 v127, v136, v137
	v_pk_fma_f32 v[130:131], v[130:131], v[140:141], v[142:143] op_sel_hi:[1,0,0]
	v_pk_mul_f32 v[128:129], v[132:133], v[132:133]
	v_pk_mul_f32 v[130:131], v[130:131], v[130:131]
	v_cvt_pk_fp8_f32 v127, v128, v129 op_sel:[0,0,1]
	v_cvt_pk_fp8_f32 v126, v130, v131 op_sel:[0,0,1]
	v_mov_b64_e32 v[134:135], s[22:23]
	v_add_u32_e32 v160, 0xb0, v146
	v_ashrrev_i32_e32 v161, 31, v160
	v_mfma_f32_16x16x32_fp8_fp8 v[128:131], v[124:125], v[134:135], 0
	v_lshlrev_b64 v[132:133], 13, v[160:161]
	v_lshl_add_u64 v[132:133], s[10:11], 0, v[132:133]
	v_lshl_add_u64 v[132:133], v[132:133], 0, v[144:145]
	v_mfma_f32_16x16x32_fp8_fp8 v[140:143], v[126:127], v[134:135], v[128:131]
	s_mov_b64 s[0:1], s[20:21]
	global_store_dwordx4 v[132:133], v[124:127], off sc1
.LBB2_83:
	s_and_saveexec_b64 s[4:5], s[0:1]
	s_cbranch_execz .LBB2_85
	s_lshl_b32 s0, s64, 2
	s_or_b32 s0, s0, s46
	s_ashr_i32 s1, s0, 31
	s_lshl_b64 s[0:1], s[0:1], 14
	s_add_u32 s0, s2, s0
	s_addc_u32 s1, s3, s1
	s_waitcnt lgkmcnt(0)
	v_lshl_add_u64 v[124:125], v[160:161], 2, s[0:1]
	v_lshlrev_b32_e32 v194, 2, v192
	v_lshl_add_u64 v[124:125], v[124:125], 0, v[194:195]
	global_store_dwordx4 v[124:125], v[140:143], off sc1

.LBB2_86:
	s_andn2_b64 vcc, exec, s[0:1]
	s_cbranch_vccnz .LBB2_25
	s_waitcnt lgkmcnt(2)
	ds_read_b128 v[132:135], v163
	ds_read_b32 v152, v162 offset:2048
	ds_read_b128 v[136:139], v163 offset:1024
	s_waitcnt lgkmcnt(4)
	ds_read_b128 v[128:131], v163 offset:16
	s_waitcnt lgkmcnt(4)
	ds_read_b128 v[124:127], v163 offset:1040
	v_cvt_f32_i32_e32 v121, v121
	v_cvt_f32_i32_e32 v123, v123
	v_cvt_f32_i32_e32 v122, v122
	v_cvt_f32_i32_e32 v120, v120
	s_waitcnt lgkmcnt(3)
	v_pk_mul_f32 v[140:141], v[132:133], v[152:153] op_sel_hi:[1,0]
	v_pk_mul_f32 v[142:143], v[134:135], v[152:153] op_sel_hi:[1,0]
	s_waitcnt lgkmcnt(2)
	v_pk_fma_f32 v[148:149], v[140:141], v[148:149], v[136:137]
	v_pk_fma_f32 v[154:155], v[142:143], v[150:151], v[138:139]
	s_waitcnt lgkmcnt(1)
	v_pk_mul_f32 v[140:141], v[128:129], v[152:153] op_sel_hi:[1,0]
	v_pk_mul_f32 v[142:143], v[130:131], v[152:153] op_sel_hi:[1,0]
	s_waitcnt lgkmcnt(0)
	v_pk_fma_f32 v[158:159], v[140:141], v[120:121], v[124:125]
	v_pk_fma_f32 v[156:157], v[142:143], v[122:123], v[126:127]
	ds_read_b128 v[140:143], v163 offset:32
	ds_read_b128 v[120:123], v163 offset:1056
	v_cvt_f32_i32_e32 v161, v119
	v_cvt_f32_i32_e32 v160, v118
	v_cvt_f32_i32_e32 v165, v113
	v_cvt_f32_i32_e32 v164, v112
	v_cvt_f32_i32_e32 v167, v115
	v_cvt_f32_i32_e32 v166, v114
	ds_read_b128 v[112:115], v163 offset:48
	v_cvt_f32_i32_e32 v151, v117
	v_cvt_f32_i32_e32 v150, v116
	ds_read_b128 v[116:119], v163 offset:1072
	s_waitcnt lgkmcnt(3)
	v_pk_mul_f32 v[168:169], v[142:143], v[152:153] op_sel_hi:[1,0]
	v_pk_mul_f32 v[148:149], v[148:149], v[148:149]
	s_waitcnt lgkmcnt(2)
	v_pk_fma_f32 v[160:161], v[168:169], v[160:161], v[122:123]
	v_pk_mul_f32 v[168:169], v[140:141], v[152:153] op_sel_hi:[1,0]
	v_ashrrev_i32_e32 v147, 31, v146
	v_pk_fma_f32 v[168:169], v[168:169], v[150:151], v[120:121]
	s_waitcnt lgkmcnt(1)
	v_pk_mul_f32 v[150:151], v[114:115], v[152:153] op_sel_hi:[1,0]
	v_cvt_f32_i32_e32 v109, v109
	s_waitcnt lgkmcnt(0)
	v_pk_fma_f32 v[166:167], v[150:151], v[166:167], v[118:119]
	v_pk_mul_f32 v[150:151], v[112:113], v[152:153] op_sel_hi:[1,0]
	v_cvt_f32_i32_e32 v108, v108
	v_pk_fma_f32 v[164:165], v[150:151], v[164:165], v[116:117]
	v_cvt_f32_i32_e32 v111, v111
	v_cvt_pk_fp8_f32 v150, v148, v149
	v_pk_mul_f32 v[148:149], v[158:159], v[158:159]
	v_cvt_f32_i32_e32 v110, v110
	v_cvt_pk_fp8_f32 v151, v148, v149
	v_pk_mul_f32 v[148:149], v[168:169], v[168:169]
	v_cvt_f32_i32_e32 v105, v105
	v_cvt_pk_fp8_f32 v152, v148, v149
	v_pk_mul_f32 v[148:149], v[164:165], v[164:165]
	v_cvt_f32_i32_e32 v104, v104
	v_cvt_pk_fp8_f32 v153, v148, v149
	v_pk_mul_f32 v[148:149], v[154:155], v[154:155]
	v_pk_mul_f32 v[154:155], v[166:167], v[166:167]
	v_cvt_pk_fp8_f32 v150, v148, v149 op_sel:[0,0,1]
	v_pk_mul_f32 v[148:149], v[156:157], v[156:157]
	v_cvt_pk_fp8_f32 v153, v154, v155 op_sel:[0,0,1]
	v_cvt_pk_fp8_f32 v151, v148, v149 op_sel:[0,0,1]
	v_pk_mul_f32 v[148:149], v[160:161], v[160:161]
	v_cvt_f32_i32_e32 v107, v107
	v_cvt_pk_fp8_f32 v152, v148, v149 op_sel:[0,0,1]
	v_lshlrev_b64 v[148:149], 11, v[146:147]
	v_lshl_add_u64 v[148:149], s[8:9], 0, v[148:149]
	v_lshl_add_u64 v[148:149], v[148:149], 0, v[144:145]
	global_store_dwordx4 v[148:149], v[150:153], off sc1
	ds_read_b32 v150, v162 offset:2112
	v_cvt_f32_i32_e32 v106, v106
	v_cvt_f32_i32_e32 v101, v101
	v_cvt_f32_i32_e32 v100, v100
	v_cvt_f32_i32_e32 v93, v93
	s_waitcnt lgkmcnt(0)
	v_pk_mul_f32 v[152:153], v[132:133], v[150:151] op_sel_hi:[1,0]
	v_cvt_f32_i32_e32 v95, v95
	v_cvt_f32_i32_e32 v94, v94
	v_cvt_f32_i32_e32 v92, v92
	v_pk_mul_f32 v[154:155], v[134:135], v[150:151] op_sel_hi:[1,0]
	v_pk_fma_f32 v[108:109], v[152:153], v[108:109], v[136:137]
	v_pk_mul_f32 v[152:153], v[128:129], v[150:151] op_sel_hi:[1,0]
	v_pk_fma_f32 v[110:111], v[154:155], v[110:111], v[138:139]
	v_pk_mul_f32 v[154:155], v[130:131], v[150:151] op_sel_hi:[1,0]
	v_pk_fma_f32 v[104:105], v[152:153], v[104:105], v[124:125]
	v_pk_mul_f32 v[152:153], v[140:141], v[150:151] op_sel_hi:[1,0]
	v_pk_fma_f32 v[106:107], v[154:155], v[106:107], v[126:127]
	v_pk_mul_f32 v[154:155], v[142:143], v[150:151] op_sel_hi:[1,0]
	v_pk_fma_f32 v[100:101], v[152:153], v[100:101], v[120:121]
	v_pk_mul_f32 v[152:153], v[112:113], v[150:151] op_sel_hi:[1,0]
	v_pk_mul_f32 v[150:151], v[114:115], v[150:151] op_sel_hi:[1,0]
	v_cvt_f32_i32_e32 v103, v103
	v_cvt_f32_i32_e32 v102, v102
	v_pk_fma_f32 v[94:95], v[150:151], v[94:95], v[118:119]
	v_pk_fma_f32 v[92:93], v[152:153], v[92:93], v[116:117]
	v_pk_mul_f32 v[108:109], v[108:109], v[108:109]
	v_pk_mul_f32 v[104:105], v[104:105], v[104:105]
	v_pk_mul_f32 v[100:101], v[100:101], v[100:101]
	v_pk_mul_f32 v[150:151], v[94:95], v[94:95]
	v_pk_mul_f32 v[152:153], v[92:93], v[92:93]
	v_pk_fma_f32 v[102:103], v[154:155], v[102:103], v[122:123]
	v_cvt_pk_fp8_f32 v92, v108, v109
	v_cvt_pk_fp8_f32 v93, v104, v105
	v_cvt_pk_fp8_f32 v94, v100, v101
	v_cvt_pk_fp8_f32 v95, v152, v153
	v_pk_mul_f32 v[110:111], v[110:111], v[110:111]
	v_pk_mul_f32 v[106:107], v[106:107], v[106:107]
	v_pk_mul_f32 v[102:103], v[102:103], v[102:103]
	v_or_b32_e32 v100, 16, v146
	v_cvt_pk_fp8_f32 v92, v110, v111 op_sel:[0,0,1]
	v_cvt_pk_fp8_f32 v93, v106, v107 op_sel:[0,0,1]
	v_cvt_pk_fp8_f32 v94, v102, v103 op_sel:[0,0,1]
	v_cvt_pk_fp8_f32 v95, v150, v151 op_sel:[0,0,1]
	v_ashrrev_i32_e32 v101, 31, v100
	v_lshlrev_b64 v[100:101], 11, v[100:101]
	v_lshl_add_u64 v[100:101], s[8:9], 0, v[100:101]
	v_lshl_add_u64 v[100:101], v[100:101], 0, v[144:145]
	global_store_dwordx4 v[100:101], v[92:95], off sc1
	ds_read_b32 v92, v162 offset:2176
	v_cvt_f32_i32_e32 v99, v99
	v_cvt_f32_i32_e32 v98, v98
	v_cvt_f32_i32_e32 v95, v97
	v_cvt_f32_i32_e32 v94, v96
	v_cvt_f32_i32_e32 v89, v89
	v_cvt_f32_i32_e32 v88, v88
	s_waitcnt lgkmcnt(0)
	v_pk_mul_f32 v[100:101], v[134:135], v[92:93] op_sel_hi:[1,0]
	v_cvt_f32_i32_e32 v91, v91
	v_cvt_f32_i32_e32 v90, v90
	v_cvt_f32_i32_e32 v85, v85
	v_cvt_f32_i32_e32 v84, v84
	v_pk_mul_f32 v[96:97], v[132:133], v[92:93] op_sel_hi:[1,0]
	v_pk_fma_f32 v[98:99], v[100:101], v[98:99], v[138:139]
	v_cvt_f32_i32_e32 v77, v77
	v_cvt_f32_i32_e32 v79, v79
	v_cvt_f32_i32_e32 v78, v78
	v_cvt_f32_i32_e32 v76, v76
	v_pk_fma_f32 v[94:95], v[96:97], v[94:95], v[136:137]
	v_pk_mul_f32 v[96:97], v[98:99], v[98:99]
	v_pk_mul_f32 v[98:99], v[128:129], v[92:93] op_sel_hi:[1,0]
	v_pk_mul_f32 v[100:101], v[130:131], v[92:93] op_sel_hi:[1,0]
	v_pk_fma_f32 v[88:89], v[98:99], v[88:89], v[124:125]
	v_pk_mul_f32 v[98:99], v[140:141], v[92:93] op_sel_hi:[1,0]
	v_pk_fma_f32 v[90:91], v[100:101], v[90:91], v[126:127]
	v_pk_mul_f32 v[100:101], v[142:143], v[92:93] op_sel_hi:[1,0]
	v_pk_fma_f32 v[84:85], v[98:99], v[84:85], v[120:121]
	v_pk_mul_f32 v[98:99], v[112:113], v[92:93] op_sel_hi:[1,0]
	v_pk_mul_f32 v[92:93], v[114:115], v[92:93] op_sel_hi:[1,0]
	v_cvt_f32_i32_e32 v87, v87
	v_cvt_f32_i32_e32 v86, v86
	v_pk_fma_f32 v[78:79], v[92:93], v[78:79], v[118:119]
	v_pk_fma_f32 v[76:77], v[98:99], v[76:77], v[116:117]
	v_pk_mul_f32 v[94:95], v[94:95], v[94:95]
	v_pk_mul_f32 v[88:89], v[88:89], v[88:89]
	v_pk_mul_f32 v[84:85], v[84:85], v[84:85]
	v_pk_mul_f32 v[92:93], v[78:79], v[78:79]
	v_pk_mul_f32 v[98:99], v[76:77], v[76:77]
	v_pk_fma_f32 v[86:87], v[100:101], v[86:87], v[122:123]
	v_cvt_pk_fp8_f32 v76, v94, v95
	v_cvt_pk_fp8_f32 v77, v88, v89
	v_cvt_pk_fp8_f32 v78, v84, v85
	v_cvt_pk_fp8_f32 v79, v98, v99
	v_pk_mul_f32 v[90:91], v[90:91], v[90:91]
	v_pk_mul_f32 v[86:87], v[86:87], v[86:87]
	v_or_b32_e32 v84, 32, v146
	v_cvt_pk_fp8_f32 v76, v96, v97 op_sel:[0,0,1]
	v_cvt_pk_fp8_f32 v77, v90, v91 op_sel:[0,0,1]
	v_cvt_pk_fp8_f32 v78, v86, v87 op_sel:[0,0,1]
	v_cvt_pk_fp8_f32 v79, v92, v93 op_sel:[0,0,1]
	v_ashrrev_i32_e32 v85, 31, v84
	v_lshlrev_b64 v[84:85], 11, v[84:85]
	v_lshl_add_u64 v[84:85], s[8:9], 0, v[84:85]
	v_lshl_add_u64 v[84:85], v[84:85], 0, v[144:145]
	global_store_dwordx4 v[84:85], v[76:79], off sc1
	ds_read_b32 v76, v162 offset:2240
	v_cvt_f32_i32_e32 v83, v83
	v_cvt_f32_i32_e32 v82, v82
	v_cvt_f32_i32_e32 v79, v81
	v_cvt_f32_i32_e32 v78, v80
	v_cvt_f32_i32_e32 v73, v73
	v_cvt_f32_i32_e32 v72, v72
	s_waitcnt lgkmcnt(0)
	v_pk_mul_f32 v[84:85], v[134:135], v[76:77] op_sel_hi:[1,0]
	v_cvt_f32_i32_e32 v75, v75
	v_cvt_f32_i32_e32 v74, v74
	v_cvt_f32_i32_e32 v69, v69
	v_cvt_f32_i32_e32 v68, v68
	v_pk_mul_f32 v[80:81], v[132:133], v[76:77] op_sel_hi:[1,0]
	v_pk_fma_f32 v[82:83], v[84:85], v[82:83], v[138:139]
	v_cvt_f32_i32_e32 v65, v65
	v_cvt_f32_i32_e32 v67, v67
	v_cvt_f32_i32_e32 v66, v66
	v_cvt_f32_i32_e32 v64, v64
	v_pk_fma_f32 v[78:79], v[80:81], v[78:79], v[136:137]
	v_pk_mul_f32 v[80:81], v[82:83], v[82:83]
	v_pk_mul_f32 v[82:83], v[128:129], v[76:77] op_sel_hi:[1,0]
	v_pk_mul_f32 v[84:85], v[130:131], v[76:77] op_sel_hi:[1,0]
	v_pk_fma_f32 v[72:73], v[82:83], v[72:73], v[124:125]
	v_pk_mul_f32 v[82:83], v[140:141], v[76:77] op_sel_hi:[1,0]
	v_pk_fma_f32 v[74:75], v[84:85], v[74:75], v[126:127]
	v_pk_mul_f32 v[84:85], v[142:143], v[76:77] op_sel_hi:[1,0]
	v_pk_fma_f32 v[68:69], v[82:83], v[68:69], v[120:121]
	v_pk_mul_f32 v[82:83], v[112:113], v[76:77] op_sel_hi:[1,0]
	v_pk_mul_f32 v[76:77], v[114:115], v[76:77] op_sel_hi:[1,0]
	v_cvt_f32_i32_e32 v71, v71
	v_cvt_f32_i32_e32 v70, v70
	v_pk_fma_f32 v[66:67], v[76:77], v[66:67], v[118:119]
	v_pk_fma_f32 v[64:65], v[82:83], v[64:65], v[116:117]
	v_pk_mul_f32 v[78:79], v[78:79], v[78:79]
	v_pk_mul_f32 v[72:73], v[72:73], v[72:73]
	v_pk_mul_f32 v[68:69], v[68:69], v[68:69]
	v_pk_mul_f32 v[76:77], v[66:67], v[66:67]
	v_pk_mul_f32 v[82:83], v[64:65], v[64:65]
	v_pk_fma_f32 v[70:71], v[84:85], v[70:71], v[122:123]
	v_cvt_pk_fp8_f32 v64, v78, v79
	v_cvt_pk_fp8_f32 v65, v72, v73
	v_cvt_pk_fp8_f32 v66, v68, v69
	v_cvt_pk_fp8_f32 v67, v82, v83
	v_pk_mul_f32 v[74:75], v[74:75], v[74:75]
	v_pk_mul_f32 v[70:71], v[70:71], v[70:71]
	v_or_b32_e32 v68, 48, v146
	v_cvt_pk_fp8_f32 v64, v80, v81 op_sel:[0,0,1]
	v_cvt_pk_fp8_f32 v65, v74, v75 op_sel:[0,0,1]
	v_cvt_pk_fp8_f32 v66, v70, v71 op_sel:[0,0,1]
	v_cvt_pk_fp8_f32 v67, v76, v77 op_sel:[0,0,1]
	v_ashrrev_i32_e32 v69, 31, v68
	v_lshlrev_b64 v[68:69], 11, v[68:69]
	v_lshl_add_u64 v[68:69], s[8:9], 0, v[68:69]
	v_lshl_add_u64 v[68:69], v[68:69], 0, v[144:145]
	global_store_dwordx4 v[68:69], v[64:67], off sc1
	ds_read_b32 v64, v162 offset:2560
	v_cvt_f32_i32_e32 v61, v61
	v_cvt_f32_i32_e32 v60, v60
	v_cvt_f32_i32_e32 v63, v63
	v_cvt_f32_i32_e32 v62, v62
	v_cvt_f32_i32_e32 v57, v57
	v_cvt_f32_i32_e32 v56, v56
	v_cvt_f32_i32_e32 v59, v59
	v_cvt_f32_i32_e32 v58, v58
	v_cvt_f32_i32_e32 v49, v49
	v_cvt_f32_i32_e32 v48, v48
	s_waitcnt lgkmcnt(0)
	v_pk_mul_f32 v[66:67], v[132:133], v[64:65] op_sel_hi:[1,0]
	v_cvt_f32_i32_e32 v41, v41
	v_cvt_f32_i32_e32 v43, v43
	v_cvt_f32_i32_e32 v42, v42
	v_cvt_f32_i32_e32 v40, v40
	v_pk_mul_f32 v[68:69], v[134:135], v[64:65] op_sel_hi:[1,0]
	v_pk_fma_f32 v[60:61], v[66:67], v[60:61], v[136:137]
	v_pk_mul_f32 v[66:67], v[128:129], v[64:65] op_sel_hi:[1,0]
	v_pk_fma_f32 v[62:63], v[68:69], v[62:63], v[138:139]
	v_pk_mul_f32 v[68:69], v[130:131], v[64:65] op_sel_hi:[1,0]
	v_pk_fma_f32 v[56:57], v[66:67], v[56:57], v[124:125]
	v_pk_mul_f32 v[66:67], v[140:141], v[64:65] op_sel_hi:[1,0]
	v_pk_fma_f32 v[58:59], v[68:69], v[58:59], v[126:127]
	v_pk_mul_f32 v[68:69], v[142:143], v[64:65] op_sel_hi:[1,0]
	v_pk_fma_f32 v[48:49], v[66:67], v[48:49], v[120:121]
	v_pk_mul_f32 v[66:67], v[112:113], v[64:65] op_sel_hi:[1,0]
	v_pk_mul_f32 v[64:65], v[114:115], v[64:65] op_sel_hi:[1,0]
	v_cvt_f32_i32_e32 v51, v51
	v_cvt_f32_i32_e32 v50, v50
	v_pk_fma_f32 v[42:43], v[64:65], v[42:43], v[118:119]
	v_pk_fma_f32 v[40:41], v[66:67], v[40:41], v[116:117]
	v_pk_mul_f32 v[60:61], v[60:61], v[60:61]
	v_pk_mul_f32 v[56:57], v[56:57], v[56:57]
	v_pk_mul_f32 v[48:49], v[48:49], v[48:49]
	v_pk_mul_f32 v[64:65], v[42:43], v[42:43]
	v_pk_mul_f32 v[66:67], v[40:41], v[40:41]
	v_pk_fma_f32 v[50:51], v[68:69], v[50:51], v[122:123]
	v_cvt_pk_fp8_f32 v40, v60, v61
	v_cvt_pk_fp8_f32 v41, v56, v57
	v_cvt_pk_fp8_f32 v42, v48, v49
	v_cvt_pk_fp8_f32 v43, v66, v67
	v_pk_mul_f32 v[62:63], v[62:63], v[62:63]
	v_pk_mul_f32 v[58:59], v[58:59], v[58:59]
	v_pk_mul_f32 v[50:51], v[50:51], v[50:51]
	v_cvt_pk_fp8_f32 v40, v62, v63 op_sel:[0,0,1]
	v_cvt_pk_fp8_f32 v41, v58, v59 op_sel:[0,0,1]
	v_cvt_pk_fp8_f32 v42, v50, v51 op_sel:[0,0,1]
	v_cvt_pk_fp8_f32 v43, v64, v65 op_sel:[0,0,1]
	v_add_co_u32_e32 v48, vcc, s58, v148
	v_cvt_f32_i32_e32 v45, v45
	s_nop 0
	v_addc_co_u32_e32 v49, vcc, 0, v149, vcc
	global_store_dwordx4 v[48:49], v[40:43], off sc1
	ds_read_b32 v40, v162 offset:2624
	v_cvt_f32_i32_e32 v49, v55
	v_cvt_f32_i32_e32 v43, v53
	v_cvt_f32_i32_e32 v42, v52
	v_cvt_f32_i32_e32 v48, v54
	v_cvt_f32_i32_e32 v44, v44
	v_cvt_f32_i32_e32 v47, v47
	v_cvt_f32_i32_e32 v46, v46
	v_cvt_f32_i32_e32 v33, v33
	v_cvt_f32_i32_e32 v32, v32
	s_waitcnt lgkmcnt(0)
	v_pk_mul_f32 v[50:51], v[132:133], v[40:41] op_sel_hi:[1,0]
	v_cvt_f32_i32_e32 v25, v25
	v_cvt_f32_i32_e32 v27, v27
	v_cvt_f32_i32_e32 v26, v26
	v_cvt_f32_i32_e32 v24, v24
	v_pk_mul_f32 v[52:53], v[134:135], v[40:41] op_sel_hi:[1,0]
	v_pk_fma_f32 v[42:43], v[50:51], v[42:43], v[136:137]
	v_pk_mul_f32 v[50:51], v[128:129], v[40:41] op_sel_hi:[1,0]
	v_pk_fma_f32 v[48:49], v[52:53], v[48:49], v[138:139]
	v_pk_mul_f32 v[52:53], v[130:131], v[40:41] op_sel_hi:[1,0]
	v_pk_fma_f32 v[44:45], v[50:51], v[44:45], v[124:125]
	v_pk_mul_f32 v[50:51], v[140:141], v[40:41] op_sel_hi:[1,0]
	v_pk_fma_f32 v[46:47], v[52:53], v[46:47], v[126:127]
	v_pk_mul_f32 v[52:53], v[142:143], v[40:41] op_sel_hi:[1,0]
	v_pk_fma_f32 v[32:33], v[50:51], v[32:33], v[120:121]
	v_pk_mul_f32 v[50:51], v[112:113], v[40:41] op_sel_hi:[1,0]
	v_pk_mul_f32 v[40:41], v[114:115], v[40:41] op_sel_hi:[1,0]
	v_cvt_f32_i32_e32 v35, v35
	v_cvt_f32_i32_e32 v34, v34
	v_pk_fma_f32 v[26:27], v[40:41], v[26:27], v[118:119]
	v_pk_fma_f32 v[24:25], v[50:51], v[24:25], v[116:117]
	v_pk_mul_f32 v[42:43], v[42:43], v[42:43]
	v_pk_mul_f32 v[44:45], v[44:45], v[44:45]
	v_pk_mul_f32 v[32:33], v[32:33], v[32:33]
	v_pk_mul_f32 v[40:41], v[26:27], v[26:27]
	v_pk_mul_f32 v[50:51], v[24:25], v[24:25]
	v_pk_fma_f32 v[34:35], v[52:53], v[34:35], v[122:123]
	v_cvt_pk_fp8_f32 v24, v42, v43
	v_cvt_pk_fp8_f32 v25, v44, v45
	v_cvt_pk_fp8_f32 v26, v32, v33
	v_cvt_pk_fp8_f32 v27, v50, v51
	v_pk_mul_f32 v[48:49], v[48:49], v[48:49]
	v_pk_mul_f32 v[46:47], v[46:47], v[46:47]
	v_pk_mul_f32 v[34:35], v[34:35], v[34:35]
	v_cvt_pk_fp8_f32 v24, v48, v49 op_sel:[0,0,1]
	v_cvt_pk_fp8_f32 v25, v46, v47 op_sel:[0,0,1]
	v_cvt_pk_fp8_f32 v26, v34, v35 op_sel:[0,0,1]
	v_cvt_pk_fp8_f32 v27, v40, v41 op_sel:[0,0,1]
	v_add_co_u32_e32 v32, vcc, s59, v148
	v_cvt_f32_i32_e32 v29, v29
	s_nop 0
	v_addc_co_u32_e32 v33, vcc, 0, v149, vcc
	global_store_dwordx4 v[32:33], v[24:27], off sc1
	ds_read_b32 v24, v162 offset:2688
	v_cvt_f32_i32_e32 v33, v39
	v_cvt_f32_i32_e32 v27, v37
	v_cvt_f32_i32_e32 v26, v36
	v_cvt_f32_i32_e32 v32, v38
	v_cvt_f32_i32_e32 v28, v28
	v_cvt_f32_i32_e32 v31, v31
	v_cvt_f32_i32_e32 v30, v30
	v_cvt_f32_i32_e32 v17, v17
	v_cvt_f32_i32_e32 v16, v16
	s_waitcnt lgkmcnt(0)
	v_pk_mul_f32 v[34:35], v[132:133], v[24:25] op_sel_hi:[1,0]
	v_cvt_f32_i32_e32 v9, v9
	v_cvt_f32_i32_e32 v11, v11
	v_cvt_f32_i32_e32 v10, v10
	v_cvt_f32_i32_e32 v8, v8
	v_pk_mul_f32 v[36:37], v[134:135], v[24:25] op_sel_hi:[1,0]
	v_pk_fma_f32 v[26:27], v[34:35], v[26:27], v[136:137]
	v_pk_mul_f32 v[34:35], v[128:129], v[24:25] op_sel_hi:[1,0]
	v_pk_fma_f32 v[32:33], v[36:37], v[32:33], v[138:139]
	v_pk_mul_f32 v[36:37], v[130:131], v[24:25] op_sel_hi:[1,0]
	v_pk_fma_f32 v[28:29], v[34:35], v[28:29], v[124:125]
	v_pk_mul_f32 v[34:35], v[140:141], v[24:25] op_sel_hi:[1,0]
	v_pk_fma_f32 v[30:31], v[36:37], v[30:31], v[126:127]
	v_pk_mul_f32 v[36:37], v[142:143], v[24:25] op_sel_hi:[1,0]
	v_pk_fma_f32 v[16:17], v[34:35], v[16:17], v[120:121]
	v_pk_mul_f32 v[34:35], v[112:113], v[24:25] op_sel_hi:[1,0]
	v_pk_mul_f32 v[24:25], v[114:115], v[24:25] op_sel_hi:[1,0]
	v_cvt_f32_i32_e32 v19, v19
	v_cvt_f32_i32_e32 v18, v18
	v_pk_fma_f32 v[10:11], v[24:25], v[10:11], v[118:119]
	v_pk_fma_f32 v[8:9], v[34:35], v[8:9], v[116:117]
	v_pk_mul_f32 v[26:27], v[26:27], v[26:27]
	v_pk_mul_f32 v[28:29], v[28:29], v[28:29]
	v_pk_mul_f32 v[16:17], v[16:17], v[16:17]
	v_pk_mul_f32 v[24:25], v[10:11], v[10:11]
	v_pk_mul_f32 v[34:35], v[8:9], v[8:9]
	v_pk_fma_f32 v[18:19], v[36:37], v[18:19], v[122:123]
	v_cvt_pk_fp8_f32 v8, v26, v27
	v_cvt_pk_fp8_f32 v9, v28, v29
	v_cvt_pk_fp8_f32 v10, v16, v17
	v_cvt_pk_fp8_f32 v11, v34, v35
	v_pk_mul_f32 v[32:33], v[32:33], v[32:33]
	v_pk_mul_f32 v[30:31], v[30:31], v[30:31]
	v_pk_mul_f32 v[18:19], v[18:19], v[18:19]
	v_cvt_pk_fp8_f32 v8, v32, v33 op_sel:[0,0,1]
	v_cvt_pk_fp8_f32 v9, v30, v31 op_sel:[0,0,1]
	v_cvt_pk_fp8_f32 v10, v18, v19 op_sel:[0,0,1]
	v_cvt_pk_fp8_f32 v11, v24, v25 op_sel:[0,0,1]
	v_add_co_u32_e32 v16, vcc, s60, v148
	v_cvt_f32_i32_e32 v13, v13
	s_nop 0
	v_addc_co_u32_e32 v17, vcc, 0, v149, vcc
	global_store_dwordx4 v[16:17], v[8:11], off sc1
	ds_read_b32 v8, v162 offset:2752
	v_cvt_f32_i32_e32 v17, v23
	v_cvt_f32_i32_e32 v11, v21
	v_cvt_f32_i32_e32 v10, v20
	v_cvt_f32_i32_e32 v16, v22
	v_cvt_f32_i32_e32 v12, v12
	v_cvt_f32_i32_e32 v15, v15
	v_cvt_f32_i32_e32 v14, v14
	v_cvt_f32_i32_e32 v5, v5
	v_cvt_f32_i32_e32 v4, v4
	s_waitcnt lgkmcnt(0)
	v_pk_mul_f32 v[18:19], v[132:133], v[8:9] op_sel_hi:[1,0]
	v_cvt_f32_i32_e32 v1, v1
	v_cvt_f32_i32_e32 v3, v3
	v_cvt_f32_i32_e32 v2, v2
	v_cvt_f32_i32_e32 v0, v0
	v_pk_mul_f32 v[20:21], v[134:135], v[8:9] op_sel_hi:[1,0]
	v_pk_fma_f32 v[10:11], v[18:19], v[10:11], v[136:137]
	v_pk_mul_f32 v[18:19], v[128:129], v[8:9] op_sel_hi:[1,0]
	v_pk_fma_f32 v[16:17], v[20:21], v[16:17], v[138:139]
	v_pk_mul_f32 v[20:21], v[130:131], v[8:9] op_sel_hi:[1,0]
	v_pk_fma_f32 v[12:13], v[18:19], v[12:13], v[124:125]
	v_pk_mul_f32 v[18:19], v[140:141], v[8:9] op_sel_hi:[1,0]
	v_pk_fma_f32 v[14:15], v[20:21], v[14:15], v[126:127]
	v_pk_mul_f32 v[20:21], v[142:143], v[8:9] op_sel_hi:[1,0]
	v_pk_fma_f32 v[4:5], v[18:19], v[4:5], v[120:121]
	v_pk_mul_f32 v[18:19], v[112:113], v[8:9] op_sel_hi:[1,0]
	v_pk_mul_f32 v[8:9], v[114:115], v[8:9] op_sel_hi:[1,0]
	v_cvt_f32_i32_e32 v7, v7
	v_cvt_f32_i32_e32 v6, v6
	v_pk_fma_f32 v[2:3], v[8:9], v[2:3], v[118:119]
	v_pk_fma_f32 v[0:1], v[18:19], v[0:1], v[116:117]
	v_pk_mul_f32 v[10:11], v[10:11], v[10:11]
	v_pk_mul_f32 v[12:13], v[12:13], v[12:13]
	v_pk_mul_f32 v[4:5], v[4:5], v[4:5]
	v_pk_mul_f32 v[8:9], v[2:3], v[2:3]
	v_pk_mul_f32 v[18:19], v[0:1], v[0:1]
	v_pk_fma_f32 v[6:7], v[20:21], v[6:7], v[122:123]
	v_cvt_pk_fp8_f32 v0, v10, v11
	v_cvt_pk_fp8_f32 v1, v12, v13
	v_cvt_pk_fp8_f32 v2, v4, v5
	v_cvt_pk_fp8_f32 v3, v18, v19
	v_pk_mul_f32 v[16:17], v[16:17], v[16:17]
	v_pk_mul_f32 v[14:15], v[14:15], v[14:15]
	v_pk_mul_f32 v[6:7], v[6:7], v[6:7]
	v_cvt_pk_fp8_f32 v0, v16, v17 op_sel:[0,0,1]
	v_cvt_pk_fp8_f32 v1, v14, v15 op_sel:[0,0,1]
	v_cvt_pk_fp8_f32 v2, v6, v7 op_sel:[0,0,1]
	v_cvt_pk_fp8_f32 v3, v8, v9 op_sel:[0,0,1]
	v_add_co_u32_e32 v4, vcc, 0x58000, v148
	s_nop 1
	v_addc_co_u32_e32 v5, vcc, 0, v149, vcc
	global_store_dwordx4 v[4:5], v[0:3], off sc1
	s_branch .LBB2_25

	.amdhsa_kernel _ZN2rb6k_gemmILi2ENS_7SchedP1ENS_5EpiP1EEEvT0_T1_
		.amdhsa_group_segment_fixed_size 0
		.amdhsa_private_segment_fixed_size 0
		.amdhsa_kernarg_size 88
		.amdhsa_user_sgpr_count 2
		.amdhsa_user_sgpr_dispatch_ptr 0
		.amdhsa_user_sgpr_queue_ptr 0
		.amdhsa_user_sgpr_kernarg_segment_ptr 1
		.amdhsa_user_sgpr_dispatch_id 0
		.amdhsa_user_sgpr_kernarg_preload_length 0
		.amdhsa_user_sgpr_kernarg_preload_offset 0
		.amdhsa_user_sgpr_private_segment_size 0
		.amdhsa_uses_dynamic_stack 0
		.amdhsa_enable_private_segment 0
		.amdhsa_system_sgpr_workgroup_id_x 1
		.amdhsa_system_sgpr_workgroup_id_y 0
		.amdhsa_system_sgpr_workgroup_id_z 0
		.amdhsa_system_sgpr_workgroup_info 0
		.amdhsa_system_vgpr_workitem_id 0
		.amdhsa_next_free_vgpr 212
		.amdhsa_next_free_sgpr 80
		.amdhsa_accum_offset 212
		.amdhsa_reserve_vcc 1
		.amdhsa_float_round_mode_32 0
		.amdhsa_float_round_mode_16_64 0
		.amdhsa_float_denorm_mode_32 3
		.amdhsa_float_denorm_mode_16_64 3
		.amdhsa_dx10_clamp 1
		.amdhsa_ieee_mode 1
		.amdhsa_fp16_overflow 0
		.amdhsa_tg_split 0
		.amdhsa_exception_fp_ieee_invalid_op 0
		.amdhsa_exception_fp_denorm_src 0
		.amdhsa_exception_fp_ieee_div_zero 0
		.amdhsa_exception_fp_ieee_overflow 0
		.amdhsa_exception_fp_ieee_underflow 0
		.amdhsa_exception_fp_ieee_inexact 0
		.amdhsa_exception_int_div_zero 0
	.end_amdhsa_kernel

_ZN2rb6k_gemmILi1ENS_7SchedP2ENS_7EpiSlabEEEvT0_T1_:
	v_lshrrev_b32_e32 v1, 5, v0
	v_lshlrev_b32_e32 v2, 4, v0
	s_movk_i32 s4, 0x70
	v_and_b32_e32 v1, 4, v1
	v_lshrrev_b32_e32 v5, 3, v0
	v_xor_b32_e32 v3, v2, v0
	v_bitop3_b32 v4, v2, s4, v0 bitop3:0x48
	v_and_or_b32 v7, v5, 3, v1
	v_lshrrev_b32_e32 v1, 1, v0
	v_or_b32_e32 v2, 0x2000, v2
	v_and_b32_e32 v8, 48, v1
	v_lshl_or_b32 v1, v5, 13, v4
	v_lshrrev_b32_e32 v5, 6, v2
	v_lshlrev_b32_e32 v2, 6, v2
	s_mov_b32 s4, 0xfe070
	v_bitop3_b32 v195, v2, s4, v3 bitop3:0xc8
	s_lshl_b32 s4, s2, 2
	s_load_dwordx4 s[20:23], s[0:1], 0x0
	s_load_dwordx2 s[60:61], s[0:1], 0x18
	s_and_b32 s4, s4, 4
	s_bfe_u32 s26, s2, 0x20003
	s_or_b32 s29, s4, s26
	s_lshl_b32 s4, s2, 3
	v_readfirstlane_b32 s3, v0
	s_and_b32 s24, s4, 0xffffff00
	s_lshr_b32 s39, s3, 6
	s_bfe_u32 s30, s2, 0x20001
	s_ashr_i32 s25, s24, 31
	s_lshr_b32 s28, s3, 8
	s_lshl_b32 s6, s39, 10
	s_lshl_b32 s7, s29, 21
	s_lshl_b32 s27, s30, 11
	s_lshl_b64 s[4:5], s[24:25], 13
	s_waitcnt lgkmcnt(0)
	s_cmpk_gt_u32 s3, 0xff
	s_cbranch_scc1 .Lp2_rs_skip
	v_lshlrev_b32_e32 v209, 2, v0
	s_cmpk_gt_u32 s2, 0x7f
	s_cbranch_scc1 .Lp2_rs_x
	s_and_b32 s64, s2, 7
	s_lshl_b32 s64, s64, 18
	s_lshr_b32 s65, s2, 3
	s_lshl_b32 s65, s65, 10
	s_add_u32 s62, s60, 0xd00c000
	s_addc_u32 s63, s61, 0
	s_add_u32 s62, s62, s65
	s_addc_u32 s63, s63, 0
	s_add_i32 s64, s64, s65
	s_add_u32 s60, s60, 0xd800000
	s_addc_u32 s61, s61, 0
	s_add_u32 s60, s60, s64
	s_addc_u32 s61, s61, 0
	global_load_dword v100, v209, s[60:61] nt
	s_add_u32 s60, s60, 0x4000
	s_addc_u32 s61, s61, 0
	global_load_dword v101, v209, s[60:61] nt
	s_add_u32 s60, s60, 0x4000
	s_addc_u32 s61, s61, 0
	global_load_dword v102, v209, s[60:61] nt
	s_add_u32 s60, s60, 0x4000
	s_addc_u32 s61, s61, 0
	global_load_dword v103, v209, s[60:61] nt
	s_add_u32 s60, s60, 0x4000
	s_addc_u32 s61, s61, 0
	global_load_dword v104, v209, s[60:61] nt
	s_add_u32 s60, s60, 0x4000
	s_addc_u32 s61, s61, 0
	global_load_dword v105, v209, s[60:61] nt
	s_add_u32 s60, s60, 0x4000
	s_addc_u32 s61, s61, 0
	global_load_dword v106, v209, s[60:61] nt
	s_add_u32 s60, s60, 0x4000
	s_addc_u32 s61, s61, 0
	global_load_dword v107, v209, s[60:61] nt
	s_add_u32 s60, s60, 0x4000
	s_addc_u32 s61, s61, 0
	global_load_dword v108, v209, s[60:61] nt
	s_add_u32 s60, s60, 0x4000
	s_addc_u32 s61, s61, 0
	global_load_dword v109, v209, s[60:61] nt
	s_add_u32 s60, s60, 0x4000
	s_addc_u32 s61, s61, 0
	global_load_dword v110, v209, s[60:61] nt
	s_add_u32 s60, s60, 0x4000
	s_addc_u32 s61, s61, 0
	global_load_dword v111, v209, s[60:61] nt
	s_add_u32 s60, s60, 0x4000
	s_addc_u32 s61, s61, 0
	global_load_dword v112, v209, s[60:61] nt
	s_add_u32 s60, s60, 0x4000
	s_addc_u32 s61, s61, 0
	global_load_dword v113, v209, s[60:61] nt
	s_add_u32 s60, s60, 0x4000
	s_addc_u32 s61, s61, 0
	global_load_dword v114, v209, s[60:61] nt
	s_add_u32 s60, s60, 0x4000
	s_addc_u32 s61, s61, 0
	global_load_dword v115, v209, s[60:61] nt
	s_mov_b32 s66, 0
	s_branch .Lp2_rs_skip
.Lp2_rs_x:
	s_add_i32 s64, s2, 0xffffff80
	s_and_b32 s65, s64, 15
	s_lshl_b32 s65, s65, 18
	s_lshr_b32 s64, s64, 4
	s_lshl_b32 s64, s64, 10
	s_add_u32 s62, s60, 0xd01a000
	s_addc_u32 s63, s61, 0
	s_add_u32 s62, s62, s64
	s_addc_u32 s63, s63, 0
	s_add_i32 s64, s64, s65
	s_add_u32 s60, s60, 0xd400000
	s_addc_u32 s61, s61, 0
	s_add_u32 s60, s60, s64
	s_addc_u32 s61, s61, 0
	global_load_dword v100, v209, s[60:61] nt
	s_add_u32 s60, s60, 0x2000
	s_addc_u32 s61, s61, 0
	global_load_dword v101, v209, s[60:61] nt
	s_add_u32 s60, s60, 0x2000
	s_addc_u32 s61, s61, 0
	global_load_dword v102, v209, s[60:61] nt
	s_add_u32 s60, s60, 0x2000
	s_addc_u32 s61, s61, 0
	global_load_dword v103, v209, s[60:61] nt
	s_add_u32 s60, s60, 0x2000
	s_addc_u32 s61, s61, 0
	global_load_dword v104, v209, s[60:61] nt
	s_add_u32 s60, s60, 0x2000
	s_addc_u32 s61, s61, 0
	global_load_dword v105, v209, s[60:61] nt
	s_add_u32 s60, s60, 0x2000
	s_addc_u32 s61, s61, 0
	global_load_dword v106, v209, s[60:61] nt
	s_add_u32 s60, s60, 0x2000
	s_addc_u32 s61, s61, 0
	global_load_dword v107, v209, s[60:61] nt
	s_add_u32 s60, s60, 0x2000
	s_addc_u32 s61, s61, 0
	global_load_dword v108, v209, s[60:61] nt
	s_add_u32 s60, s60, 0x2000
	s_addc_u32 s61, s61, 0
	global_load_dword v109, v209, s[60:61] nt
	s_add_u32 s60, s60, 0x2000
	s_addc_u32 s61, s61, 0
	global_load_dword v110, v209, s[60:61] nt
	s_add_u32 s60, s60, 0x2000
	s_addc_u32 s61, s61, 0
	global_load_dword v111, v209, s[60:61] nt
	s_add_u32 s60, s60, 0x2000
	s_addc_u32 s61, s61, 0
	global_load_dword v112, v209, s[60:61] nt
	s_add_u32 s60, s60, 0x2000
	s_addc_u32 s61, s61, 0
	global_load_dword v113, v209, s[60:61] nt
	s_add_u32 s60, s60, 0x2000
	s_addc_u32 s61, s61, 0
	global_load_dword v114, v209, s[60:61] nt
	s_add_u32 s60, s60, 0x2000
	s_addc_u32 s61, s61, 0
	global_load_dword v115, v209, s[60:61] nt
	s_add_u32 s60, s60, 0x2000
	s_addc_u32 s61, s61, 0
	global_load_dword v116, v209, s[60:61] nt
	s_add_u32 s60, s60, 0x2000
	s_addc_u32 s61, s61, 0
	global_load_dword v117, v209, s[60:61] nt
	s_add_u32 s60, s60, 0x2000
	s_addc_u32 s61, s61, 0
	global_load_dword v118, v209, s[60:61] nt
	s_add_u32 s60, s60, 0x2000
	s_addc_u32 s61, s61, 0
	global_load_dword v119, v209, s[60:61] nt
	s_add_u32 s60, s60, 0x2000
	s_addc_u32 s61, s61, 0
	global_load_dword v120, v209, s[60:61] nt
	s_add_u32 s60, s60, 0x2000
	s_addc_u32 s61, s61, 0
	global_load_dword v121, v209, s[60:61] nt
	s_add_u32 s60, s60, 0x2000
	s_addc_u32 s61, s61, 0
	global_load_dword v122, v209, s[60:61] nt
	s_add_u32 s60, s60, 0x2000
	s_addc_u32 s61, s61, 0
	global_load_dword v123, v209, s[60:61] nt
	s_add_u32 s60, s60, 0x2000
	s_addc_u32 s61, s61, 0
	global_load_dword v124, v209, s[60:61] nt
	s_add_u32 s60, s60, 0x2000
	s_addc_u32 s61, s61, 0
	global_load_dword v125, v209, s[60:61] nt
	s_add_u32 s60, s60, 0x2000
	s_addc_u32 s61, s61, 0
	global_load_dword v126, v209, s[60:61] nt
	s_add_u32 s60, s60, 0x2000
	s_addc_u32 s61, s61, 0
	global_load_dword v127, v209, s[60:61] nt
	s_add_u32 s60, s60, 0x2000
	s_addc_u32 s61, s61, 0
	global_load_dword v128, v209, s[60:61] nt
	s_add_u32 s60, s60, 0x2000
	s_addc_u32 s61, s61, 0
	global_load_dword v129, v209, s[60:61] nt
	s_add_u32 s60, s60, 0x2000
	s_addc_u32 s61, s61, 0
	global_load_dword v130, v209, s[60:61] nt
	s_add_u32 s60, s60, 0x2000
	s_addc_u32 s61, s61, 0
	global_load_dword v131, v209, s[60:61] nt
	s_mov_b32 s66, 1
.Lp2_rs_skip:
	s_add_u32 s4, s22, s4
	s_addc_u32 s5, s23, s5
	s_add_u32 s8, s4, s27
	v_lshrrev_b32_e32 v6, 2, v0
	s_addc_u32 s25, s5, 0
	s_add_i32 s31, s6, 0
	v_and_b32_e32 v6, 64, v6
	s_and_b32 s9, s25, 0xffff
	s_add_i32 s33, s31, 0x10000
	s_add_i32 s34, s31, 0x12000
	v_or3_b32 v6, v8, v6, v7
	v_and_b32_e32 v5, 0xc0, v5
	s_mov_b32 s15, 0x20000
	s_mov_b32 s14, -1
	s_add_u32 s4, s20, s7
	v_lshl_or_b32 v194, v6, 13, v4
	v_or3_b32 v5, v8, v5, v7
	s_mov_b32 s10, s14
	s_mov_b32 s11, s15
	s_mov_b32 m0, s33
	s_addc_u32 s5, s21, 0
	v_lshl_or_b32 v196, v5, 13, v4
	buffer_load_dwordx4 v194, s[8:11], 0 offen lds
	s_mov_b32 m0, s34
	s_add_u32 s16, s4, s27
	buffer_load_dwordx4 v196, s[8:11], 0 offen lds
	s_addc_u32 s9, s5, 0
	s_and_b32 s17, s9, 0xffff
	s_mov_b32 s18, s14
	s_mov_b32 s19, s15
	s_mov_b32 m0, s31
	s_add_i32 s35, s31, 0x2000
	buffer_load_dwordx4 v1, s[16:19], 0 offen lds
	s_mov_b32 m0, s35
	s_add_u32 s12, s8, 0x10000
	buffer_load_dwordx4 v195, s[16:19], 0 offen lds
	s_addc_u32 s4, s25, 0
	s_add_i32 s17, s31, 0x14000
	s_and_b32 s13, s4, 0xffff
	s_mov_b32 m0, s17
	s_add_i32 s36, s31, 0x16000
	buffer_load_dwordx4 v194, s[12:15], 0 offen lds
	s_mov_b32 m0, s36
	s_nop 0
	buffer_load_dwordx4 v196, s[12:15], 0 offen lds
	s_add_u32 s12, s16, 0x100000
	s_addc_u32 s4, s9, 0
	s_add_i32 s37, s31, 0x4000
	s_and_b32 s13, s4, 0xffff
	s_mov_b32 m0, s37
	s_add_i32 s38, s31, 0x6000
	buffer_load_dwordx4 v1, s[12:15], 0 offen lds
	s_mov_b32 m0, s38
	s_cmp_lg_u32 s28, 1
	buffer_load_dwordx4 v195, s[12:15], 0 offen lds
	s_cbranch_scc1 .LBB3_2
	s_barrier
.LBB3_2:
	s_and_b32 s39, s39, 3
	s_add_u32 s12, s8, 0x80
	s_load_dwordx4 s[4:7], s[0:1], 0x18
	s_addc_u32 s0, s25, 0
	s_add_i32 s40, s31, 0x18000
	s_and_b32 s13, s0, 0xffff
	s_mov_b32 m0, s40
	s_add_i32 s41, s31, 0x1a000
	s_waitcnt vmcnt(4)
	s_cmpk_gt_u32 s3, 0xff
	s_cbranch_scc1 .Lp2_sum_skip
	v_add_f32_e32 v100, v100, v104
	v_add_f32_e32 v101, v101, v105
	v_add_f32_e32 v102, v102, v106
	v_add_f32_e32 v103, v103, v107
	v_add_f32_e32 v100, v100, v108
	v_add_f32_e32 v101, v101, v109
	v_add_f32_e32 v102, v102, v110
	v_add_f32_e32 v103, v103, v111
	v_add_f32_e32 v100, v100, v112
	v_add_f32_e32 v101, v101, v113
	v_add_f32_e32 v102, v102, v114
	v_add_f32_e32 v103, v103, v115
	s_cmp_eq_u32 s66, 0
	s_cbranch_scc1 .Lp2_sum_fin
	v_add_f32_e32 v100, v100, v116
	v_add_f32_e32 v101, v101, v117
	v_add_f32_e32 v102, v102, v118
	v_add_f32_e32 v103, v103, v119
	v_add_f32_e32 v100, v100, v120
	v_add_f32_e32 v101, v101, v121
	v_add_f32_e32 v102, v102, v122
	v_add_f32_e32 v103, v103, v123
	v_add_f32_e32 v100, v100, v124
	v_add_f32_e32 v101, v101, v125
	v_add_f32_e32 v102, v102, v126
	v_add_f32_e32 v103, v103, v127
	v_add_f32_e32 v100, v100, v128
	v_add_f32_e32 v101, v101, v129
	v_add_f32_e32 v102, v102, v130
	v_add_f32_e32 v103, v103, v131
.Lp2_sum_fin:
	v_add_f32_e32 v100, v100, v101
	v_add_f32_e32 v102, v102, v103
	v_add_f32_e32 v208, v100, v102
.Lp2_sum_skip:
	s_barrier
	buffer_load_dwordx4 v194, s[12:15], 0 offen lds
	s_mov_b32 m0, s41
	v_lshrrev_b32_e32 v2, 4, v0
	buffer_load_dwordx4 v196, s[12:15], 0 offen lds
	s_add_u32 s12, s16, 0x80
	s_addc_u32 s0, s9, 0
	s_add_i32 s42, s31, 0x8000
	s_and_b32 s13, s0, 0xffff
	s_mov_b32 m0, s42
	s_add_i32 s43, s31, 0xa000
	buffer_load_dwordx4 v1, s[12:15], 0 offen lds
	s_mov_b32 m0, s43
	v_and_b32_e32 v197, 15, v0
	buffer_load_dwordx4 v195, s[12:15], 0 offen lds
	s_add_u32 s12, s8, 0x10080
	s_addc_u32 s0, s25, 0
	s_add_i32 s44, s31, 0x1c000
	s_and_b32 s13, s0, 0xffff
	s_mov_b32 m0, s44
	s_add_i32 s45, s31, 0x1e000
	buffer_load_dwordx4 v194, s[12:15], 0 offen lds
	s_mov_b32 m0, s45
	s_and_b32 s0, s2, 1
	buffer_load_dwordx4 v196, s[12:15], 0 offen lds
	s_lshl_b32 s0, s0, 23
	s_lshl_b32 s1, s26, 21
	v_bfe_u32 v3, v0, 1, 3
	s_or_b32 s0, s0, s1
	v_bitop3_b32 v2, v2, v3, 3 bitop3:0x6c
	v_lshlrev_b32_e32 v3, 7, v197
	s_add_i32 s46, s31, 0xc000
	s_add_i32 s47, s31, 0xe000
	s_or_b32 s0, s27, s0
	v_lshlrev_b32_e32 v2, 4, v2
	v_lshl_or_b32 v4, s28, 13, v3
	v_lshl_or_b32 v3, s39, 12, v3
	s_waitcnt vmcnt(6)
	s_add_u32 s48, s20, s0
	v_or_b32_e32 v5, v4, v2
	v_bitop3_b32 v4, v4, 64, v2 bitop3:0x36
	v_or_b32_e32 v198, v3, v2
	v_bitop3_b32 v199, v3, 64, v2 bitop3:0x36
	s_addc_u32 s49, s21, 0
	v_mov_b32_e32 v66, 0
	s_add_i32 s0, 0, 0x10000
	s_add_i32 s1, 0, 0x14000
	s_mov_b32 s50, -2
	s_mov_b64 s[10:11], 0
	v_add_u32_e32 v200, 0, v5
	v_add_u32_e32 v201, 0, v4
	v_mov_b32_e32 v67, v66
	v_mov_b32_e32 v68, v66
	v_mov_b32_e32 v69, v66
	v_mov_b32_e32 v70, v66
	v_mov_b32_e32 v71, v66
	v_mov_b32_e32 v72, v66
	v_mov_b32_e32 v73, v66
	v_mov_b32_e32 v82, v66
	v_mov_b32_e32 v83, v66
	v_mov_b32_e32 v84, v66
	v_mov_b32_e32 v85, v66
	v_mov_b32_e32 v86, v66
	v_mov_b32_e32 v87, v66
	v_mov_b32_e32 v88, v66
	v_mov_b32_e32 v89, v66
	v_mov_b32_e32 v98, v66
	v_mov_b32_e32 v99, v66
	v_mov_b32_e32 v100, v66
	v_mov_b32_e32 v101, v66
	v_mov_b32_e32 v102, v66
	v_mov_b32_e32 v103, v66
	v_mov_b32_e32 v104, v66
	v_mov_b32_e32 v105, v66
	v_mov_b32_e32 v114, v66
	v_mov_b32_e32 v115, v66
	v_mov_b32_e32 v116, v66
	v_mov_b32_e32 v117, v66
	v_mov_b32_e32 v118, v66
	v_mov_b32_e32 v119, v66
	v_mov_b32_e32 v120, v66
	v_mov_b32_e32 v121, v66
	v_mov_b32_e32 v74, v66
	v_mov_b32_e32 v75, v66
	v_mov_b32_e32 v76, v66
	v_mov_b32_e32 v77, v66
	v_mov_b32_e32 v78, v66
	v_mov_b32_e32 v79, v66
	v_mov_b32_e32 v80, v66
	v_mov_b32_e32 v81, v66
	v_mov_b32_e32 v90, v66
	v_mov_b32_e32 v91, v66
	v_mov_b32_e32 v92, v66
	v_mov_b32_e32 v93, v66
	v_mov_b32_e32 v94, v66
	v_mov_b32_e32 v95, v66
	v_mov_b32_e32 v96, v66
	v_mov_b32_e32 v97, v66
	v_mov_b32_e32 v106, v66
	v_mov_b32_e32 v107, v66
	v_mov_b32_e32 v108, v66
	v_mov_b32_e32 v109, v66
	v_mov_b32_e32 v110, v66
	v_mov_b32_e32 v111, v66
	v_mov_b32_e32 v112, v66
	v_mov_b32_e32 v113, v66
	v_mov_b32_e32 v122, v66
	v_mov_b32_e32 v123, v66
	v_mov_b32_e32 v124, v66
	v_mov_b32_e32 v125, v66
	v_mov_b32_e32 v126, v66
	v_mov_b32_e32 v127, v66
	v_mov_b32_e32 v128, v66
	v_mov_b32_e32 v129, v66
	v_mov_b32_e32 v130, v66
	v_mov_b32_e32 v131, v66
	v_mov_b32_e32 v132, v66
	v_mov_b32_e32 v133, v66
	v_mov_b32_e32 v134, v66
	v_mov_b32_e32 v135, v66
	v_mov_b32_e32 v136, v66
	v_mov_b32_e32 v137, v66
	v_mov_b32_e32 v146, v66
	v_mov_b32_e32 v147, v66
	v_mov_b32_e32 v148, v66
	v_mov_b32_e32 v149, v66
	v_mov_b32_e32 v150, v66
	v_mov_b32_e32 v151, v66
	v_mov_b32_e32 v152, v66
	v_mov_b32_e32 v153, v66
	v_mov_b32_e32 v162, v66
	v_mov_b32_e32 v163, v66
	v_mov_b32_e32 v164, v66
	v_mov_b32_e32 v165, v66
	v_mov_b32_e32 v166, v66
	v_mov_b32_e32 v167, v66
	v_mov_b32_e32 v168, v66
	v_mov_b32_e32 v169, v66
	v_mov_b32_e32 v178, v66
	v_mov_b32_e32 v179, v66
	v_mov_b32_e32 v180, v66
	v_mov_b32_e32 v181, v66
	v_mov_b32_e32 v182, v66
	v_mov_b32_e32 v183, v66
	v_mov_b32_e32 v184, v66
	v_mov_b32_e32 v185, v66
	v_mov_b32_e32 v138, v66
	v_mov_b32_e32 v139, v66
	v_mov_b32_e32 v140, v66
	v_mov_b32_e32 v141, v66
	v_mov_b32_e32 v142, v66
	v_mov_b32_e32 v143, v66
	v_mov_b32_e32 v144, v66
	v_mov_b32_e32 v145, v66
	v_mov_b32_e32 v154, v66
	v_mov_b32_e32 v155, v66
	v_mov_b32_e32 v156, v66
	v_mov_b32_e32 v157, v66
	v_mov_b32_e32 v158, v66
	v_mov_b32_e32 v159, v66
	v_mov_b32_e32 v160, v66
	v_mov_b32_e32 v161, v66
	v_mov_b32_e32 v170, v66
	v_mov_b32_e32 v171, v66
	v_mov_b32_e32 v172, v66
	v_mov_b32_e32 v173, v66
	v_mov_b32_e32 v174, v66
	v_mov_b32_e32 v175, v66
	v_mov_b32_e32 v176, v66
	v_mov_b32_e32 v177, v66
	v_mov_b32_e32 v186, v66
	v_mov_b32_e32 v187, v66
	v_mov_b32_e32 v188, v66
	v_mov_b32_e32 v189, v66
	v_mov_b32_e32 v190, v66
	v_mov_b32_e32 v191, v66
	v_mov_b32_e32 v192, v66
	v_mov_b32_e32 v193, v66
	v_bfe_u32 v202, v0, 4, 2
	v_add_u32_e32 v203, s0, v198
	v_add_u32_e32 v204, s0, v199
	v_add_u32_e32 v205, s1, v198
	v_add_u32_e32 v206, s1, v199
	s_barrier
	s_branch .LBB3_4
.LBB3_3:
	s_waitcnt vmcnt(6)
	s_barrier
	s_setprio 1
	v_mfma_f32_16x16x128_f8f6f4 v[118:121], v[26:33], v[58:65], v[118:121]
	s_add_i32 s50, s50, 2
	s_add_u32 s10, s10, 0x100
	s_addc_u32 s11, s11, 0
	s_cmp_gt_u32 s50, 13
	v_mfma_f32_16x16x128_f8f6f4 v[114:117], v[18:25], v[58:65], v[114:117]
	v_mfma_f32_16x16x128_f8f6f4 v[102:105], v[26:33], v[50:57], v[102:105]
	v_mfma_f32_16x16x128_f8f6f4 v[98:101], v[18:25], v[50:57], v[98:101]
	v_mfma_f32_16x16x128_f8f6f4 v[86:89], v[26:33], v[42:49], v[86:89]
	v_mfma_f32_16x16x128_f8f6f4 v[82:85], v[18:25], v[42:49], v[82:85]
	v_mfma_f32_16x16x128_f8f6f4 v[70:73], v[26:33], v[34:41], v[70:73]
	v_mfma_f32_16x16x128_f8f6f4 v[66:69], v[18:25], v[34:41], v[66:69]
	s_setprio 0
	s_barrier
	s_cbranch_scc1 .LBB3_20
.LBB3_4:
	s_cmpk_eq_i32 s10, 0x700
	s_cselect_b64 s[18:19], -1, 0
	s_cmpk_lg_i32 s10, 0x700
	ds_read_b128 v[2:5], v203
	ds_read_b128 v[10:13], v203 offset:2048
	ds_read_b128 v[6:9], v204
	ds_read_b128 v[14:17], v204 offset:2048
	s_cselect_b64 s[26:27], -1, 0
	s_add_u32 s54, s48, s10
	s_addc_u32 s55, s49, s11
	s_add_u32 s51, s8, s10
	s_addc_u32 s52, s25, s11
	s_add_u32 s20, s51, 0x100
	s_addc_u32 s53, s52, 0
	s_add_u32 s12, s54, 0x100080
	s_addc_u32 s0, s55, 0
	s_and_b32 s13, s0, 0xffff
	s_mov_b32 m0, s46
	ds_read_b128 v[58:61], v200
	ds_read_b128 v[50:53], v200 offset:2048
	ds_read_b128 v[62:65], v201
	ds_read_b128 v[54:57], v201 offset:2048
	ds_read_b128 v[42:45], v200 offset:4096
	ds_read_b128 v[34:37], v200 offset:6144
	ds_read_b128 v[46:49], v201 offset:4096
	ds_read_b128 v[38:41], v201 offset:6144
	buffer_load_dwordx4 v1, s[12:15], 0 offen lds
	s_mov_b32 m0, s47
	s_nop 0
	buffer_load_dwordx4 v195, s[12:15], 0 offen lds
	s_waitcnt lgkmcnt(8)
	s_barrier
	s_waitcnt lgkmcnt(0)
	s_setprio 1
	v_mfma_f32_16x16x128_f8f6f4 v[190:193], v[2:9], v[58:65], v[190:193]
	v_mfma_f32_16x16x128_f8f6f4 v[186:189], v[10:17], v[58:65], v[186:189]
	v_mfma_f32_16x16x128_f8f6f4 v[174:177], v[2:9], v[50:57], v[174:177]
	v_mfma_f32_16x16x128_f8f6f4 v[170:173], v[10:17], v[50:57], v[170:173]
	v_mfma_f32_16x16x128_f8f6f4 v[158:161], v[2:9], v[42:49], v[158:161]
	v_mfma_f32_16x16x128_f8f6f4 v[154:157], v[10:17], v[42:49], v[154:157]
	v_mfma_f32_16x16x128_f8f6f4 v[142:145], v[2:9], v[34:41], v[142:145]
	v_mfma_f32_16x16x128_f8f6f4 v[138:141], v[10:17], v[34:41], v[138:141]
	s_setprio 0
	s_barrier
	ds_read_b128 v[26:29], v205
	ds_read_b128 v[18:21], v205 offset:2048
	ds_read_b128 v[30:33], v206
	ds_read_b128 v[22:25], v206 offset:2048
	s_and_b64 vcc, exec, s[18:19]
	s_cbranch_vccnz .LBB3_6
	s_and_b32 s21, s53, 0xffff
	s_mov_b32 s22, s14
	s_mov_b32 s23, s15
	s_mov_b32 m0, s33
	s_nop 0
	buffer_load_dwordx4 v194, s[20:23], 0 offen lds
	s_mov_b32 m0, s34
	s_nop 0
	buffer_load_dwordx4 v196, s[20:23], 0 offen lds
.LBB3_6:
	s_barrier
	s_waitcnt lgkmcnt(0)
	s_setprio 1
	v_mfma_f32_16x16x128_f8f6f4 v[182:185], v[26:33], v[58:65], v[182:185]
	s_add_u32 s12, s54, 0x100
	s_addc_u32 s21, s55, 0
	v_mfma_f32_16x16x128_f8f6f4 v[178:181], v[18:25], v[58:65], v[178:181]
	v_mfma_f32_16x16x128_f8f6f4 v[166:169], v[26:33], v[50:57], v[166:169]
	v_mfma_f32_16x16x128_f8f6f4 v[162:165], v[18:25], v[50:57], v[162:165]
	v_mfma_f32_16x16x128_f8f6f4 v[150:153], v[26:33], v[42:49], v[150:153]
	v_mfma_f32_16x16x128_f8f6f4 v[146:149], v[18:25], v[42:49], v[146:149]
	v_mfma_f32_16x16x128_f8f6f4 v[134:137], v[26:33], v[34:41], v[134:137]
	v_mfma_f32_16x16x128_f8f6f4 v[130:133], v[18:25], v[34:41], v[130:133]
	s_setprio 0
	s_barrier
	ds_read_b128 v[58:61], v200 offset:16384
	ds_read_b128 v[50:53], v200 offset:18432
	ds_read_b128 v[62:65], v201 offset:16384
	ds_read_b128 v[54:57], v201 offset:18432
	ds_read_b128 v[42:45], v200 offset:20480
	ds_read_b128 v[34:37], v200 offset:22528
	ds_read_b128 v[46:49], v201 offset:20480
	ds_read_b128 v[38:41], v201 offset:22528
	v_cndmask_b32_e64 v207, 0, 1, s[26:27]
	v_cmp_ne_u32_e64 s[0:1], 1, v207
	s_andn2_b64 vcc, exec, s[26:27]
	s_cbranch_vccnz .LBB3_8
	s_and_b32 s13, s21, 0xffff
	s_mov_b32 m0, s31
	s_nop 0
	buffer_load_dwordx4 v1, s[12:15], 0 offen lds
	s_mov_b32 m0, s35
	s_nop 0
	buffer_load_dwordx4 v195, s[12:15], 0 offen lds
.LBB3_8:
	s_barrier
	s_waitcnt lgkmcnt(0)
	s_setprio 1
	v_mfma_f32_16x16x128_f8f6f4 v[126:129], v[2:9], v[58:65], v[126:129]
	v_mfma_f32_16x16x128_f8f6f4 v[122:125], v[10:17], v[58:65], v[122:125]
	v_mfma_f32_16x16x128_f8f6f4 v[110:113], v[2:9], v[50:57], v[110:113]
	v_mfma_f32_16x16x128_f8f6f4 v[106:109], v[10:17], v[50:57], v[106:109]
	v_mfma_f32_16x16x128_f8f6f4 v[94:97], v[2:9], v[42:49], v[94:97]
	v_mfma_f32_16x16x128_f8f6f4 v[90:93], v[10:17], v[42:49], v[90:93]
	v_mfma_f32_16x16x128_f8f6f4 v[78:81], v[2:9], v[34:41], v[78:81]
	v_mfma_f32_16x16x128_f8f6f4 v[74:77], v[10:17], v[34:41], v[74:77]
	s_setprio 0
	s_barrier
	s_and_b64 vcc, exec, s[0:1]
	s_mov_b64 s[22:23], -1
	s_cbranch_vccnz .LBB3_10
	s_add_u32 s56, s51, 0x10100
	s_addc_u32 s13, s52, 0
	s_mov_b32 m0, s17
	s_and_b32 s57, s13, 0xffff
	s_mov_b32 s58, s14
	s_mov_b32 s59, s15
	buffer_load_dwordx4 v194, s[56:59], 0 offen lds
	s_mov_b32 m0, s36
	s_mov_b64 s[22:23], 0
	buffer_load_dwordx4 v196, s[56:59], 0 offen lds
	s_waitcnt vmcnt(6)

.LBB3_12:
	s_barrier
	s_setprio 1
	v_mfma_f32_16x16x128_f8f6f4 v[118:121], v[26:33], v[58:65], v[118:121]
	s_add_i32 s13, 0, 0x18000
	v_add_u32_e32 v2, s13, v198
	v_add_u32_e32 v6, s13, v199
	v_mfma_f32_16x16x128_f8f6f4 v[114:117], v[18:25], v[58:65], v[114:117]
	v_mfma_f32_16x16x128_f8f6f4 v[102:105], v[26:33], v[50:57], v[102:105]
	v_mfma_f32_16x16x128_f8f6f4 v[98:101], v[18:25], v[50:57], v[98:101]
	v_mfma_f32_16x16x128_f8f6f4 v[86:89], v[26:33], v[42:49], v[86:89]
	v_mfma_f32_16x16x128_f8f6f4 v[82:85], v[18:25], v[42:49], v[82:85]
	v_mfma_f32_16x16x128_f8f6f4 v[70:73], v[26:33], v[34:41], v[70:73]
	v_mfma_f32_16x16x128_f8f6f4 v[66:69], v[18:25], v[34:41], v[66:69]
	s_setprio 0
	s_barrier
	ds_read_b128 v[10:13], v2
	ds_read_b128 v[2:5], v2 offset:2048
	ds_read_b128 v[14:17], v6
	ds_read_b128 v[6:9], v6 offset:2048
	ds_read_b128 v[58:61], v200 offset:32768
	ds_read_b128 v[50:53], v200 offset:34816
	ds_read_b128 v[62:65], v201 offset:32768
	ds_read_b128 v[54:57], v201 offset:34816
	ds_read_b128 v[42:45], v200 offset:36864
	ds_read_b128 v[34:37], v200 offset:38912
	ds_read_b128 v[46:49], v201 offset:36864
	ds_read_b128 v[38:41], v201 offset:38912
	s_and_b64 vcc, exec, s[0:1]
	s_cbranch_vccnz .LBB3_14
	s_add_u32 s56, s54, 0x100100
	s_addc_u32 s13, s55, 0
	s_and_b32 s57, s13, 0xffff
	s_mov_b32 s58, s14
	s_mov_b32 s59, s15
	s_mov_b32 m0, s37
	s_nop 0
	buffer_load_dwordx4 v1, s[56:59], 0 offen lds
	s_mov_b32 m0, s38
	s_nop 0
	buffer_load_dwordx4 v195, s[56:59], 0 offen lds
.LBB3_14:
	s_waitcnt lgkmcnt(8)
	s_barrier
	s_waitcnt lgkmcnt(0)
	s_setprio 1
	v_mfma_f32_16x16x128_f8f6f4 v[190:193], v[10:17], v[58:65], v[190:193]
	v_mfma_f32_16x16x128_f8f6f4 v[186:189], v[2:9], v[58:65], v[186:189]
	v_mfma_f32_16x16x128_f8f6f4 v[174:177], v[10:17], v[50:57], v[174:177]
	v_mfma_f32_16x16x128_f8f6f4 v[170:173], v[2:9], v[50:57], v[170:173]
	v_mfma_f32_16x16x128_f8f6f4 v[158:161], v[10:17], v[42:49], v[158:161]
	v_mfma_f32_16x16x128_f8f6f4 v[154:157], v[2:9], v[42:49], v[154:157]
	v_mfma_f32_16x16x128_f8f6f4 v[142:145], v[10:17], v[34:41], v[142:145]
	v_mfma_f32_16x16x128_f8f6f4 v[138:141], v[2:9], v[34:41], v[138:141]
	s_setprio 0
	s_barrier
	s_add_i32 s13, 0, 0x1c000
	v_add_u32_e32 v18, s13, v198
	v_add_u32_e32 v22, s13, v199
	ds_read_b128 v[26:29], v18
	ds_read_b128 v[18:21], v18 offset:2048
	ds_read_b128 v[30:33], v22
	ds_read_b128 v[22:25], v22 offset:2048
	s_and_b64 vcc, exec, s[0:1]
	s_cbranch_vccnz .LBB3_16
	s_and_b64 s[22:23], exec, s[18:19]
	s_cselect_b32 s20, s8, s20
	s_cselect_b32 s13, s25, s53
	s_add_u32 s56, s20, 0x80
	s_addc_u32 s13, s13, 0
	s_and_b32 s57, s13, 0xffff
	s_mov_b32 s58, s14
	s_mov_b32 s59, s15
	s_mov_b32 m0, s40
	s_nop 0
	buffer_load_dwordx4 v194, s[56:59], 0 offen lds
	s_mov_b32 m0, s41
	s_nop 0
	buffer_load_dwordx4 v196, s[56:59], 0 offen lds
.LBB3_16:
	s_barrier
	s_waitcnt lgkmcnt(0)
	s_setprio 1
	v_mfma_f32_16x16x128_f8f6f4 v[182:185], v[26:33], v[58:65], v[182:185]
	v_mfma_f32_16x16x128_f8f6f4 v[178:181], v[18:25], v[58:65], v[178:181]
	v_mfma_f32_16x16x128_f8f6f4 v[166:169], v[26:33], v[50:57], v[166:169]
	v_mfma_f32_16x16x128_f8f6f4 v[162:165], v[18:25], v[50:57], v[162:165]
	v_mfma_f32_16x16x128_f8f6f4 v[150:153], v[26:33], v[42:49], v[150:153]
	v_mfma_f32_16x16x128_f8f6f4 v[146:149], v[18:25], v[42:49], v[146:149]
	v_mfma_f32_16x16x128_f8f6f4 v[134:137], v[26:33], v[34:41], v[134:137]
	v_mfma_f32_16x16x128_f8f6f4 v[130:133], v[18:25], v[34:41], v[130:133]
	s_setprio 0
	s_barrier
	ds_read_b128 v[58:61], v200 offset:49152
	ds_read_b128 v[50:53], v200 offset:51200
	ds_read_b128 v[62:65], v201 offset:49152
	ds_read_b128 v[54:57], v201 offset:51200
	ds_read_b128 v[42:45], v200 offset:53248
	ds_read_b128 v[34:37], v200 offset:55296
	ds_read_b128 v[46:49], v201 offset:53248
	ds_read_b128 v[38:41], v201 offset:55296
	s_and_b64 vcc, exec, s[0:1]
	s_cbranch_vccnz .LBB3_18
	s_and_b64 s[18:19], exec, s[18:19]
	s_cselect_b32 s12, s16, s12
	s_cselect_b32 s13, s9, s21
	s_add_u32 s12, s12, 0x80
	s_addc_u32 s13, s13, 0
	s_and_b32 s13, s13, 0xffff
	s_mov_b32 m0, s42
	s_nop 0
	buffer_load_dwordx4 v1, s[12:15], 0 offen lds
	s_mov_b32 m0, s43
	s_nop 0
	buffer_load_dwordx4 v195, s[12:15], 0 offen lds
.LBB3_18:
	s_barrier
	s_waitcnt lgkmcnt(0)
	s_setprio 1
	v_mfma_f32_16x16x128_f8f6f4 v[126:129], v[10:17], v[58:65], v[126:129]
	v_mfma_f32_16x16x128_f8f6f4 v[122:125], v[2:9], v[58:65], v[122:125]
	v_mfma_f32_16x16x128_f8f6f4 v[110:113], v[10:17], v[50:57], v[110:113]
	v_mfma_f32_16x16x128_f8f6f4 v[106:109], v[2:9], v[50:57], v[106:109]
	v_mfma_f32_16x16x128_f8f6f4 v[94:97], v[10:17], v[42:49], v[94:97]
	v_mfma_f32_16x16x128_f8f6f4 v[90:93], v[2:9], v[42:49], v[90:93]
	v_mfma_f32_16x16x128_f8f6f4 v[78:81], v[10:17], v[34:41], v[78:81]
	v_mfma_f32_16x16x128_f8f6f4 v[74:77], v[2:9], v[34:41], v[74:77]
	s_setprio 0
	s_barrier
	s_and_b64 vcc, exec, s[0:1]
	s_cbranch_vccnz .LBB3_3
	s_add_u32 s12, s51, 0x10180
	s_addc_u32 s0, s52, 0
	s_and_b32 s13, s0, 0xffff
	s_mov_b32 m0, s44
	s_nop 0
	buffer_load_dwordx4 v194, s[12:15], 0 offen lds
	s_mov_b32 m0, s45
	s_nop 0
	buffer_load_dwordx4 v196, s[12:15], 0 offen lds
	s_branch .LBB3_3
.LBB3_20:
	s_cmpk_gt_u32 s3, 0xff
	s_cbranch_scc1 .Lp2_at_skip
	global_atomic_add_f32 v209, v208, s[62:63]
.Lp2_at_skip:
	s_lshl_b32 s1, s30, 22
	s_mov_b32 s0, 0x3d800000
	s_nop 15
	s_nop 15
	v_pk_mul_f32 v[8:9], v[190:191], s[0:1] op_sel_hi:[1,0]
	v_pk_mul_f32 v[16:17], v[186:187], s[0:1] op_sel_hi:[1,0]
	v_pk_mul_f32 v[20:21], v[182:183], s[0:1] op_sel_hi:[1,0]
	v_pk_mul_f32 v[24:25], v[178:179], s[0:1] op_sel_hi:[1,0]
	v_cvt_pk_fp8_f32 v6, v8, v9
	v_lshlrev_b32_e32 v1, 4, v202
	v_cvt_pk_fp8_f32 v7, v16, v17
	v_cvt_pk_fp8_f32 v8, v20, v21
	v_cvt_pk_fp8_f32 v9, v24, v25
	v_lshl_or_b32 v1, s39, 6, v1
	v_or_b32_e32 v2, s24, v1
	v_lshl_or_b32 v1, s29, 8, v197
	v_pk_mul_f32 v[12:13], v[192:193], s[0:1] op_sel_hi:[1,0]
	v_pk_mul_f32 v[14:15], v[188:189], s[0:1] op_sel_hi:[1,0]
	v_pk_mul_f32 v[18:19], v[184:185], s[0:1] op_sel_hi:[1,0]
	v_pk_mul_f32 v[22:23], v[180:181], s[0:1] op_sel_hi:[1,0]
	v_lshl_add_u32 v4, s28, 6, v1
	v_mov_b32_e32 v5, 0
	v_cvt_pk_fp8_f32 v6, v12, v13 op_sel:[0,0,1]
	v_cvt_pk_fp8_f32 v7, v14, v15 op_sel:[0,0,1]
	v_cvt_pk_fp8_f32 v8, v18, v19 op_sel:[0,0,1]
	v_cvt_pk_fp8_f32 v9, v22, v23 op_sel:[0,0,1]
	s_add_u32 s6, s6, s1
	v_lshlrev_b64 v[10:11], 11, v[4:5]
	s_addc_u32 s7, s7, 0
	v_ashrrev_i32_e32 v3, 31, v2
	v_lshl_add_u64 v[10:11], s[6:7], 0, v[10:11]
	v_lshl_add_u64 v[10:11], v[10:11], 0, v[2:3]
	global_store_dwordx4 v[10:11], v[6:9], off sc1
	v_pk_mul_f32 v[16:17], v[170:171], s[0:1] op_sel_hi:[1,0]
	v_pk_mul_f32 v[20:21], v[166:167], s[0:1] op_sel_hi:[1,0]
	v_pk_mul_f32 v[8:9], v[174:175], s[0:1] op_sel_hi:[1,0]
	v_pk_mul_f32 v[24:25], v[162:163], s[0:1] op_sel_hi:[1,0]
	v_cvt_pk_fp8_f32 v6, v8, v9
	v_pk_mul_f32 v[12:13], v[176:177], s[0:1] op_sel_hi:[1,0]
	v_cvt_pk_fp8_f32 v7, v16, v17
	v_cvt_pk_fp8_f32 v8, v20, v21
	v_cvt_pk_fp8_f32 v9, v24, v25
	v_pk_mul_f32 v[14:15], v[172:173], s[0:1] op_sel_hi:[1,0]
	v_pk_mul_f32 v[18:19], v[168:169], s[0:1] op_sel_hi:[1,0]
	v_pk_mul_f32 v[22:23], v[164:165], s[0:1] op_sel_hi:[1,0]
	v_or_b32_e32 v10, 16, v4
	v_mov_b32_e32 v11, v5
	v_cvt_pk_fp8_f32 v6, v12, v13 op_sel:[0,0,1]
	v_cvt_pk_fp8_f32 v7, v14, v15 op_sel:[0,0,1]
	v_cvt_pk_fp8_f32 v8, v18, v19 op_sel:[0,0,1]
	v_cvt_pk_fp8_f32 v9, v22, v23 op_sel:[0,0,1]
	v_lshlrev_b64 v[10:11], 11, v[10:11]
	v_lshl_add_u64 v[10:11], s[6:7], 0, v[10:11]
	v_lshl_add_u64 v[10:11], v[10:11], 0, v[2:3]
	global_store_dwordx4 v[10:11], v[6:9], off sc1
	v_pk_mul_f32 v[16:17], v[154:155], s[0:1] op_sel_hi:[1,0]
	v_pk_mul_f32 v[20:21], v[150:151], s[0:1] op_sel_hi:[1,0]
	v_pk_mul_f32 v[8:9], v[158:159], s[0:1] op_sel_hi:[1,0]
	v_pk_mul_f32 v[24:25], v[146:147], s[0:1] op_sel_hi:[1,0]
	v_cvt_pk_fp8_f32 v6, v8, v9
	v_pk_mul_f32 v[12:13], v[160:161], s[0:1] op_sel_hi:[1,0]
	v_cvt_pk_fp8_f32 v7, v16, v17
	v_cvt_pk_fp8_f32 v8, v20, v21
	v_cvt_pk_fp8_f32 v9, v24, v25
	v_pk_mul_f32 v[14:15], v[156:157], s[0:1] op_sel_hi:[1,0]
	v_pk_mul_f32 v[18:19], v[152:153], s[0:1] op_sel_hi:[1,0]
	v_pk_mul_f32 v[22:23], v[148:149], s[0:1] op_sel_hi:[1,0]
	v_or_b32_e32 v10, 32, v4
	v_mov_b32_e32 v11, v5
	v_cvt_pk_fp8_f32 v6, v12, v13 op_sel:[0,0,1]
	v_cvt_pk_fp8_f32 v7, v14, v15 op_sel:[0,0,1]
	v_cvt_pk_fp8_f32 v8, v18, v19 op_sel:[0,0,1]
	v_cvt_pk_fp8_f32 v9, v22, v23 op_sel:[0,0,1]
	v_lshlrev_b64 v[10:11], 11, v[10:11]
	v_lshl_add_u64 v[10:11], s[6:7], 0, v[10:11]
	v_lshl_add_u64 v[10:11], v[10:11], 0, v[2:3]
	global_store_dwordx4 v[10:11], v[6:9], off sc1
	v_pk_mul_f32 v[16:17], v[138:139], s[0:1] op_sel_hi:[1,0]
	v_pk_mul_f32 v[20:21], v[134:135], s[0:1] op_sel_hi:[1,0]
	v_pk_mul_f32 v[8:9], v[142:143], s[0:1] op_sel_hi:[1,0]
	v_pk_mul_f32 v[24:25], v[130:131], s[0:1] op_sel_hi:[1,0]
	v_cvt_pk_fp8_f32 v6, v8, v9
	v_pk_mul_f32 v[12:13], v[144:145], s[0:1] op_sel_hi:[1,0]
	v_cvt_pk_fp8_f32 v7, v16, v17
	v_cvt_pk_fp8_f32 v8, v20, v21
	v_cvt_pk_fp8_f32 v9, v24, v25
	v_pk_mul_f32 v[14:15], v[140:141], s[0:1] op_sel_hi:[1,0]
	v_pk_mul_f32 v[18:19], v[136:137], s[0:1] op_sel_hi:[1,0]
	v_pk_mul_f32 v[22:23], v[132:133], s[0:1] op_sel_hi:[1,0]
	v_or_b32_e32 v10, 48, v4
	v_mov_b32_e32 v11, v5
	v_cvt_pk_fp8_f32 v6, v12, v13 op_sel:[0,0,1]
	v_cvt_pk_fp8_f32 v7, v14, v15 op_sel:[0,0,1]
	v_cvt_pk_fp8_f32 v8, v18, v19 op_sel:[0,0,1]
	v_cvt_pk_fp8_f32 v9, v22, v23 op_sel:[0,0,1]
	v_lshlrev_b64 v[10:11], 11, v[10:11]
	v_lshl_add_u64 v[10:11], s[6:7], 0, v[10:11]
	v_lshl_add_u64 v[10:11], v[10:11], 0, v[2:3]
	global_store_dwordx4 v[10:11], v[6:9], off sc1
	v_pk_mul_f32 v[16:17], v[122:123], s[0:1] op_sel_hi:[1,0]
	v_pk_mul_f32 v[20:21], v[118:119], s[0:1] op_sel_hi:[1,0]
	v_pk_mul_f32 v[8:9], v[126:127], s[0:1] op_sel_hi:[1,0]
	v_pk_mul_f32 v[24:25], v[114:115], s[0:1] op_sel_hi:[1,0]
	v_cvt_pk_fp8_f32 v6, v8, v9
	v_pk_mul_f32 v[12:13], v[128:129], s[0:1] op_sel_hi:[1,0]
	v_cvt_pk_fp8_f32 v7, v16, v17
	v_cvt_pk_fp8_f32 v8, v20, v21
	v_cvt_pk_fp8_f32 v9, v24, v25
	v_pk_mul_f32 v[14:15], v[124:125], s[0:1] op_sel_hi:[1,0]
	v_pk_mul_f32 v[18:19], v[120:121], s[0:1] op_sel_hi:[1,0]
	v_pk_mul_f32 v[22:23], v[116:117], s[0:1] op_sel_hi:[1,0]
	v_add_u32_e32 v10, 0x80, v4
	v_mov_b32_e32 v11, v5
	v_cvt_pk_fp8_f32 v6, v12, v13 op_sel:[0,0,1]
	v_cvt_pk_fp8_f32 v7, v14, v15 op_sel:[0,0,1]
	v_cvt_pk_fp8_f32 v8, v18, v19 op_sel:[0,0,1]
	v_cvt_pk_fp8_f32 v9, v22, v23 op_sel:[0,0,1]
	v_lshlrev_b64 v[10:11], 11, v[10:11]
	v_lshl_add_u64 v[10:11], s[6:7], 0, v[10:11]
	v_lshl_add_u64 v[10:11], v[10:11], 0, v[2:3]
	global_store_dwordx4 v[10:11], v[6:9], off sc1
	v_pk_mul_f32 v[16:17], v[106:107], s[0:1] op_sel_hi:[1,0]
	v_pk_mul_f32 v[20:21], v[102:103], s[0:1] op_sel_hi:[1,0]
	v_pk_mul_f32 v[8:9], v[110:111], s[0:1] op_sel_hi:[1,0]
	v_pk_mul_f32 v[24:25], v[98:99], s[0:1] op_sel_hi:[1,0]
	v_cvt_pk_fp8_f32 v6, v8, v9
	v_pk_mul_f32 v[12:13], v[112:113], s[0:1] op_sel_hi:[1,0]
	v_cvt_pk_fp8_f32 v7, v16, v17
	v_cvt_pk_fp8_f32 v8, v20, v21
	v_cvt_pk_fp8_f32 v9, v24, v25
	v_pk_mul_f32 v[14:15], v[108:109], s[0:1] op_sel_hi:[1,0]
	v_pk_mul_f32 v[18:19], v[104:105], s[0:1] op_sel_hi:[1,0]
	v_pk_mul_f32 v[22:23], v[100:101], s[0:1] op_sel_hi:[1,0]
	v_add_u32_e32 v10, 0x90, v4
	v_mov_b32_e32 v11, v5
	v_cvt_pk_fp8_f32 v6, v12, v13 op_sel:[0,0,1]
	v_cvt_pk_fp8_f32 v7, v14, v15 op_sel:[0,0,1]
	v_cvt_pk_fp8_f32 v8, v18, v19 op_sel:[0,0,1]
	v_cvt_pk_fp8_f32 v9, v22, v23 op_sel:[0,0,1]
	v_lshlrev_b64 v[10:11], 11, v[10:11]
	v_lshl_add_u64 v[10:11], s[6:7], 0, v[10:11]
	v_lshl_add_u64 v[10:11], v[10:11], 0, v[2:3]
	global_store_dwordx4 v[10:11], v[6:9], off sc1
	v_pk_mul_f32 v[16:17], v[90:91], s[0:1] op_sel_hi:[1,0]
	v_pk_mul_f32 v[20:21], v[86:87], s[0:1] op_sel_hi:[1,0]
	v_pk_mul_f32 v[8:9], v[94:95], s[0:1] op_sel_hi:[1,0]
	v_pk_mul_f32 v[24:25], v[82:83], s[0:1] op_sel_hi:[1,0]
	v_cvt_pk_fp8_f32 v6, v8, v9
	v_pk_mul_f32 v[12:13], v[96:97], s[0:1] op_sel_hi:[1,0]
	v_cvt_pk_fp8_f32 v7, v16, v17
	v_cvt_pk_fp8_f32 v8, v20, v21
	v_cvt_pk_fp8_f32 v9, v24, v25
	v_pk_mul_f32 v[14:15], v[92:93], s[0:1] op_sel_hi:[1,0]
	v_pk_mul_f32 v[18:19], v[88:89], s[0:1] op_sel_hi:[1,0]
	v_pk_mul_f32 v[22:23], v[84:85], s[0:1] op_sel_hi:[1,0]
	v_add_u32_e32 v10, 0xa0, v4
	v_mov_b32_e32 v11, v5
	v_cvt_pk_fp8_f32 v6, v12, v13 op_sel:[0,0,1]
	v_cvt_pk_fp8_f32 v7, v14, v15 op_sel:[0,0,1]
	v_cvt_pk_fp8_f32 v8, v18, v19 op_sel:[0,0,1]
	v_cvt_pk_fp8_f32 v9, v22, v23 op_sel:[0,0,1]
	v_lshlrev_b64 v[10:11], 11, v[10:11]
	v_lshl_add_u64 v[10:11], s[6:7], 0, v[10:11]
	v_lshl_add_u64 v[10:11], v[10:11], 0, v[2:3]
	global_store_dwordx4 v[10:11], v[6:9], off sc1
	v_pk_mul_f32 v[14:15], v[74:75], s[0:1] op_sel_hi:[1,0]
	v_pk_mul_f32 v[18:19], v[70:71], s[0:1] op_sel_hi:[1,0]
	v_pk_mul_f32 v[8:9], v[78:79], s[0:1] op_sel_hi:[1,0]
	v_pk_mul_f32 v[22:23], v[66:67], s[0:1] op_sel_hi:[1,0]
	v_cvt_pk_fp8_f32 v6, v8, v9
	v_pk_mul_f32 v[10:11], v[80:81], s[0:1] op_sel_hi:[1,0]
	v_cvt_pk_fp8_f32 v7, v14, v15
	v_cvt_pk_fp8_f32 v8, v18, v19
	v_cvt_pk_fp8_f32 v9, v22, v23
	v_pk_mul_f32 v[12:13], v[76:77], s[0:1] op_sel_hi:[1,0]
	v_pk_mul_f32 v[16:17], v[72:73], s[0:1] op_sel_hi:[1,0]
	v_pk_mul_f32 v[20:21], v[68:69], s[0:1] op_sel_hi:[1,0]
	v_add_u32_e32 v4, 0xb0, v4
	v_cvt_pk_fp8_f32 v6, v10, v11 op_sel:[0,0,1]
	v_cvt_pk_fp8_f32 v7, v12, v13 op_sel:[0,0,1]
	v_cvt_pk_fp8_f32 v8, v16, v17 op_sel:[0,0,1]
	v_cvt_pk_fp8_f32 v9, v20, v21 op_sel:[0,0,1]
	v_lshlrev_b64 v[4:5], 11, v[4:5]
	v_lshl_add_u64 v[4:5], s[6:7], 0, v[4:5]
	v_lshl_add_u64 v[2:3], v[4:5], 0, v[2:3]
	global_store_dwordx4 v[2:3], v[6:9], off sc1
	s_waitcnt vmcnt(0)
	s_cmpk_gt_u32 s3, 0xff
	s_cbranch_scc1 .LBB3_27
	s_barrier

	.amdhsa_kernel _ZN2rb6k_gemmILi1ENS_7SchedP2ENS_7EpiSlabEEEvT0_T1_
		.amdhsa_group_segment_fixed_size 0
		.amdhsa_private_segment_fixed_size 0
		.amdhsa_kernarg_size 40
		.amdhsa_user_sgpr_count 2
		.amdhsa_user_sgpr_dispatch_ptr 0
		.amdhsa_user_sgpr_queue_ptr 0
		.amdhsa_user_sgpr_kernarg_segment_ptr 1
		.amdhsa_user_sgpr_dispatch_id 0
		.amdhsa_user_sgpr_kernarg_preload_length 0
		.amdhsa_user_sgpr_kernarg_preload_offset 0
		.amdhsa_user_sgpr_private_segment_size 0
		.amdhsa_uses_dynamic_stack 0
		.amdhsa_enable_private_segment 0
		.amdhsa_system_sgpr_workgroup_id_x 1
		.amdhsa_system_sgpr_workgroup_id_y 0
		.amdhsa_system_sgpr_workgroup_id_z 0
		.amdhsa_system_sgpr_workgroup_info 0
		.amdhsa_system_vgpr_workitem_id 0
		.amdhsa_next_free_vgpr 210
		.amdhsa_next_free_sgpr 67
		.amdhsa_accum_offset 212
		.amdhsa_reserve_vcc 1
		.amdhsa_float_round_mode_32 0
		.amdhsa_float_round_mode_16_64 0
		.amdhsa_float_denorm_mode_32 3
		.amdhsa_float_denorm_mode_16_64 3
		.amdhsa_dx10_clamp 1
		.amdhsa_ieee_mode 1
		.amdhsa_fp16_overflow 0
		.amdhsa_tg_split 0
		.amdhsa_exception_fp_ieee_invalid_op 0
		.amdhsa_exception_fp_denorm_src 0
		.amdhsa_exception_fp_ieee_div_zero 0
		.amdhsa_exception_fp_ieee_overflow 0
		.amdhsa_exception_fp_ieee_underflow 0
		.amdhsa_exception_fp_ieee_inexact 0
		.amdhsa_exception_int_div_zero 0
	.end_amdhsa_kernel

.LBB4_13:
	s_waitcnt vmcnt(6)
	s_barrier
	s_setprio 1
	v_mfma_f32_16x16x128_f8f6f4 v[116:119], v[24:31], v[56:63], v[116:119]
	s_add_i32 s44, s44, 2
	s_add_u32 s10, s10, 0x100
	s_addc_u32 s11, s11, 0
	s_cmp_gt_u32 s44, 13
	v_mfma_f32_16x16x128_f8f6f4 v[112:115], v[16:23], v[56:63], v[112:115]
	v_mfma_f32_16x16x128_f8f6f4 v[100:103], v[24:31], v[48:55], v[100:103]
	v_mfma_f32_16x16x128_f8f6f4 v[96:99], v[16:23], v[48:55], v[96:99]
	v_mfma_f32_16x16x128_f8f6f4 v[84:87], v[24:31], v[40:47], v[84:87]
	v_mfma_f32_16x16x128_f8f6f4 v[80:83], v[16:23], v[40:47], v[80:83]
	v_mfma_f32_16x16x128_f8f6f4 v[68:71], v[24:31], v[32:39], v[68:71]
	v_mfma_f32_16x16x128_f8f6f4 v[64:67], v[16:23], v[32:39], v[64:67]
	s_setprio 0
	s_barrier
	s_cbranch_scc1 .LBB4_30
.LBB4_14:
	s_cmpk_eq_i32 s10, 0x700
	s_cselect_b64 s[18:19], -1, 0
	s_cmpk_lg_i32 s10, 0x700
	ds_read_b128 v[0:3], v202
	ds_read_b128 v[8:11], v202 offset:2048
	ds_read_b128 v[4:7], v203
	ds_read_b128 v[12:15], v203 offset:2048
	s_cselect_b64 s[24:25], -1, 0
	s_add_u32 s49, s16, s10
	s_addc_u32 s50, s9, s11
	s_add_u32 s46, s8, s10
	s_addc_u32 s47, s3, s11
	s_add_u32 s20, s46, 0x100
	s_addc_u32 s48, s47, 0
	s_add_u32 s12, s49, 0x40080
	s_addc_u32 s0, s50, 0
	s_and_b32 s13, s0, 0xffff
	s_mov_b32 m0, s42
	ds_read_b128 v[56:59], v200
	ds_read_b128 v[48:51], v200 offset:2048
	ds_read_b128 v[60:63], v201
	ds_read_b128 v[52:55], v201 offset:2048
	ds_read_b128 v[40:43], v200 offset:4096
	ds_read_b128 v[32:35], v200 offset:6144
	ds_read_b128 v[44:47], v201 offset:4096
	ds_read_b128 v[36:39], v201 offset:6144
	buffer_load_dwordx4 v192, s[12:15], 0 offen lds
	s_mov_b32 m0, s43
	s_nop 0
	buffer_load_dwordx4 v194, s[12:15], 0 offen lds
	s_waitcnt lgkmcnt(8)
	s_barrier
	s_waitcnt lgkmcnt(0)
	s_setprio 1
	v_mfma_f32_16x16x128_f8f6f4 v[188:191], v[0:7], v[56:63], v[188:191]
	v_mfma_f32_16x16x128_f8f6f4 v[184:187], v[8:15], v[56:63], v[184:187]
	v_mfma_f32_16x16x128_f8f6f4 v[172:175], v[0:7], v[48:55], v[172:175]
	v_mfma_f32_16x16x128_f8f6f4 v[168:171], v[8:15], v[48:55], v[168:171]
	v_mfma_f32_16x16x128_f8f6f4 v[156:159], v[0:7], v[40:47], v[156:159]
	v_mfma_f32_16x16x128_f8f6f4 v[152:155], v[8:15], v[40:47], v[152:155]
	v_mfma_f32_16x16x128_f8f6f4 v[140:143], v[0:7], v[32:39], v[140:143]
	v_mfma_f32_16x16x128_f8f6f4 v[136:139], v[8:15], v[32:39], v[136:139]
	s_setprio 0
	s_barrier
	ds_read_b128 v[24:27], v204
	ds_read_b128 v[16:19], v204 offset:2048
	ds_read_b128 v[28:31], v205
	ds_read_b128 v[20:23], v205 offset:2048
	s_and_b64 vcc, exec, s[18:19]
	s_cbranch_vccnz .LBB4_16
	s_and_b32 s21, s48, 0xffff
	s_mov_b32 s22, s14
	s_mov_b32 s23, s15
	s_mov_b32 m0, s28
	s_nop 0
	buffer_load_dwordx4 v193, s[20:23], 0 offen lds
	s_mov_b32 m0, s29
	s_nop 0
	buffer_load_dwordx4 v195, s[20:23], 0 offen lds
.LBB4_16:
	s_barrier
	s_waitcnt lgkmcnt(0)
	s_setprio 1
	v_mfma_f32_16x16x128_f8f6f4 v[180:183], v[24:31], v[56:63], v[180:183]
	s_add_u32 s12, s49, 0x100
	s_addc_u32 s21, s50, 0
	v_mfma_f32_16x16x128_f8f6f4 v[176:179], v[16:23], v[56:63], v[176:179]
	v_mfma_f32_16x16x128_f8f6f4 v[164:167], v[24:31], v[48:55], v[164:167]
	v_mfma_f32_16x16x128_f8f6f4 v[160:163], v[16:23], v[48:55], v[160:163]
	v_mfma_f32_16x16x128_f8f6f4 v[148:151], v[24:31], v[40:47], v[148:151]
	v_mfma_f32_16x16x128_f8f6f4 v[144:147], v[16:23], v[40:47], v[144:147]
	v_mfma_f32_16x16x128_f8f6f4 v[132:135], v[24:31], v[32:39], v[132:135]
	v_mfma_f32_16x16x128_f8f6f4 v[128:131], v[16:23], v[32:39], v[128:131]
	s_setprio 0
	s_barrier
	ds_read_b128 v[56:59], v200 offset:16384
	ds_read_b128 v[48:51], v200 offset:18432
	ds_read_b128 v[60:63], v201 offset:16384
	ds_read_b128 v[52:55], v201 offset:18432
	ds_read_b128 v[40:43], v200 offset:20480
	ds_read_b128 v[32:35], v200 offset:22528
	ds_read_b128 v[44:47], v201 offset:20480
	ds_read_b128 v[36:39], v201 offset:22528
	v_cndmask_b32_e64 v206, 0, 1, s[24:25]
	v_cmp_ne_u32_e64 s[0:1], 1, v206
	s_andn2_b64 vcc, exec, s[24:25]
	s_cbranch_vccnz .LBB4_18
	s_and_b32 s13, s21, 0xffff
	s_mov_b32 m0, s7
	s_nop 0
	buffer_load_dwordx4 v192, s[12:15], 0 offen lds
	s_mov_b32 m0, s30
	s_nop 0
	buffer_load_dwordx4 v194, s[12:15], 0 offen lds
.LBB4_18:
	s_barrier
	s_waitcnt lgkmcnt(0)
	s_setprio 1
	v_mfma_f32_16x16x128_f8f6f4 v[124:127], v[0:7], v[56:63], v[124:127]
	v_mfma_f32_16x16x128_f8f6f4 v[120:123], v[8:15], v[56:63], v[120:123]
	v_mfma_f32_16x16x128_f8f6f4 v[108:111], v[0:7], v[48:55], v[108:111]
	v_mfma_f32_16x16x128_f8f6f4 v[104:107], v[8:15], v[48:55], v[104:107]
	v_mfma_f32_16x16x128_f8f6f4 v[92:95], v[0:7], v[40:47], v[92:95]
	v_mfma_f32_16x16x128_f8f6f4 v[88:91], v[8:15], v[40:47], v[88:91]
	v_mfma_f32_16x16x128_f8f6f4 v[76:79], v[0:7], v[32:39], v[76:79]
	v_mfma_f32_16x16x128_f8f6f4 v[72:75], v[8:15], v[32:39], v[72:75]
	s_setprio 0
	s_barrier
	s_and_b64 vcc, exec, s[0:1]
	s_mov_b64 s[22:23], -1
	s_cbranch_vccnz .LBB4_20
	s_add_u32 s52, s46, 0x4100
	s_addc_u32 s13, s47, 0
	s_mov_b32 m0, s17
	s_and_b32 s53, s13, 0xffff
	s_mov_b32 s54, s14
	s_mov_b32 s55, s15
	buffer_load_dwordx4 v193, s[52:55], 0 offen lds
	s_mov_b32 m0, s31
	s_mov_b64 s[22:23], 0
	buffer_load_dwordx4 v195, s[52:55], 0 offen lds
	s_waitcnt vmcnt(6)

.LBB4_22:
	s_barrier
	s_setprio 1
	v_mfma_f32_16x16x128_f8f6f4 v[116:119], v[24:31], v[56:63], v[116:119]
	v_add_u32_e32 v0, s45, v198
	v_add_u32_e32 v4, s45, v199
	v_mfma_f32_16x16x128_f8f6f4 v[112:115], v[16:23], v[56:63], v[112:115]
	v_mfma_f32_16x16x128_f8f6f4 v[100:103], v[24:31], v[48:55], v[100:103]
	v_mfma_f32_16x16x128_f8f6f4 v[96:99], v[16:23], v[48:55], v[96:99]
	v_mfma_f32_16x16x128_f8f6f4 v[84:87], v[24:31], v[40:47], v[84:87]
	v_mfma_f32_16x16x128_f8f6f4 v[80:83], v[16:23], v[40:47], v[80:83]
	v_mfma_f32_16x16x128_f8f6f4 v[68:71], v[24:31], v[32:39], v[68:71]
	v_mfma_f32_16x16x128_f8f6f4 v[64:67], v[16:23], v[32:39], v[64:67]
	s_setprio 0
	s_barrier
	ds_read_b128 v[8:11], v0
	ds_read_b128 v[0:3], v0 offset:2048
	ds_read_b128 v[12:15], v4
	ds_read_b128 v[4:7], v4 offset:2048
	ds_read_b128 v[56:59], v200 offset:32768
	ds_read_b128 v[48:51], v200 offset:34816
	ds_read_b128 v[60:63], v201 offset:32768
	ds_read_b128 v[52:55], v201 offset:34816
	ds_read_b128 v[40:43], v200 offset:36864
	ds_read_b128 v[32:35], v200 offset:38912
	ds_read_b128 v[44:47], v201 offset:36864
	ds_read_b128 v[36:39], v201 offset:38912
	s_and_b64 vcc, exec, s[0:1]
	s_cbranch_vccnz .LBB4_24
	s_add_u32 s52, s49, 0x40100
	s_addc_u32 s13, s50, 0
	s_and_b32 s53, s13, 0xffff
	s_mov_b32 s54, s14
	s_mov_b32 s55, s15
	s_mov_b32 m0, s34
	s_nop 0
	buffer_load_dwordx4 v192, s[52:55], 0 offen lds
	s_mov_b32 m0, s35
	s_nop 0
	buffer_load_dwordx4 v194, s[52:55], 0 offen lds
.LBB4_24:
	s_waitcnt lgkmcnt(8)
	s_barrier
	s_waitcnt lgkmcnt(0)
	s_setprio 1
	v_mfma_f32_16x16x128_f8f6f4 v[188:191], v[8:15], v[56:63], v[188:191]
	v_mfma_f32_16x16x128_f8f6f4 v[184:187], v[0:7], v[56:63], v[184:187]
	v_mfma_f32_16x16x128_f8f6f4 v[172:175], v[8:15], v[48:55], v[172:175]
	v_mfma_f32_16x16x128_f8f6f4 v[168:171], v[0:7], v[48:55], v[168:171]
	v_mfma_f32_16x16x128_f8f6f4 v[156:159], v[8:15], v[40:47], v[156:159]
	v_mfma_f32_16x16x128_f8f6f4 v[152:155], v[0:7], v[40:47], v[152:155]
	v_mfma_f32_16x16x128_f8f6f4 v[140:143], v[8:15], v[32:39], v[140:143]
	v_mfma_f32_16x16x128_f8f6f4 v[136:139], v[0:7], v[32:39], v[136:139]
	s_setprio 0
	s_barrier
	s_add_i32 s13, 0, 0x1c000
	v_add_u32_e32 v16, s13, v198
	v_add_u32_e32 v20, s13, v199
	ds_read_b128 v[24:27], v16
	ds_read_b128 v[16:19], v16 offset:2048
	ds_read_b128 v[28:31], v20
	ds_read_b128 v[20:23], v20 offset:2048
	s_and_b64 vcc, exec, s[0:1]
	s_cbranch_vccnz .LBB4_26
	s_and_b64 s[22:23], exec, s[18:19]
	s_cselect_b32 s20, s8, s20
	s_cselect_b32 s13, s3, s48
	s_add_u32 s48, s20, 0x80
	s_addc_u32 s13, s13, 0
	s_and_b32 s49, s13, 0xffff
	s_mov_b32 s50, s14
	s_mov_b32 s51, s15
	s_mov_b32 m0, s36
	s_nop 0
	buffer_load_dwordx4 v193, s[48:51], 0 offen lds
	s_mov_b32 m0, s37
	s_nop 0
	buffer_load_dwordx4 v195, s[48:51], 0 offen lds
.LBB4_26:
	s_barrier
	s_waitcnt lgkmcnt(0)
	s_setprio 1
	v_mfma_f32_16x16x128_f8f6f4 v[180:183], v[24:31], v[56:63], v[180:183]
	v_mfma_f32_16x16x128_f8f6f4 v[176:179], v[16:23], v[56:63], v[176:179]
	v_mfma_f32_16x16x128_f8f6f4 v[164:167], v[24:31], v[48:55], v[164:167]
	v_mfma_f32_16x16x128_f8f6f4 v[160:163], v[16:23], v[48:55], v[160:163]
	v_mfma_f32_16x16x128_f8f6f4 v[148:151], v[24:31], v[40:47], v[148:151]
	v_mfma_f32_16x16x128_f8f6f4 v[144:147], v[16:23], v[40:47], v[144:147]
	v_mfma_f32_16x16x128_f8f6f4 v[132:135], v[24:31], v[32:39], v[132:135]
	v_mfma_f32_16x16x128_f8f6f4 v[128:131], v[16:23], v[32:39], v[128:131]
	s_setprio 0
	s_barrier
	ds_read_b128 v[56:59], v200 offset:49152
	ds_read_b128 v[48:51], v200 offset:51200
	ds_read_b128 v[60:63], v201 offset:49152
	ds_read_b128 v[52:55], v201 offset:51200
	ds_read_b128 v[40:43], v200 offset:53248
	ds_read_b128 v[32:35], v200 offset:55296
	ds_read_b128 v[44:47], v201 offset:53248
	ds_read_b128 v[36:39], v201 offset:55296
	s_and_b64 vcc, exec, s[0:1]
	s_cbranch_vccnz .LBB4_28
	s_and_b64 s[18:19], exec, s[18:19]
	s_cselect_b32 s12, s16, s12
	s_cselect_b32 s13, s9, s21
	s_add_u32 s12, s12, 0x80
	s_addc_u32 s13, s13, 0
	s_and_b32 s13, s13, 0xffff
	s_mov_b32 m0, s38
	s_nop 0
	buffer_load_dwordx4 v192, s[12:15], 0 offen lds
	s_mov_b32 m0, s39
	s_nop 0
	buffer_load_dwordx4 v194, s[12:15], 0 offen lds
.LBB4_28:
	s_barrier
	s_waitcnt lgkmcnt(0)
	s_setprio 1
	v_mfma_f32_16x16x128_f8f6f4 v[124:127], v[8:15], v[56:63], v[124:127]
	v_mfma_f32_16x16x128_f8f6f4 v[120:123], v[0:7], v[56:63], v[120:123]
	v_mfma_f32_16x16x128_f8f6f4 v[108:111], v[8:15], v[48:55], v[108:111]
	v_mfma_f32_16x16x128_f8f6f4 v[104:107], v[0:7], v[48:55], v[104:107]
	v_mfma_f32_16x16x128_f8f6f4 v[92:95], v[8:15], v[40:47], v[92:95]
	v_mfma_f32_16x16x128_f8f6f4 v[88:91], v[0:7], v[40:47], v[88:91]
	v_mfma_f32_16x16x128_f8f6f4 v[76:79], v[8:15], v[32:39], v[76:79]
	v_mfma_f32_16x16x128_f8f6f4 v[72:75], v[0:7], v[32:39], v[72:75]
	s_setprio 0
	s_barrier
	s_and_b64 vcc, exec, s[0:1]
	s_cbranch_vccnz .LBB4_13
	s_add_u32 s12, s46, 0x4180
	s_addc_u32 s0, s47, 0
	s_and_b32 s13, s0, 0xffff
	s_mov_b32 m0, s40
	s_nop 0
	buffer_load_dwordx4 v193, s[12:15], 0 offen lds
	s_mov_b32 m0, s41
	s_nop 0
	buffer_load_dwordx4 v195, s[12:15], 0 offen lds
	s_branch .LBB4_13
.LBB4_30:
	s_lshl_b32 s0, s33, 8
	s_add_i32 s0, s0, 0
	v_lshl_add_u32 v0, v197, 6, s0
	v_lshl_or_b32 v1, s27, 6, v196
	v_add_u32_e32 v0, 0x20000, v0
	s_nop 15
	s_nop 15
	v_add_u32_e32 v22, s6, v1
	ds_read_b128 v[12:15], v0
	ds_read_b128 v[8:11], v0 offset:16
	ds_read_b128 v[4:7], v0 offset:32
	ds_read_b128 v[0:3], v0 offset:48
	s_waitcnt lgkmcnt(3)
	v_pk_mul_f32 v[20:21], v[188:189], v[12:13]
	s_waitcnt lgkmcnt(2)
	v_pk_mul_f32 v[28:29], v[184:185], v[8:9]
	s_waitcnt lgkmcnt(1)
	v_pk_mul_f32 v[32:33], v[180:181], v[4:5]
	s_waitcnt lgkmcnt(0)
	v_pk_mul_f32 v[36:37], v[176:177], v[0:1]
	v_cvt_pk_fp8_f32 v18, v20, v21
	v_lshlrev_b32_e32 v16, 4, v197
	v_cvt_pk_fp8_f32 v19, v28, v29
	v_cvt_pk_fp8_f32 v20, v32, v33
	v_cvt_pk_fp8_f32 v21, v36, v37
	v_lshl_or_b32 v16, s33, 6, v16
	v_or_b32_e32 v24, s2, v16
	v_pk_mul_f32 v[16:17], v[190:191], v[14:15]
	v_pk_mul_f32 v[26:27], v[186:187], v[10:11]
	v_pk_mul_f32 v[30:31], v[182:183], v[6:7]
	v_pk_mul_f32 v[34:35], v[178:179], v[2:3]
	v_ashrrev_i32_e32 v23, 31, v22
	v_cvt_pk_fp8_f32 v18, v16, v17 op_sel:[0,0,1]
	v_cvt_pk_fp8_f32 v19, v26, v27 op_sel:[0,0,1]
	v_cvt_pk_fp8_f32 v20, v30, v31 op_sel:[0,0,1]
	v_cvt_pk_fp8_f32 v21, v34, v35 op_sel:[0,0,1]
	v_lshlrev_b64 v[16:17], 13, v[22:23]
	v_ashrrev_i32_e32 v25, 31, v24
	v_lshl_add_u64 v[16:17], s[4:5], 0, v[16:17]
	v_lshl_add_u64 v[16:17], v[16:17], 0, v[24:25]
	global_store_dwordx4 v[16:17], v[18:21], off sc1
	v_pk_mul_f32 v[32:33], v[168:169], v[8:9]
	v_pk_mul_f32 v[36:37], v[164:165], v[4:5]
	v_pk_mul_f32 v[20:21], v[172:173], v[12:13]
	v_pk_mul_f32 v[40:41], v[160:161], v[0:1]
	v_cvt_pk_fp8_f32 v18, v20, v21
	v_or_b32_e32 v26, 16, v22
	v_cvt_pk_fp8_f32 v19, v32, v33
	v_cvt_pk_fp8_f32 v20, v36, v37
	v_cvt_pk_fp8_f32 v21, v40, v41
	v_pk_mul_f32 v[28:29], v[174:175], v[14:15]
	v_pk_mul_f32 v[30:31], v[170:171], v[10:11]
	v_pk_mul_f32 v[34:35], v[166:167], v[6:7]
	v_pk_mul_f32 v[38:39], v[162:163], v[2:3]
	v_ashrrev_i32_e32 v27, 31, v26
	v_cvt_pk_fp8_f32 v18, v28, v29 op_sel:[0,0,1]
	v_cvt_pk_fp8_f32 v19, v30, v31 op_sel:[0,0,1]
	v_cvt_pk_fp8_f32 v20, v34, v35 op_sel:[0,0,1]
	v_cvt_pk_fp8_f32 v21, v38, v39 op_sel:[0,0,1]
	v_lshlrev_b64 v[26:27], 13, v[26:27]
	v_lshl_add_u64 v[26:27], s[4:5], 0, v[26:27]
	v_lshl_add_u64 v[26:27], v[26:27], 0, v[24:25]
	global_store_dwordx4 v[26:27], v[18:21], off sc1
	v_pk_mul_f32 v[32:33], v[152:153], v[8:9]
	v_pk_mul_f32 v[36:37], v[148:149], v[4:5]
	v_pk_mul_f32 v[20:21], v[156:157], v[12:13]
	v_pk_mul_f32 v[40:41], v[144:145], v[0:1]
	v_cvt_pk_fp8_f32 v18, v20, v21
	v_or_b32_e32 v26, 32, v22
	v_cvt_pk_fp8_f32 v19, v32, v33
	v_cvt_pk_fp8_f32 v20, v36, v37
	v_cvt_pk_fp8_f32 v21, v40, v41
	v_pk_mul_f32 v[28:29], v[158:159], v[14:15]
	v_pk_mul_f32 v[30:31], v[154:155], v[10:11]
	v_pk_mul_f32 v[34:35], v[150:151], v[6:7]
	v_pk_mul_f32 v[38:39], v[146:147], v[2:3]
	v_ashrrev_i32_e32 v27, 31, v26
	v_cvt_pk_fp8_f32 v18, v28, v29 op_sel:[0,0,1]
	v_cvt_pk_fp8_f32 v19, v30, v31 op_sel:[0,0,1]
	v_cvt_pk_fp8_f32 v20, v34, v35 op_sel:[0,0,1]
	v_cvt_pk_fp8_f32 v21, v38, v39 op_sel:[0,0,1]
	v_lshlrev_b64 v[26:27], 13, v[26:27]
	v_lshl_add_u64 v[26:27], s[4:5], 0, v[26:27]
	v_lshl_add_u64 v[26:27], v[26:27], 0, v[24:25]
	global_store_dwordx4 v[26:27], v[18:21], off sc1
	v_pk_mul_f32 v[30:31], v[136:137], v[8:9]
	v_pk_mul_f32 v[34:35], v[132:133], v[4:5]
	v_pk_mul_f32 v[20:21], v[140:141], v[12:13]
	v_pk_mul_f32 v[38:39], v[128:129], v[0:1]
	v_cvt_pk_fp8_f32 v18, v20, v21
	v_or_b32_e32 v22, 48, v22
	v_cvt_pk_fp8_f32 v19, v30, v31
	v_cvt_pk_fp8_f32 v20, v34, v35
	v_cvt_pk_fp8_f32 v21, v38, v39
	v_pk_mul_f32 v[26:27], v[142:143], v[14:15]
	v_pk_mul_f32 v[28:29], v[138:139], v[10:11]
	v_pk_mul_f32 v[32:33], v[134:135], v[6:7]
	v_pk_mul_f32 v[36:37], v[130:131], v[2:3]
	v_ashrrev_i32_e32 v23, 31, v22
	v_cvt_pk_fp8_f32 v18, v26, v27 op_sel:[0,0,1]
	v_cvt_pk_fp8_f32 v19, v28, v29 op_sel:[0,0,1]
	v_cvt_pk_fp8_f32 v20, v32, v33 op_sel:[0,0,1]
	v_cvt_pk_fp8_f32 v21, v36, v37 op_sel:[0,0,1]
	v_lshlrev_b64 v[22:23], 13, v[22:23]
	v_lshl_add_u64 v[22:23], s[4:5], 0, v[22:23]
	v_lshl_add_u64 v[22:23], v[22:23], 0, v[24:25]
	global_store_dwordx4 v[22:23], v[18:21], off sc1
	v_pk_mul_f32 v[26:27], v[120:121], v[8:9]
	v_pk_mul_f32 v[30:31], v[116:117], v[4:5]
	v_pk_mul_f32 v[20:21], v[124:125], v[12:13]
	v_pk_mul_f32 v[34:35], v[112:113], v[0:1]
	v_cvt_pk_fp8_f32 v18, v20, v21
	v_pk_mul_f32 v[22:23], v[126:127], v[14:15]
	v_cvt_pk_fp8_f32 v19, v26, v27
	v_cvt_pk_fp8_f32 v20, v30, v31
	v_cvt_pk_fp8_f32 v21, v34, v35
	v_pk_mul_f32 v[24:25], v[122:123], v[10:11]
	v_pk_mul_f32 v[28:29], v[118:119], v[6:7]
	v_pk_mul_f32 v[32:33], v[114:115], v[2:3]
	v_cvt_pk_fp8_f32 v18, v22, v23 op_sel:[0,0,1]
	v_cvt_pk_fp8_f32 v19, v24, v25 op_sel:[0,0,1]
	v_cvt_pk_fp8_f32 v20, v28, v29 op_sel:[0,0,1]
	v_cvt_pk_fp8_f32 v21, v32, v33 op_sel:[0,0,1]
	s_mov_b32 s0, 0x100000
	v_add_co_u32_e32 v22, vcc, s0, v16
	v_pk_mul_f32 v[26:27], v[104:105], v[8:9]
	s_nop 0
	v_addc_co_u32_e32 v23, vcc, 0, v17, vcc
	global_store_dwordx4 v[22:23], v[18:21], off sc1
	v_pk_mul_f32 v[30:31], v[100:101], v[4:5]
	v_pk_mul_f32 v[34:35], v[96:97], v[0:1]
	v_pk_mul_f32 v[20:21], v[108:109], v[12:13]
	v_pk_mul_f32 v[22:23], v[110:111], v[14:15]
	v_cvt_pk_fp8_f32 v18, v20, v21
	v_cvt_pk_fp8_f32 v19, v26, v27
	v_cvt_pk_fp8_f32 v20, v30, v31
	v_cvt_pk_fp8_f32 v21, v34, v35
	v_pk_mul_f32 v[24:25], v[106:107], v[10:11]
	v_pk_mul_f32 v[28:29], v[102:103], v[6:7]
	v_pk_mul_f32 v[32:33], v[98:99], v[2:3]
	v_cvt_pk_fp8_f32 v18, v22, v23 op_sel:[0,0,1]
	v_cvt_pk_fp8_f32 v19, v24, v25 op_sel:[0,0,1]
	v_cvt_pk_fp8_f32 v20, v28, v29 op_sel:[0,0,1]
	v_cvt_pk_fp8_f32 v21, v32, v33 op_sel:[0,0,1]
	s_mov_b32 s0, 0x120000
	v_add_co_u32_e32 v22, vcc, s0, v16
	v_pk_mul_f32 v[26:27], v[88:89], v[8:9]
	s_nop 0
	v_addc_co_u32_e32 v23, vcc, 0, v17, vcc
	global_store_dwordx4 v[22:23], v[18:21], off sc1
	v_pk_mul_f32 v[30:31], v[84:85], v[4:5]
	v_pk_mul_f32 v[34:35], v[80:81], v[0:1]
	v_pk_mul_f32 v[20:21], v[92:93], v[12:13]
	v_pk_mul_f32 v[22:23], v[94:95], v[14:15]
	v_cvt_pk_fp8_f32 v18, v20, v21
	v_cvt_pk_fp8_f32 v19, v26, v27
	v_cvt_pk_fp8_f32 v20, v30, v31
	v_cvt_pk_fp8_f32 v21, v34, v35
	v_pk_mul_f32 v[24:25], v[90:91], v[10:11]
	v_pk_mul_f32 v[28:29], v[86:87], v[6:7]
	v_pk_mul_f32 v[32:33], v[82:83], v[2:3]
	v_cvt_pk_fp8_f32 v18, v22, v23 op_sel:[0,0,1]
	v_cvt_pk_fp8_f32 v19, v24, v25 op_sel:[0,0,1]
	v_cvt_pk_fp8_f32 v20, v28, v29 op_sel:[0,0,1]
	v_cvt_pk_fp8_f32 v21, v32, v33 op_sel:[0,0,1]
	s_mov_b32 s0, 0x140000
	v_add_co_u32_e32 v22, vcc, s0, v16
	v_pk_mul_f32 v[12:13], v[76:77], v[12:13]
	s_nop 0
	v_addc_co_u32_e32 v23, vcc, 0, v17, vcc
	global_store_dwordx4 v[22:23], v[18:21], off sc1
	v_pk_mul_f32 v[8:9], v[72:73], v[8:9]
	v_pk_mul_f32 v[4:5], v[68:69], v[4:5]
	v_pk_mul_f32 v[18:19], v[66:67], v[2:3]
	v_pk_mul_f32 v[20:21], v[64:65], v[0:1]
	v_pk_mul_f32 v[14:15], v[78:79], v[14:15]
	v_cvt_pk_fp8_f32 v0, v12, v13
	v_cvt_pk_fp8_f32 v1, v8, v9
	v_cvt_pk_fp8_f32 v2, v4, v5
	v_cvt_pk_fp8_f32 v3, v20, v21
	v_pk_mul_f32 v[10:11], v[74:75], v[10:11]
	v_pk_mul_f32 v[6:7], v[70:71], v[6:7]
	v_cvt_pk_fp8_f32 v0, v14, v15 op_sel:[0,0,1]
	v_cvt_pk_fp8_f32 v1, v10, v11 op_sel:[0,0,1]
	v_cvt_pk_fp8_f32 v2, v6, v7 op_sel:[0,0,1]
	v_cvt_pk_fp8_f32 v3, v18, v19 op_sel:[0,0,1]
	v_add_co_u32_e32 v4, vcc, 0x160000, v16
	s_cmpk_lt_u32 s26, 0x100
	s_nop 0
	v_addc_co_u32_e32 v5, vcc, 0, v17, vcc
	global_store_dwordx4 v[4:5], v[0:3], off sc1
	s_waitcnt vmcnt(0)
	s_cbranch_scc0 .LBB4_32
	s_barrier

.LBB5_17:
	s_waitcnt vmcnt(6)
	s_barrier
	s_setprio 1
	v_mfma_f32_16x16x128_f8f6f4 v[108:111], v[24:31], v[56:63], v[108:111]
	s_add_i32 s45, s45, 2
	s_add_u32 s14, s14, 0x100
	s_addc_u32 s15, s15, 0
	s_cmp_gt_u32 s45, 13
	v_mfma_f32_16x16x128_f8f6f4 v[104:107], v[16:23], v[56:63], v[104:107]
	v_mfma_f32_16x16x128_f8f6f4 v[92:95], v[24:31], v[48:55], v[92:95]
	v_mfma_f32_16x16x128_f8f6f4 v[88:91], v[16:23], v[48:55], v[88:91]
	v_mfma_f32_16x16x128_f8f6f4 v[80:83], v[24:31], v[40:47], v[80:83]
	v_mfma_f32_16x16x128_f8f6f4 v[76:79], v[16:23], v[40:47], v[76:79]
	v_mfma_f32_16x16x128_f8f6f4 v[68:71], v[24:31], v[32:39], v[68:71]
	v_mfma_f32_16x16x128_f8f6f4 v[64:67], v[16:23], v[32:39], v[64:67]
	s_setprio 0
	s_barrier
	s_cbranch_scc1 .LBB5_34
.LBB5_18:
	s_cmpk_eq_i32 s14, 0x700
	s_cselect_b64 s[18:19], -1, 0
	s_cmpk_lg_i32 s14, 0x700
	ds_read_b128 v[0:3], v200
	ds_read_b128 v[8:11], v200 offset:2048
	ds_read_b128 v[4:7], v201
	ds_read_b128 v[12:15], v201 offset:2048
	s_cselect_b64 s[26:27], -1, 0
	s_add_u32 s50, s16, s14
	s_addc_u32 s51, s13, s15
	s_add_u32 s47, s12, s14
	s_addc_u32 s48, s7, s15
	s_add_u32 s20, s47, 0x100
	s_addc_u32 s49, s48, 0
	s_add_u32 s8, s50, 0x40080
	s_addc_u32 s0, s51, 0
	s_and_b32 s9, s0, 0xffff
	s_mov_b32 m0, s43
	ds_read_b128 v[56:59], v198
	ds_read_b128 v[48:51], v198 offset:2048
	ds_read_b128 v[60:63], v199
	ds_read_b128 v[52:55], v199 offset:2048
	ds_read_b128 v[40:43], v198 offset:4096
	ds_read_b128 v[32:35], v198 offset:6144
	ds_read_b128 v[44:47], v199 offset:4096
	ds_read_b128 v[36:39], v199 offset:6144
	buffer_load_dwordx4 v192, s[8:11], 0 offen lds
	s_mov_b32 m0, s44
	s_nop 0
	buffer_load_dwordx4 v193, s[8:11], 0 offen lds
	s_waitcnt lgkmcnt(8)
	s_barrier
	s_waitcnt lgkmcnt(0)
	s_setprio 1
	v_mfma_f32_16x16x128_f8f6f4 v[188:191], v[0:7], v[56:63], v[188:191]
	v_mfma_f32_16x16x128_f8f6f4 v[184:187], v[8:15], v[56:63], v[184:187]
	v_mfma_f32_16x16x128_f8f6f4 v[176:179], v[0:7], v[48:55], v[176:179]
	v_mfma_f32_16x16x128_f8f6f4 v[168:171], v[8:15], v[48:55], v[168:171]
	v_mfma_f32_16x16x128_f8f6f4 v[160:163], v[0:7], v[40:47], v[160:163]
	v_mfma_f32_16x16x128_f8f6f4 v[152:155], v[8:15], v[40:47], v[152:155]
	v_mfma_f32_16x16x128_f8f6f4 v[144:147], v[0:7], v[32:39], v[144:147]
	v_mfma_f32_16x16x128_f8f6f4 v[136:139], v[8:15], v[32:39], v[136:139]
	s_setprio 0
	s_barrier
	ds_read_b128 v[24:27], v202
	ds_read_b128 v[16:19], v202 offset:2048
	ds_read_b128 v[28:31], v203
	ds_read_b128 v[20:23], v203 offset:2048
	s_and_b64 vcc, exec, s[18:19]
	s_cbranch_vccnz .LBB5_20
	s_and_b32 s21, s49, 0xffff
	s_mov_b32 s22, s10
	s_mov_b32 s23, s11
	s_mov_b32 m0, s29
	s_nop 0
	buffer_load_dwordx4 v192, s[20:23], 0 offen lds
	s_mov_b32 m0, s30
	s_nop 0
	buffer_load_dwordx4 v193, s[20:23], 0 offen lds
.LBB5_20:
	s_barrier
	s_waitcnt lgkmcnt(0)
	s_setprio 1
	v_mfma_f32_16x16x128_f8f6f4 v[180:183], v[24:31], v[56:63], v[180:183]
	s_add_u32 s8, s50, 0x100
	s_addc_u32 s21, s51, 0
	v_mfma_f32_16x16x128_f8f6f4 v[172:175], v[16:23], v[56:63], v[172:175]
	v_mfma_f32_16x16x128_f8f6f4 v[164:167], v[24:31], v[48:55], v[164:167]
	v_mfma_f32_16x16x128_f8f6f4 v[156:159], v[16:23], v[48:55], v[156:159]
	v_mfma_f32_16x16x128_f8f6f4 v[148:151], v[24:31], v[40:47], v[148:151]
	v_mfma_f32_16x16x128_f8f6f4 v[140:143], v[16:23], v[40:47], v[140:143]
	v_mfma_f32_16x16x128_f8f6f4 v[132:135], v[24:31], v[32:39], v[132:135]
	v_mfma_f32_16x16x128_f8f6f4 v[128:131], v[16:23], v[32:39], v[128:131]
	s_setprio 0
	s_barrier
	ds_read_b128 v[56:59], v198 offset:16384
	ds_read_b128 v[48:51], v198 offset:18432
	ds_read_b128 v[60:63], v199 offset:16384
	ds_read_b128 v[52:55], v199 offset:18432
	ds_read_b128 v[40:43], v198 offset:20480
	ds_read_b128 v[32:35], v198 offset:22528
	ds_read_b128 v[44:47], v199 offset:20480
	ds_read_b128 v[36:39], v199 offset:22528
	v_cndmask_b32_e64 v204, 0, 1, s[26:27]
	v_cmp_ne_u32_e64 s[0:1], 1, v204
	s_andn2_b64 vcc, exec, s[26:27]
	s_cbranch_vccnz .LBB5_22
	s_and_b32 s9, s21, 0xffff
	s_mov_b32 m0, s25
	s_nop 0
	buffer_load_dwordx4 v192, s[8:11], 0 offen lds
	s_mov_b32 m0, s31
	s_nop 0
	buffer_load_dwordx4 v193, s[8:11], 0 offen lds
.LBB5_22:
	s_barrier
	s_waitcnt lgkmcnt(0)
	s_setprio 1
	v_mfma_f32_16x16x128_f8f6f4 v[124:127], v[0:7], v[56:63], v[124:127]
	v_mfma_f32_16x16x128_f8f6f4 v[120:123], v[8:15], v[56:63], v[120:123]
	v_mfma_f32_16x16x128_f8f6f4 v[116:119], v[0:7], v[48:55], v[116:119]
	v_mfma_f32_16x16x128_f8f6f4 v[112:115], v[8:15], v[48:55], v[112:115]
	v_mfma_f32_16x16x128_f8f6f4 v[100:103], v[0:7], v[40:47], v[100:103]
	v_mfma_f32_16x16x128_f8f6f4 v[96:99], v[8:15], v[40:47], v[96:99]
	v_mfma_f32_16x16x128_f8f6f4 v[84:87], v[0:7], v[32:39], v[84:87]
	v_mfma_f32_16x16x128_f8f6f4 v[72:75], v[8:15], v[32:39], v[72:75]
	s_setprio 0
	s_barrier
	s_and_b64 vcc, exec, s[0:1]
	s_mov_b64 s[22:23], -1
	s_cbranch_vccnz .LBB5_24
	s_add_u32 s52, s47, 0x40100
	s_addc_u32 s9, s48, 0
	s_mov_b32 m0, s17
	s_and_b32 s53, s9, 0xffff
	s_mov_b32 s54, s10
	s_mov_b32 s55, s11
	buffer_load_dwordx4 v192, s[52:55], 0 offen lds
	s_mov_b32 m0, s33
	s_mov_b64 s[22:23], 0
	buffer_load_dwordx4 v193, s[52:55], 0 offen lds
	s_waitcnt vmcnt(6)

.LBB5_26:
	s_barrier
	s_setprio 1
	v_mfma_f32_16x16x128_f8f6f4 v[108:111], v[24:31], v[56:63], v[108:111]
	v_add_u32_e32 v0, s46, v196
	v_add_u32_e32 v4, s46, v197
	v_mfma_f32_16x16x128_f8f6f4 v[104:107], v[16:23], v[56:63], v[104:107]
	v_mfma_f32_16x16x128_f8f6f4 v[92:95], v[24:31], v[48:55], v[92:95]
	v_mfma_f32_16x16x128_f8f6f4 v[88:91], v[16:23], v[48:55], v[88:91]
	v_mfma_f32_16x16x128_f8f6f4 v[80:83], v[24:31], v[40:47], v[80:83]
	v_mfma_f32_16x16x128_f8f6f4 v[76:79], v[16:23], v[40:47], v[76:79]
	v_mfma_f32_16x16x128_f8f6f4 v[68:71], v[24:31], v[32:39], v[68:71]
	v_mfma_f32_16x16x128_f8f6f4 v[64:67], v[16:23], v[32:39], v[64:67]
	s_setprio 0
	s_barrier
	ds_read_b128 v[8:11], v0
	ds_read_b128 v[0:3], v0 offset:2048
	ds_read_b128 v[12:15], v4
	ds_read_b128 v[4:7], v4 offset:2048
	ds_read_b128 v[56:59], v198 offset:32768
	ds_read_b128 v[48:51], v198 offset:34816
	ds_read_b128 v[60:63], v199 offset:32768
	ds_read_b128 v[52:55], v199 offset:34816
	ds_read_b128 v[40:43], v198 offset:36864
	ds_read_b128 v[32:35], v198 offset:38912
	ds_read_b128 v[44:47], v199 offset:36864
	ds_read_b128 v[36:39], v199 offset:38912
	s_and_b64 vcc, exec, s[0:1]
	s_cbranch_vccnz .LBB5_28
	s_add_u32 s52, s50, 0x40100
	s_addc_u32 s9, s51, 0
	s_and_b32 s53, s9, 0xffff
	s_mov_b32 s54, s10
	s_mov_b32 s55, s11
	s_mov_b32 m0, s34
	s_nop 0
	buffer_load_dwordx4 v192, s[52:55], 0 offen lds
	s_mov_b32 m0, s36
	s_nop 0
	buffer_load_dwordx4 v193, s[52:55], 0 offen lds
.LBB5_28:
	s_waitcnt lgkmcnt(8)
	s_barrier
	s_waitcnt lgkmcnt(0)
	s_setprio 1
	v_mfma_f32_16x16x128_f8f6f4 v[188:191], v[8:15], v[56:63], v[188:191]
	v_mfma_f32_16x16x128_f8f6f4 v[184:187], v[0:7], v[56:63], v[184:187]
	v_mfma_f32_16x16x128_f8f6f4 v[176:179], v[8:15], v[48:55], v[176:179]
	v_mfma_f32_16x16x128_f8f6f4 v[168:171], v[0:7], v[48:55], v[168:171]
	v_mfma_f32_16x16x128_f8f6f4 v[160:163], v[8:15], v[40:47], v[160:163]
	v_mfma_f32_16x16x128_f8f6f4 v[152:155], v[0:7], v[40:47], v[152:155]
	v_mfma_f32_16x16x128_f8f6f4 v[144:147], v[8:15], v[32:39], v[144:147]
	v_mfma_f32_16x16x128_f8f6f4 v[136:139], v[0:7], v[32:39], v[136:139]
	s_setprio 0
	s_barrier
	s_add_i32 s9, 0, 0x1c000
	v_add_u32_e32 v16, s9, v196
	v_add_u32_e32 v20, s9, v197
	ds_read_b128 v[24:27], v16
	ds_read_b128 v[16:19], v16 offset:2048
	ds_read_b128 v[28:31], v20
	ds_read_b128 v[20:23], v20 offset:2048
	s_and_b64 vcc, exec, s[0:1]
	s_cbranch_vccnz .LBB5_30
	s_and_b64 s[22:23], exec, s[18:19]
	s_cselect_b32 s20, s12, s20
	s_cselect_b32 s9, s7, s49
	s_add_u32 s52, s20, 0x80
	s_addc_u32 s9, s9, 0
	s_and_b32 s53, s9, 0xffff
	s_mov_b32 s54, s10
	s_mov_b32 s55, s11
	s_mov_b32 m0, s37
	s_nop 0
	buffer_load_dwordx4 v192, s[52:55], 0 offen lds
	s_mov_b32 m0, s38
	s_nop 0
	buffer_load_dwordx4 v193, s[52:55], 0 offen lds
.LBB5_30:
	s_barrier
	s_waitcnt lgkmcnt(0)
	s_setprio 1
	v_mfma_f32_16x16x128_f8f6f4 v[180:183], v[24:31], v[56:63], v[180:183]
	v_mfma_f32_16x16x128_f8f6f4 v[172:175], v[16:23], v[56:63], v[172:175]
	v_mfma_f32_16x16x128_f8f6f4 v[164:167], v[24:31], v[48:55], v[164:167]
	v_mfma_f32_16x16x128_f8f6f4 v[156:159], v[16:23], v[48:55], v[156:159]
	v_mfma_f32_16x16x128_f8f6f4 v[148:151], v[24:31], v[40:47], v[148:151]
	v_mfma_f32_16x16x128_f8f6f4 v[140:143], v[16:23], v[40:47], v[140:143]
	v_mfma_f32_16x16x128_f8f6f4 v[132:135], v[24:31], v[32:39], v[132:135]
	v_mfma_f32_16x16x128_f8f6f4 v[128:131], v[16:23], v[32:39], v[128:131]
	s_setprio 0
	s_barrier
	ds_read_b128 v[56:59], v198 offset:49152
	ds_read_b128 v[48:51], v198 offset:51200
	ds_read_b128 v[60:63], v199 offset:49152
	ds_read_b128 v[52:55], v199 offset:51200
	ds_read_b128 v[40:43], v198 offset:53248
	ds_read_b128 v[32:35], v198 offset:55296
	ds_read_b128 v[44:47], v199 offset:53248
	ds_read_b128 v[36:39], v199 offset:55296
	s_and_b64 vcc, exec, s[0:1]
	s_cbranch_vccnz .LBB5_32
	s_and_b64 s[18:19], exec, s[18:19]
	s_cselect_b32 s8, s16, s8
	s_cselect_b32 s9, s13, s21
	s_add_u32 s8, s8, 0x80
	s_addc_u32 s9, s9, 0
	s_and_b32 s9, s9, 0xffff
	s_mov_b32 m0, s39
	s_nop 0
	buffer_load_dwordx4 v192, s[8:11], 0 offen lds
	s_mov_b32 m0, s40
	s_nop 0
	buffer_load_dwordx4 v193, s[8:11], 0 offen lds
.LBB5_32:
	s_barrier
	s_waitcnt lgkmcnt(0)
	s_setprio 1
	v_mfma_f32_16x16x128_f8f6f4 v[124:127], v[8:15], v[56:63], v[124:127]
	v_mfma_f32_16x16x128_f8f6f4 v[120:123], v[0:7], v[56:63], v[120:123]
	v_mfma_f32_16x16x128_f8f6f4 v[116:119], v[8:15], v[48:55], v[116:119]
	v_mfma_f32_16x16x128_f8f6f4 v[112:115], v[0:7], v[48:55], v[112:115]
	v_mfma_f32_16x16x128_f8f6f4 v[100:103], v[8:15], v[40:47], v[100:103]
	v_mfma_f32_16x16x128_f8f6f4 v[96:99], v[0:7], v[40:47], v[96:99]
	v_mfma_f32_16x16x128_f8f6f4 v[84:87], v[8:15], v[32:39], v[84:87]
	v_mfma_f32_16x16x128_f8f6f4 v[72:75], v[0:7], v[32:39], v[72:75]
	s_setprio 0
	s_barrier
	s_and_b64 vcc, exec, s[0:1]
	s_cbranch_vccnz .LBB5_17
	s_add_u32 s8, s47, 0x40180
	s_addc_u32 s0, s48, 0
	s_and_b32 s9, s0, 0xffff
	s_mov_b32 m0, s41
	s_nop 0
	buffer_load_dwordx4 v192, s[8:11], 0 offen lds
	s_mov_b32 m0, s42
	s_nop 0
	buffer_load_dwordx4 v193, s[8:11], 0 offen lds
	s_branch .LBB5_17
.LBB5_34:
	s_lshl_b32 s1, s3, 6
	v_lshlrev_b32_e32 v0, 2, v195
	v_mov_b32_e32 v24, 0x3fffffcc
	v_lshl_or_b32 v0, s35, 5, v0
	s_add_i32 s0, 0, 0x20000
	v_bitop3_b32 v24, s1, v24, v194 bitop3:0xc8
	v_or_b32_e32 v28, s24, v0
	v_lshlrev_b32_e32 v0, 2, v0
	v_add_u32_e32 v24, s0, v24
	s_nop 15
	s_nop 15
	v_add_u32_e32 v34, s0, v0
	v_add_u32_e32 v0, 0, v0
	v_add_u32_e32 v46, 0x800, v24
	v_or_b32_e32 v44, s1, v194
	v_add_u32_e32 v35, 0x20400, v0
	ds_read_b128 v[16:19], v34
	ds_read_b128 v[8:11], v34 offset:64
	ds_read_b128 v[20:23], v35
	ds_read_b128 v[12:15], v35 offset:64
	ds_read_b128 v[4:7], v34 offset:512
	ds_read_b128 v[0:3], v35 offset:512
	ds_read2_b32 v[40:41], v46 offset1:4
	v_add_u32_e32 v38, s6, v44
	v_ashrrev_i32_e32 v39, 31, v38
	v_ashrrev_i32_e32 v29, 31, v28
	v_lshlrev_b64 v[30:31], 13, v[38:39]
	s_waitcnt lgkmcnt(6)
	v_pk_fma_f32 v[26:27], s[2:3], v[190:191], v[18:19] op_sel_hi:[0,1,1]
	v_pk_fma_f32 v[24:25], s[2:3], v[188:189], v[16:17] op_sel_hi:[0,1,1]
	v_lshl_add_u64 v[30:31], s[4:5], 0, v[30:31]
	v_lshlrev_b64 v[42:43], 2, v[28:29]
	s_waitcnt lgkmcnt(0)
	v_pk_fma_f32 v[24:25], v[20:21], v[40:41], v[24:25] op_sel_hi:[1,0,1]
	v_pk_fma_f32 v[26:27], v[22:23], v[40:41], v[26:27] op_sel_hi:[1,0,1]
	v_lshl_add_u64 v[32:33], v[30:31], 0, v[42:43]
	global_store_dwordx4 v[32:33], v[24:27], off sc1
	v_pk_fma_f32 v[36:37], s[2:3], v[182:183], v[6:7] op_sel_hi:[0,1,1]
	v_pk_fma_f32 v[36:37], v[2:3], v[40:41], v[36:37] op_sel_hi:[1,0,1]
	v_pk_fma_f32 v[24:25], s[2:3], v[186:187], v[10:11] op_sel_hi:[0,1,1]
	v_pk_fma_f32 v[26:27], s[2:3], v[184:185], v[8:9] op_sel_hi:[0,1,1]
	v_pk_fma_f32 v[28:29], v[12:13], v[40:41], v[26:27] op_sel_hi:[1,0,1]
	v_pk_fma_f32 v[30:31], v[14:15], v[40:41], v[24:25] op_sel_hi:[1,0,1]
	ds_read_b128 v[24:27], v34 offset:576
	global_store_dwordx4 v[32:33], v[28:31], off offset:64 sc1
	ds_read_b128 v[28:31], v35 offset:576
	v_pk_fma_f32 v[34:35], s[2:3], v[180:181], v[4:5] op_sel_hi:[0,1,1]
	v_pk_fma_f32 v[34:35], v[0:1], v[40:41], v[34:35] op_sel_hi:[1,0,1]
	global_store_dwordx4 v[32:33], v[34:37], off offset:512 sc1
	v_add_u32_e32 v48, 0x80, v44
	v_add_u32_e32 v49, 0x90, v44
	s_waitcnt lgkmcnt(1)
	v_pk_fma_f32 v[36:37], s[2:3], v[174:175], v[26:27] op_sel_hi:[0,1,1]
	v_pk_fma_f32 v[34:35], s[2:3], v[172:173], v[24:25] op_sel_hi:[0,1,1]
	s_waitcnt lgkmcnt(0)
	v_pk_fma_f32 v[34:35], v[28:29], v[40:41], v[34:35] op_sel_hi:[1,0,1]
	v_pk_fma_f32 v[36:37], v[30:31], v[40:41], v[36:37] op_sel_hi:[1,0,1]
	global_store_dwordx4 v[32:33], v[34:37], off offset:576 sc1
	v_add_u32_e32 v50, 0xa0, v44
	v_add_u32_e32 v51, 0xb0, v44
	v_or_b32_e32 v34, 16, v38
	v_ashrrev_i32_e32 v35, 31, v34
	v_lshlrev_b64 v[34:35], 13, v[34:35]
	v_lshl_add_u64 v[34:35], s[4:5], 0, v[34:35]
	v_lshl_add_u64 v[44:45], v[34:35], 0, v[42:43]
	v_pk_fma_f32 v[36:37], s[2:3], v[178:179], v[18:19] op_sel_hi:[0,1,1]
	v_pk_fma_f32 v[34:35], s[2:3], v[176:177], v[16:17] op_sel_hi:[0,1,1]
	v_mov_b32_e32 v40, v41
	v_pk_fma_f32 v[34:35], v[20:21], v[40:41], v[34:35] op_sel_hi:[1,0,1]
	v_pk_fma_f32 v[36:37], v[22:23], v[40:41], v[36:37] op_sel_hi:[1,0,1]
	global_store_dwordx4 v[44:45], v[34:37], off sc1
	s_cmpk_lt_u32 s28, 0x100
	s_nop 0
	v_pk_fma_f32 v[36:37], s[2:3], v[170:171], v[10:11] op_sel_hi:[0,1,1]
	v_pk_fma_f32 v[34:35], s[2:3], v[168:169], v[8:9] op_sel_hi:[0,1,1]
	v_pk_fma_f32 v[34:35], v[12:13], v[40:41], v[34:35] op_sel_hi:[1,0,1]
	v_pk_fma_f32 v[36:37], v[14:15], v[40:41], v[36:37] op_sel_hi:[1,0,1]
	global_store_dwordx4 v[44:45], v[34:37], off offset:64 sc1
	s_nop 1
	v_pk_fma_f32 v[36:37], s[2:3], v[166:167], v[6:7] op_sel_hi:[0,1,1]
	v_pk_fma_f32 v[34:35], s[2:3], v[164:165], v[4:5] op_sel_hi:[0,1,1]
	v_pk_fma_f32 v[34:35], v[0:1], v[40:41], v[34:35] op_sel_hi:[1,0,1]
	v_pk_fma_f32 v[36:37], v[2:3], v[40:41], v[36:37] op_sel_hi:[1,0,1]
	global_store_dwordx4 v[44:45], v[34:37], off offset:512 sc1
	s_nop 1
	v_pk_fma_f32 v[36:37], s[2:3], v[158:159], v[26:27] op_sel_hi:[0,1,1]
	v_pk_fma_f32 v[34:35], s[2:3], v[156:157], v[24:25] op_sel_hi:[0,1,1]
	v_pk_fma_f32 v[34:35], v[28:29], v[40:41], v[34:35] op_sel_hi:[1,0,1]
	v_pk_fma_f32 v[36:37], v[30:31], v[40:41], v[36:37] op_sel_hi:[1,0,1]
	global_store_dwordx4 v[44:45], v[34:37], off offset:576 sc1
	ds_read2_b32 v[40:41], v46 offset0:8 offset1:12
	v_pk_fma_f32 v[46:47], s[2:3], v[160:161], v[16:17] op_sel_hi:[0,1,1]
	v_or_b32_e32 v34, 32, v38
	v_ashrrev_i32_e32 v35, 31, v34
	v_lshlrev_b64 v[34:35], 13, v[34:35]
	v_lshl_add_u64 v[34:35], s[4:5], 0, v[34:35]
	v_lshl_add_u64 v[44:45], v[34:35], 0, v[42:43]
	v_pk_fma_f32 v[34:35], s[2:3], v[162:163], v[18:19] op_sel_hi:[0,1,1]
	s_waitcnt lgkmcnt(0)
	v_pk_fma_f32 v[36:37], v[22:23], v[40:41], v[34:35] op_sel_hi:[1,0,1]
	v_pk_fma_f32 v[34:35], v[20:21], v[40:41], v[46:47] op_sel_hi:[1,0,1]
	global_store_dwordx4 v[44:45], v[34:37], off sc1
	v_pk_fma_f32 v[46:47], s[2:3], v[152:153], v[8:9] op_sel_hi:[0,1,1]
	s_nop 0
	v_pk_fma_f32 v[34:35], s[2:3], v[154:155], v[10:11] op_sel_hi:[0,1,1]
	v_pk_fma_f32 v[36:37], v[14:15], v[40:41], v[34:35] op_sel_hi:[1,0,1]
	v_pk_fma_f32 v[34:35], v[12:13], v[40:41], v[46:47] op_sel_hi:[1,0,1]
	global_store_dwordx4 v[44:45], v[34:37], off offset:64 sc1
	v_pk_fma_f32 v[46:47], s[2:3], v[148:149], v[4:5] op_sel_hi:[0,1,1]
	s_nop 0
	v_pk_fma_f32 v[34:35], s[2:3], v[150:151], v[6:7] op_sel_hi:[0,1,1]
	v_pk_fma_f32 v[36:37], v[2:3], v[40:41], v[34:35] op_sel_hi:[1,0,1]
	v_pk_fma_f32 v[34:35], v[0:1], v[40:41], v[46:47] op_sel_hi:[1,0,1]
	global_store_dwordx4 v[44:45], v[34:37], off offset:512 sc1
	v_pk_fma_f32 v[46:47], s[2:3], v[140:141], v[24:25] op_sel_hi:[0,1,1]
	s_nop 0
	v_pk_fma_f32 v[34:35], s[2:3], v[142:143], v[26:27] op_sel_hi:[0,1,1]
	v_pk_fma_f32 v[36:37], v[30:31], v[40:41], v[34:35] op_sel_hi:[1,0,1]
	v_pk_fma_f32 v[34:35], v[28:29], v[40:41], v[46:47] op_sel_hi:[1,0,1]
	global_store_dwordx4 v[44:45], v[34:37], off offset:576 sc1
	v_mov_b32_e32 v40, v41
	s_nop 0
	v_or_b32_e32 v34, 48, v38
	v_ashrrev_i32_e32 v35, 31, v34
	v_lshlrev_b64 v[34:35], 13, v[34:35]
	v_lshl_add_u64 v[34:35], s[4:5], 0, v[34:35]
	v_lshl_add_u64 v[38:39], v[34:35], 0, v[42:43]
	v_pk_fma_f32 v[34:35], s[2:3], v[146:147], v[18:19] op_sel_hi:[0,1,1]
	v_pk_fma_f32 v[42:43], s[2:3], v[144:145], v[16:17] op_sel_hi:[0,1,1]
	v_pk_fma_f32 v[36:37], v[22:23], v[40:41], v[34:35] op_sel_hi:[1,0,1]
	v_pk_fma_f32 v[34:35], v[20:21], v[40:41], v[42:43] op_sel_hi:[1,0,1]
	global_store_dwordx4 v[38:39], v[34:37], off sc1
	v_pk_fma_f32 v[42:43], s[2:3], v[136:137], v[8:9] op_sel_hi:[0,1,1]
	s_mov_b64 s[4:5], 0x100000
	v_pk_fma_f32 v[34:35], s[2:3], v[138:139], v[10:11] op_sel_hi:[0,1,1]
	v_pk_fma_f32 v[36:37], v[14:15], v[40:41], v[34:35] op_sel_hi:[1,0,1]
	v_pk_fma_f32 v[34:35], v[12:13], v[40:41], v[42:43] op_sel_hi:[1,0,1]
	global_store_dwordx4 v[38:39], v[34:37], off offset:64 sc1
	v_pk_fma_f32 v[42:43], s[2:3], v[132:133], v[4:5] op_sel_hi:[0,1,1]
	s_nop 0
	v_pk_fma_f32 v[34:35], s[2:3], v[134:135], v[6:7] op_sel_hi:[0,1,1]
	v_pk_fma_f32 v[36:37], v[2:3], v[40:41], v[34:35] op_sel_hi:[1,0,1]
	v_pk_fma_f32 v[34:35], v[0:1], v[40:41], v[42:43] op_sel_hi:[1,0,1]
	global_store_dwordx4 v[38:39], v[34:37], off offset:512 sc1
	v_pk_fma_f32 v[42:43], s[2:3], v[128:129], v[24:25] op_sel_hi:[0,1,1]
	s_nop 0
	v_pk_fma_f32 v[34:35], s[2:3], v[130:131], v[26:27] op_sel_hi:[0,1,1]
	v_pk_fma_f32 v[36:37], v[30:31], v[40:41], v[34:35] op_sel_hi:[1,0,1]
	v_pk_fma_f32 v[34:35], v[28:29], v[40:41], v[42:43] op_sel_hi:[1,0,1]
	global_store_dwordx4 v[38:39], v[34:37], off offset:576 sc1
	v_and_b32_e32 v39, 0x7ffffffc, v51
	v_pk_fma_f32 v[42:43], s[2:3], v[124:125], v[16:17] op_sel_hi:[0,1,1]
	v_and_b32_e32 v34, 0x7fffffcc, v48
	v_add_u32_e32 v34, s0, v34
	ds_read_b32 v38, v34 offset:2048
	v_and_b32_e32 v36, 0x7fffffdc, v49
	v_and_b32_e32 v37, 0x7fffffec, v50
	v_pk_fma_f32 v[34:35], s[2:3], v[126:127], v[18:19] op_sel_hi:[0,1,1]
	v_add_u32_e32 v36, s0, v36
	v_add_u32_e32 v37, s0, v37
	v_add_u32_e32 v39, s0, v39
	s_mov_b32 s0, 0x100000
	ds_read_b32 v44, v36 offset:2048
	ds_read_b32 v46, v37 offset:2048
	ds_read_b32 v48, v39 offset:2048
	s_waitcnt lgkmcnt(3)
	v_pk_fma_f32 v[36:37], v[22:23], v[38:39], v[34:35] op_sel_hi:[1,0,1]
	v_pk_fma_f32 v[34:35], v[20:21], v[38:39], v[42:43] op_sel_hi:[1,0,1]
	v_add_co_u32_e32 v42, vcc, s0, v32
	v_lshl_add_u64 v[40:41], v[32:33], 0, s[4:5]
	s_nop 0
	v_addc_co_u32_e32 v43, vcc, 0, v33, vcc
	global_store_dwordx4 v[42:43], v[34:37], off sc1
	v_pk_fma_f32 v[42:43], s[2:3], v[120:121], v[8:9] op_sel_hi:[0,1,1]
	s_mov_b64 s[0:1], 0x120000
	v_pk_fma_f32 v[34:35], s[2:3], v[122:123], v[10:11] op_sel_hi:[0,1,1]
	v_pk_fma_f32 v[36:37], v[14:15], v[38:39], v[34:35] op_sel_hi:[1,0,1]
	v_pk_fma_f32 v[34:35], v[12:13], v[38:39], v[42:43] op_sel_hi:[1,0,1]
	global_store_dwordx4 v[40:41], v[34:37], off offset:64 sc1
	v_pk_fma_f32 v[42:43], s[2:3], v[108:109], v[4:5] op_sel_hi:[0,1,1]
	s_nop 0
	v_pk_fma_f32 v[34:35], s[2:3], v[110:111], v[6:7] op_sel_hi:[0,1,1]
	v_pk_fma_f32 v[36:37], v[2:3], v[38:39], v[34:35] op_sel_hi:[1,0,1]
	v_pk_fma_f32 v[34:35], v[0:1], v[38:39], v[42:43] op_sel_hi:[1,0,1]
	global_store_dwordx4 v[40:41], v[34:37], off offset:512 sc1
	v_pk_fma_f32 v[42:43], s[2:3], v[104:105], v[24:25] op_sel_hi:[0,1,1]
	s_nop 0
	v_pk_fma_f32 v[34:35], s[2:3], v[106:107], v[26:27] op_sel_hi:[0,1,1]
	v_pk_fma_f32 v[36:37], v[30:31], v[38:39], v[34:35] op_sel_hi:[1,0,1]
	v_pk_fma_f32 v[34:35], v[28:29], v[38:39], v[42:43] op_sel_hi:[1,0,1]
	global_store_dwordx4 v[40:41], v[34:37], off offset:576 sc1
	v_lshl_add_u64 v[38:39], v[32:33], 0, s[0:1]
	v_pk_fma_f32 v[40:41], s[2:3], v[116:117], v[16:17] op_sel_hi:[0,1,1]
	v_pk_fma_f32 v[34:35], s[2:3], v[118:119], v[18:19] op_sel_hi:[0,1,1]
	s_mov_b32 s0, 0x120000
	s_waitcnt lgkmcnt(2)
	v_pk_fma_f32 v[36:37], v[22:23], v[44:45], v[34:35] op_sel_hi:[1,0,1]
	v_pk_fma_f32 v[34:35], v[20:21], v[44:45], v[40:41] op_sel_hi:[1,0,1]
	v_add_co_u32_e32 v40, vcc, s0, v32
	s_mov_b64 s[0:1], 0x140000
	s_nop 0
	v_addc_co_u32_e32 v41, vcc, 0, v33, vcc
	global_store_dwordx4 v[40:41], v[34:37], off sc1
	v_pk_fma_f32 v[40:41], s[2:3], v[112:113], v[8:9] op_sel_hi:[0,1,1]
	s_nop 0
	v_pk_fma_f32 v[34:35], s[2:3], v[114:115], v[10:11] op_sel_hi:[0,1,1]
	v_pk_fma_f32 v[36:37], v[14:15], v[44:45], v[34:35] op_sel_hi:[1,0,1]
	v_pk_fma_f32 v[34:35], v[12:13], v[44:45], v[40:41] op_sel_hi:[1,0,1]
	global_store_dwordx4 v[38:39], v[34:37], off offset:64 sc1
	v_pk_fma_f32 v[40:41], s[2:3], v[92:93], v[4:5] op_sel_hi:[0,1,1]
	s_nop 0
	v_pk_fma_f32 v[34:35], s[2:3], v[94:95], v[6:7] op_sel_hi:[0,1,1]
	v_pk_fma_f32 v[36:37], v[2:3], v[44:45], v[34:35] op_sel_hi:[1,0,1]
	v_pk_fma_f32 v[34:35], v[0:1], v[44:45], v[40:41] op_sel_hi:[1,0,1]
	global_store_dwordx4 v[38:39], v[34:37], off offset:512 sc1
	v_pk_fma_f32 v[40:41], s[2:3], v[88:89], v[24:25] op_sel_hi:[0,1,1]
	s_nop 0
	v_pk_fma_f32 v[34:35], s[2:3], v[90:91], v[26:27] op_sel_hi:[0,1,1]
	v_pk_fma_f32 v[36:37], v[30:31], v[44:45], v[34:35] op_sel_hi:[1,0,1]
	v_pk_fma_f32 v[34:35], v[28:29], v[44:45], v[40:41] op_sel_hi:[1,0,1]
	global_store_dwordx4 v[38:39], v[34:37], off offset:576 sc1
	v_lshl_add_u64 v[38:39], v[32:33], 0, s[0:1]
	v_pk_fma_f32 v[40:41], s[2:3], v[100:101], v[16:17] op_sel_hi:[0,1,1]
	v_pk_fma_f32 v[34:35], s[2:3], v[102:103], v[18:19] op_sel_hi:[0,1,1]
	s_mov_b32 s0, 0x140000
	s_waitcnt lgkmcnt(1)
	v_pk_fma_f32 v[36:37], v[22:23], v[46:47], v[34:35] op_sel_hi:[1,0,1]
	v_pk_fma_f32 v[34:35], v[20:21], v[46:47], v[40:41] op_sel_hi:[1,0,1]
	v_add_co_u32_e32 v40, vcc, s0, v32
	s_mov_b64 s[0:1], 0x160000
	s_nop 0
	v_addc_co_u32_e32 v41, vcc, 0, v33, vcc
	global_store_dwordx4 v[40:41], v[34:37], off sc1
	v_pk_fma_f32 v[40:41], s[2:3], v[96:97], v[8:9] op_sel_hi:[0,1,1]
	v_pk_fma_f32 v[16:17], s[2:3], v[84:85], v[16:17] op_sel_hi:[0,1,1]
	v_pk_fma_f32 v[34:35], s[2:3], v[98:99], v[10:11] op_sel_hi:[0,1,1]
	v_pk_fma_f32 v[36:37], v[14:15], v[46:47], v[34:35] op_sel_hi:[1,0,1]
	v_pk_fma_f32 v[34:35], v[12:13], v[46:47], v[40:41] op_sel_hi:[1,0,1]
	global_store_dwordx4 v[38:39], v[34:37], off offset:64 sc1
	v_pk_fma_f32 v[40:41], s[2:3], v[80:81], v[4:5] op_sel_hi:[0,1,1]
	v_pk_fma_f32 v[4:5], s[2:3], v[68:69], v[4:5] op_sel_hi:[0,1,1]
	v_pk_fma_f32 v[34:35], s[2:3], v[82:83], v[6:7] op_sel_hi:[0,1,1]
	v_pk_fma_f32 v[36:37], v[2:3], v[46:47], v[34:35] op_sel_hi:[1,0,1]
	v_pk_fma_f32 v[34:35], v[0:1], v[46:47], v[40:41] op_sel_hi:[1,0,1]
	global_store_dwordx4 v[38:39], v[34:37], off offset:512 sc1
	v_pk_fma_f32 v[40:41], s[2:3], v[76:77], v[24:25] op_sel_hi:[0,1,1]
	v_pk_fma_f32 v[6:7], s[2:3], v[70:71], v[6:7] op_sel_hi:[0,1,1]
	v_pk_fma_f32 v[34:35], s[2:3], v[78:79], v[26:27] op_sel_hi:[0,1,1]
	v_pk_fma_f32 v[36:37], v[30:31], v[46:47], v[34:35] op_sel_hi:[1,0,1]
	v_pk_fma_f32 v[34:35], v[28:29], v[46:47], v[40:41] op_sel_hi:[1,0,1]
	global_store_dwordx4 v[38:39], v[34:37], off offset:576 sc1
	s_waitcnt lgkmcnt(0)
	v_pk_fma_f32 v[2:3], v[2:3], v[48:49], v[6:7] op_sel_hi:[1,0,1]
	v_pk_fma_f32 v[0:1], v[0:1], v[48:49], v[4:5] op_sel_hi:[1,0,1]
	v_lshl_add_u64 v[34:35], v[32:33], 0, s[0:1]
	s_mov_b32 s0, 0x160000
	v_pk_fma_f32 v[18:19], s[2:3], v[86:87], v[18:19] op_sel_hi:[0,1,1]
	v_pk_fma_f32 v[16:17], v[20:21], v[48:49], v[16:17] op_sel_hi:[1,0,1]
	v_add_co_u32_e32 v20, vcc, s0, v32
	v_pk_fma_f32 v[10:11], s[2:3], v[74:75], v[10:11] op_sel_hi:[0,1,1]
	v_pk_fma_f32 v[8:9], s[2:3], v[72:73], v[8:9] op_sel_hi:[0,1,1]
	global_store_dwordx4 v[34:35], v[0:3], off offset:512 sc1
	v_pk_fma_f32 v[4:5], s[2:3], v[64:65], v[24:25] op_sel_hi:[0,1,1]
	v_pk_fma_f32 v[18:19], v[22:23], v[48:49], v[18:19] op_sel_hi:[1,0,1]
	v_pk_fma_f32 v[0:1], s[2:3], v[66:67], v[26:27] op_sel_hi:[0,1,1]
	v_addc_co_u32_e32 v21, vcc, 0, v33, vcc
	v_pk_fma_f32 v[10:11], v[14:15], v[48:49], v[10:11] op_sel_hi:[1,0,1]
	v_pk_fma_f32 v[8:9], v[12:13], v[48:49], v[8:9] op_sel_hi:[1,0,1]
	v_pk_fma_f32 v[2:3], v[30:31], v[48:49], v[0:1] op_sel_hi:[1,0,1]
	v_pk_fma_f32 v[0:1], v[28:29], v[48:49], v[4:5] op_sel_hi:[1,0,1]
	global_store_dwordx4 v[20:21], v[16:19], off sc1
	global_store_dwordx4 v[34:35], v[8:11], off offset:64 sc1
	global_store_dwordx4 v[34:35], v[0:3], off offset:576 sc1
	s_waitcnt vmcnt(0)
	s_cbranch_scc0 .LBB5_36
	s_barrier

amdhsa.kernels:
  - .agpr_count:     0
    .args:
      - .actual_access:  read_only
        .address_space:  global
        .offset:         0
        .size:           8
        .value_kind:     global_buffer
      - .actual_access:  read_only
        .address_space:  global
        .offset:         8
        .size:           8
        .value_kind:     global_buffer
      - .actual_access:  read_only
        .address_space:  global
        .offset:         16
        .size:           8
        .value_kind:     global_buffer
      - .actual_access:  read_only
        .address_space:  global
        .offset:         24
        .size:           8
        .value_kind:     global_buffer
      - .actual_access:  read_only
        .address_space:  global
        .offset:         32
        .size:           8
        .value_kind:     global_buffer
      - .actual_access:  read_only
        .address_space:  global
        .offset:         40
        .size:           8
        .value_kind:     global_buffer
      - .actual_access:  read_only
        .address_space:  global
        .offset:         48
        .size:           8
        .value_kind:     global_buffer
      - .actual_access:  read_only
        .address_space:  global
        .offset:         56
        .size:           8
        .value_kind:     global_buffer
      - .actual_access:  write_only
        .address_space:  global
        .offset:         64
        .size:           8
        .value_kind:     global_buffer
      - .offset:         72
        .size:           4
        .value_kind:     by_value
    .group_segment_fixed_size: 32768
    .kernarg_segment_align: 8
    .kernarg_segment_size: 76
    .language:       OpenCL C
    .language_version:
      - 2
      - 0
    .max_flat_workgroup_size: 256
    .name:           _ZN2rb6k_prepEPKfS1_S1_S1_S1_S1_S1_S1_Phi
    .private_segment_fixed_size: 0
    .sgpr_count:     22
    .sgpr_spill_count: 0
    .symbol:         _ZN2rb6k_prepEPKfS1_S1_S1_S1_S1_S1_S1_Phi.kd
    .uniform_work_group_size: 1
    .uses_dynamic_stack: false
    .vgpr_count:     100
    .vgpr_spill_count: 0
    .wavefront_size: 64
  - .agpr_count:     0
    .args:
      - .address_space:  global
        .offset:         0
        .size:           8
        .value_kind:     global_buffer
      - .actual_access:  read_only
        .address_space:  global
        .offset:         8
        .size:           8
        .value_kind:     global_buffer
    .group_segment_fixed_size: 0
    .kernarg_segment_align: 8
    .kernarg_segment_size: 16
    .language:       OpenCL C
    .language_version:
      - 2
      - 0
    .max_flat_workgroup_size: 256
    .name:           _ZN2rb5k_midEPhPKf
    .private_segment_fixed_size: 0
    .sgpr_count:     20
    .sgpr_spill_count: 0
    .symbol:         _ZN2rb5k_midEPhPKf.kd
    .uniform_work_group_size: 1
    .uses_dynamic_stack: false
    .vgpr_count:     86
    .vgpr_spill_count: 0
    .wavefront_size: 64
  - .agpr_count:     0
    .args:
      - .offset:         0
        .size:           24
        .value_kind:     by_value
      - .offset:         24
        .size:           64
        .value_kind:     by_value
    .group_segment_fixed_size: 0
    .kernarg_segment_align: 8
    .kernarg_segment_size: 88
    .language:       OpenCL C
    .language_version:
      - 2
      - 0
    .max_flat_workgroup_size: 512
    .name:           _ZN2rb6k_gemmILi2ENS_7SchedP1ENS_5EpiP1EEEvT0_T1_
    .private_segment_fixed_size: 0
    .sgpr_count:     86
    .sgpr_spill_count: 0
    .symbol:         _ZN2rb6k_gemmILi2ENS_7SchedP1ENS_5EpiP1EEEvT0_T1_.kd
    .uniform_work_group_size: 1
    .uses_dynamic_stack: false
    .vgpr_count:     212
    .vgpr_spill_count: 0
    .wavefront_size: 64
  - .agpr_count:     0
    .args:
      - .offset:         0
        .size:           24
        .value_kind:     by_value
      - .offset:         24
        .size:           16
        .value_kind:     by_value
    .group_segment_fixed_size: 0
    .kernarg_segment_align: 8
    .kernarg_segment_size: 40
    .language:       OpenCL C
    .language_version:
      - 2
      - 0
    .max_flat_workgroup_size: 512
    .name:           _ZN2rb6k_gemmILi1ENS_7SchedP2ENS_7EpiSlabEEEvT0_T1_
    .private_segment_fixed_size: 0
    .sgpr_count:     73
    .sgpr_spill_count: 0
    .symbol:         _ZN2rb6k_gemmILi1ENS_7SchedP2ENS_7EpiSlabEEEvT0_T1_.kd
    .uniform_work_group_size: 1
    .uses_dynamic_stack: false
    .vgpr_count:     210
    .vgpr_spill_count: 0
    .wavefront_size: 64
  - .agpr_count:     0
    .args:
      - .offset:         0
        .size:           32
        .value_kind:     by_value
      - .offset:         32
        .size:           16
        .value_kind:     by_value
    .group_segment_fixed_size: 0
    .kernarg_segment_align: 8
    .kernarg_segment_size: 48
    .language:       OpenCL C
    .language_version:
      - 2
      - 0
    .max_flat_workgroup_size: 512
    .name:           _ZN2rb6k_gemmILi1ENS_6SchedGILb1EEENS_5EpiP3EEEvT0_T1_
    .private_segment_fixed_size: 0
    .sgpr_count:     62
    .sgpr_spill_count: 0
    .symbol:         _ZN2rb6k_gemmILi1ENS_6SchedGILb1EEENS_5EpiP3EEEvT0_T1_.kd
    .uniform_work_group_size: 1
    .uses_dynamic_stack: false
    .vgpr_count:     207
    .vgpr_spill_count: 0
    .wavefront_size: 64
  - .agpr_count:     0
    .args:
      - .offset:         0
        .size:           32
        .value_kind:     by_value
      - .offset:         32
        .size:           48
        .value_kind:     by_value
    .group_segment_fixed_size: 0
    .kernarg_segment_align: 8
    .kernarg_segment_size: 80
    .language:       OpenCL C
    .language_version:
      - 2
      - 0
    .max_flat_workgroup_size: 512
    .name:           _ZN2rb6k_gemmILi1ENS_6SchedGILb1EEENS_6EpiOutEEEvT0_T1_
    .private_segment_fixed_size: 0
    .sgpr_count:     62
    .sgpr_spill_count: 0
    .symbol:         _ZN2rb6k_gemmILi1ENS_6SchedGILb1EEENS_6EpiOutEEEvT0_T1_.kd
    .uniform_work_group_size: 1
    .uses_dynamic_stack: false
    .vgpr_count:     205
    .vgpr_spill_count: 0
    .wavefront_size: 64
  - .agpr_count:     0
    .args:
      - .offset:         0
        .size:           24
        .value_kind:     by_value
      - .offset:         24
        .size:           1
        .value_kind:     by_value
    .group_segment_fixed_size: 0
    .kernarg_segment_align: 8
    .kernarg_segment_size: 28
    .language:       OpenCL C
    .language_version:
      - 2
      - 0
    .max_flat_workgroup_size: 512
    .name:           _ZN2rb6k_gemmILi2ENS_7SchedP1ENS_7EpiNullEEEvT0_T1_
    .private_segment_fixed_size: 0
    .sgpr_count:     66
    .sgpr_spill_count: 0
    .symbol:         _ZN2rb6k_gemmILi2ENS_7SchedP1ENS_7EpiNullEEEvT0_T1_.kd
    .uniform_work_group_size: 1
    .uses_dynamic_stack: false
    .vgpr_count:     205
    .vgpr_spill_count: 0
    .wavefront_size: 64
